# v67 + 135 lane^1/2/4/8 exchanges (ds_bpermute + lgkmcnt waits) replaced by v_mov_b32_dpp (router top-4/reduce8, thin-pass reductions, unit prologues); waits recomputed
# baseline (speedup 1.0000x reference)
.LBB0_103:
	s_add_i32 s16, s25, s40
	s_ashr_i32 s17, s16, 31
	s_lshl_b64 s[10:11], s[16:17], 12
	s_waitcnt lgkmcnt(0)
	v_lshl_add_u64 v[16:17], v[38:39], 0, s[10:11]
	global_load_dwordx4 v[78:81], v[16:17], off nt
	global_load_dwordx4 v[82:85], v[16:17], off offset:1024 nt
	global_load_dwordx4 v[86:89], v[16:17], off offset:2048 nt
	global_load_dwordx4 v[90:93], v[16:17], off offset:3072 nt
	s_lshl_b64 s[10:11], s[16:17], 10
	v_lshl_add_u64 v[126:127], v[40:41], 0, s[10:11]
	s_add_i32 s18, s16, 1
	s_ashr_i32 s19, s18, 31
	s_lshl_b64 s[20:21], s[18:19], 12
	v_lshl_add_u64 v[24:25], v[38:39], 0, s[20:21]
	ds_read_b128 v[94:97], v70
	ds_read_b128 v[98:101], v70 offset:1024
	ds_read_b128 v[102:105], v70 offset:2048
	ds_read_b128 v[106:109], v70 offset:3072
	ds_read_b128 v[110:113], v70 offset:7168
	ds_read_b128 v[114:117], v70 offset:6144
	ds_read_b128 v[118:121], v70 offset:5120
	ds_read_b128 v[122:125], v70 offset:4096
	v_mov_b32_e32 v45, 0
	v_mov_b32_e32 v77, 0
	v_mov_b32_e32 v144, 0
	v_mov_b32_e32 v145, 0
	s_waitcnt vmcnt(3)
	v_pk_fma_f32 v[16:17], v[78:79], v[78:79], 0 op_sel_hi:[1,1,0]
	s_nop 0
	v_pk_fma_f32 v[16:17], v[80:81], v[80:81], v[16:17]
	s_waitcnt vmcnt(2)
	v_pk_fma_f32 v[16:17], v[82:83], v[82:83], v[16:17]
	s_nop 0
	v_pk_fma_f32 v[16:17], v[84:85], v[84:85], v[16:17]
	s_waitcnt vmcnt(1)
	v_pk_fma_f32 v[16:17], v[86:87], v[86:87], v[16:17]
	s_nop 0
	v_pk_fma_f32 v[16:17], v[88:89], v[88:89], v[16:17]
	s_waitcnt vmcnt(0)
	v_pk_fma_f32 v[16:17], v[90:91], v[90:91], v[16:17]
	s_nop 0
	v_pk_fma_f32 v[16:17], v[92:93], v[92:93], v[16:17]
	s_nop 0
	v_add_f32_e32 v16, v16, v17
	s_waitcnt lgkmcnt(0)
	s_nop 1
	v_add_f32_dpp v16, v16, v16 quad_perm:[1,0,3,2] row_mask:0xf bank_mask:0xf
	s_waitcnt lgkmcnt(0)
	s_nop 1
	v_add_f32_dpp v16, v16, v16 quad_perm:[2,3,0,1] row_mask:0xf bank_mask:0xf
	s_waitcnt lgkmcnt(0)
	s_nop 1
	v_add_f32_dpp v16, v16, v16 row_half_mirror row_mask:0xf bank_mask:0xf
	s_waitcnt lgkmcnt(0)
	s_nop 1
	v_add_f32_dpp v16, v16, v16 row_mirror row_mask:0xf bank_mask:0xf
	s_waitcnt lgkmcnt(0)
	v_mov_b32_e32 v17, v16
	s_nop 1
	v_permlane16_swap_b32_e32 v16, v17
	v_add_f32_e32 v16, v16, v17
	s_waitcnt lgkmcnt(0)
	v_mov_b32_e32 v17, v16
	s_nop 1
	v_permlane32_swap_b32_e32 v16, v17
	v_add_f32_e32 v16, v16, v17
	v_fmamk_f32 v16, v16, 0x3a800000, v35
	v_mul_f32_e32 v17, 0x4f800000, v16
	v_cmp_gt_f32_e32 vcc, s28, v16
	s_nop 1
	v_cndmask_b32_e32 v26, v16, v17, vcc
	v_sqrt_f32_e32 v27, v26
	global_load_dwordx4 v[20:23], v[24:25], off nt
	global_load_dwordx4 v[16:19], v[24:25], off offset:1024 nt
	v_add_u32_e32 v28, -1, v27
	v_add_u32_e32 v29, 1, v27
	v_fma_f32 v30, -v28, v27, v26
	v_fma_f32 v31, -v29, v27, v26
	v_cmp_ge_f32_e64 s[10:11], 0, v30
	s_nop 1
	v_cndmask_b32_e64 v27, v27, v28, s[10:11]
	v_cmp_lt_f32_e64 s[10:11], 0, v31
	s_nop 1
	v_cndmask_b32_e64 v27, v27, v29, s[10:11]
	v_mul_f32_e32 v28, 0x37800000, v27
	v_cndmask_b32_e32 v27, v27, v28, vcc
	v_cmp_class_f32_e32 vcc, v26, v71
	s_nop 1
	v_cndmask_b32_e32 v128, v27, v26, vcc
	global_load_dwordx4 v[28:31], v[24:25], off offset:2048 nt
	s_nop 0
	global_load_dwordx4 v[24:27], v[24:25], off offset:3072 nt
	v_div_scale_f32 v129, s[10:11], v128, v128, 1.0
	v_rcp_f32_e32 v130, v129
	v_div_scale_f32 v131, vcc, 1.0, v128, 1.0
	v_fma_f32 v132, -v129, v130, 1.0
	v_fmac_f32_e32 v130, v132, v130
	v_mul_f32_e32 v132, v131, v130
	v_fma_f32 v133, -v129, v132, v131
	v_fmac_f32_e32 v132, v133, v130
	v_fma_f32 v129, -v129, v132, v131
	v_div_fmas_f32 v129, v129, v130, v132
	v_div_fixup_f32 v128, v129, v128, 1.0
	v_pk_mul_f32 v[78:79], v[78:79], v[128:129] op_sel_hi:[1,0]
	v_pk_mul_f32 v[82:83], v[82:83], v[128:129] op_sel_hi:[1,0]
	v_pk_fma_f32 v[130:131], v[50:51], v[78:79], v[0:1]
	v_pk_mul_f32 v[86:87], v[86:87], v[128:129] op_sel_hi:[1,0]
	v_pk_fma_f32 v[134:135], v[54:55], v[82:83], v[4:5]
	v_mul_f32_e32 v82, 0x41000000, v130
	v_mul_f32_e32 v83, 0x41000000, v131
	v_pk_mul_f32 v[80:81], v[80:81], v[128:129] op_sel_hi:[1,0]
	v_pk_mul_f32 v[90:91], v[90:91], v[128:129] op_sel_hi:[1,0]
	v_pk_fma_f32 v[138:139], v[58:59], v[86:87], v[8:9]
	v_mul_f32_e32 v86, 0x41000000, v134
	v_mul_f32_e32 v87, 0x41000000, v135
	v_med3_f32 v82, v82, s29, v73
	v_med3_f32 v83, v83, s29, v73
	v_pk_mul_f32 v[84:85], v[84:85], v[128:129] op_sel_hi:[1,0]
	v_pk_mul_f32 v[88:89], v[88:89], v[128:129] op_sel_hi:[1,0]
	v_pk_mul_f32 v[92:93], v[92:93], v[128:129] op_sel_hi:[1,0]
	v_pk_fma_f32 v[128:129], v[48:49], v[80:81], v[2:3]
	v_pk_fma_f32 v[142:143], v[62:63], v[90:91], v[12:13]
	v_mul_f32_e32 v90, 0x41000000, v138
	v_mul_f32_e32 v91, 0x41000000, v139
	v_pk_fma_f32 v[80:81], v[130:131], v[122:123], 0 op_sel_hi:[1,1,0]
	v_med3_f32 v86, v86, s29, v73
	v_med3_f32 v87, v87, s29, v73
	v_cvt_pk_fp8_f32 v45, v82, v83
	v_mul_f32_e32 v146, 0x41000000, v142
	v_mul_f32_e32 v147, 0x41000000, v143
	v_pk_fma_f32 v[78:79], v[130:131], v[94:95], 0 op_sel_hi:[1,1,0]
	v_med3_f32 v90, v90, s29, v73
	v_med3_f32 v91, v91, s29, v73
	v_pk_fma_f32 v[80:81], v[128:129], v[124:125], v[80:81]
	v_cvt_pk_fp8_f32 v77, v86, v87
	v_pk_fma_f32 v[132:133], v[52:53], v[84:85], v[6:7]
	v_mul_f32_e32 v84, 0x41000000, v128
	v_mul_f32_e32 v85, 0x41000000, v129
	v_med3_f32 v94, v146, s29, v73
	v_med3_f32 v95, v147, s29, v73
	v_pk_fma_f32 v[78:79], v[128:129], v[96:97], v[78:79]
	v_cvt_pk_fp8_f32 v144, v90, v91
	v_pk_fma_f32 v[80:81], v[134:135], v[118:119], v[80:81]
	v_pk_fma_f32 v[136:137], v[56:57], v[88:89], v[10:11]
	v_mul_f32_e32 v88, 0x41000000, v132
	v_mul_f32_e32 v89, 0x41000000, v133
	v_med3_f32 v84, v84, s29, v73
	v_med3_f32 v85, v85, s29, v73
	v_cvt_pk_fp8_f32 v145, v94, v95
	v_pk_fma_f32 v[78:79], v[134:135], v[98:99], v[78:79]
	v_pk_fma_f32 v[80:81], v[132:133], v[120:121], v[80:81]
	v_pk_fma_f32 v[140:141], v[60:61], v[92:93], v[14:15]
	v_mul_f32_e32 v92, 0x41000000, v136
	v_mul_f32_e32 v93, 0x41000000, v137
	v_med3_f32 v88, v88, s29, v73
	v_med3_f32 v89, v89, s29, v73
	v_pk_fma_f32 v[78:79], v[132:133], v[100:101], v[78:79]
	v_pk_fma_f32 v[80:81], v[138:139], v[114:115], v[80:81]
	v_cvt_pk_fp8_f32 v45, v84, v85 op_sel:[0,0,1]
	v_mul_f32_e32 v148, 0x41000000, v140
	v_mul_f32_e32 v149, 0x41000000, v141
	v_med3_f32 v92, v92, s29, v73
	v_med3_f32 v93, v93, s29, v73
	v_pk_fma_f32 v[78:79], v[138:139], v[102:103], v[78:79]
	v_pk_fma_f32 v[80:81], v[136:137], v[116:117], v[80:81]
	v_cvt_pk_fp8_f32 v77, v88, v89 op_sel:[0,0,1]
	v_med3_f32 v122, v148, s29, v73
	v_med3_f32 v123, v149, s29, v73
	v_pk_fma_f32 v[78:79], v[136:137], v[104:105], v[78:79]
	v_cvt_pk_fp8_f32 v144, v92, v93 op_sel:[0,0,1]
	v_pk_fma_f32 v[80:81], v[142:143], v[110:111], v[80:81]
	v_cvt_pk_fp8_f32 v145, v122, v123 op_sel:[0,0,1]
	v_pk_fma_f32 v[78:79], v[142:143], v[106:107], v[78:79]
	v_pk_fma_f32 v[80:81], v[140:141], v[112:113], v[80:81]
	v_pk_fma_f32 v[78:79], v[140:141], v[108:109], v[78:79]
	global_store_dword v[126:127], v45, off
	global_store_dword v[126:127], v77, off offset:256
	global_store_dword v[126:127], v144, off offset:512
	global_store_dword v[126:127], v145, off offset:768
	v_add_f32_e32 v45, v80, v81
	v_add_f32_e32 v94, v78, v79
	ds_read_b128 v[78:81], v70 offset:8192
	ds_read_b128 v[82:85], v70 offset:9216
	ds_read_b128 v[86:89], v70 offset:10240
	ds_read_b128 v[90:93], v70 offset:11264
	s_waitcnt lgkmcnt(3)
	v_pk_fma_f32 v[78:79], v[130:131], v[78:79], 0 op_sel_hi:[1,1,0]
	s_nop 0
	v_pk_fma_f32 v[78:79], v[128:129], v[80:81], v[78:79]
	s_waitcnt lgkmcnt(2)
	v_pk_fma_f32 v[78:79], v[134:135], v[82:83], v[78:79]
	s_nop 0
	v_pk_fma_f32 v[78:79], v[132:133], v[84:85], v[78:79]
	s_waitcnt lgkmcnt(1)
	v_pk_fma_f32 v[78:79], v[138:139], v[86:87], v[78:79]
	s_nop 0
	v_pk_fma_f32 v[78:79], v[136:137], v[88:89], v[78:79]
	s_waitcnt lgkmcnt(0)
	v_pk_fma_f32 v[86:87], v[142:143], v[90:91], v[78:79]
	ds_read_b128 v[78:81], v70 offset:13312
	ds_read_b128 v[82:85], v70 offset:12288
	v_pk_fma_f32 v[86:87], v[140:141], v[92:93], v[86:87]
	s_waitcnt lgkmcnt(0)
	v_pk_fma_f32 v[82:83], v[130:131], v[82:83], 0 op_sel_hi:[1,1,0]
	v_add_f32_e32 v77, v86, v87
	ds_read_b128 v[86:89], v70 offset:15360
	ds_read_b128 v[90:93], v70 offset:14336
	v_pk_fma_f32 v[82:83], v[128:129], v[84:85], v[82:83]
	s_nop 0
	v_pk_fma_f32 v[78:79], v[134:135], v[78:79], v[82:83]
	s_nop 0
	v_pk_fma_f32 v[78:79], v[132:133], v[80:81], v[78:79]
	s_waitcnt lgkmcnt(0)
	v_pk_fma_f32 v[78:79], v[138:139], v[90:91], v[78:79]
	s_nop 0
	v_pk_fma_f32 v[78:79], v[136:137], v[92:93], v[78:79]
	s_nop 0
	v_pk_fma_f32 v[78:79], v[142:143], v[86:87], v[78:79]
	s_nop 0
	v_pk_fma_f32 v[78:79], v[140:141], v[88:89], v[78:79]
	s_nop 0
	v_add_f32_e32 v95, v78, v79
	ds_read_b128 v[78:81], v70 offset:16384
	ds_read_b128 v[82:85], v70 offset:17408
	ds_read_b128 v[86:89], v70 offset:18432
	ds_read_b128 v[90:93], v70 offset:19456
	s_waitcnt lgkmcnt(3)
	v_pk_fma_f32 v[78:79], v[130:131], v[78:79], 0 op_sel_hi:[1,1,0]
	s_nop 0
	v_pk_fma_f32 v[78:79], v[128:129], v[80:81], v[78:79]
	s_waitcnt lgkmcnt(2)
	v_pk_fma_f32 v[78:79], v[134:135], v[82:83], v[78:79]
	s_nop 0
	v_pk_fma_f32 v[78:79], v[132:133], v[84:85], v[78:79]
	s_waitcnt lgkmcnt(1)
	v_pk_fma_f32 v[78:79], v[138:139], v[86:87], v[78:79]
	s_nop 0
	v_pk_fma_f32 v[78:79], v[136:137], v[88:89], v[78:79]
	s_waitcnt lgkmcnt(0)
	v_pk_fma_f32 v[86:87], v[142:143], v[90:91], v[78:79]
	ds_read_b128 v[78:81], v70 offset:21504
	ds_read_b128 v[82:85], v70 offset:20480
	v_pk_fma_f32 v[86:87], v[140:141], v[92:93], v[86:87]
	s_waitcnt lgkmcnt(0)
	v_pk_fma_f32 v[82:83], v[130:131], v[82:83], 0 op_sel_hi:[1,1,0]
	v_add_f32_e32 v96, v86, v87
	ds_read_b128 v[86:89], v70 offset:23552
	ds_read_b128 v[90:93], v70 offset:22528
	v_pk_fma_f32 v[82:83], v[128:129], v[84:85], v[82:83]
	s_nop 0
	v_pk_fma_f32 v[78:79], v[134:135], v[78:79], v[82:83]
	s_nop 0
	v_pk_fma_f32 v[78:79], v[132:133], v[80:81], v[78:79]
	s_waitcnt lgkmcnt(0)
	v_pk_fma_f32 v[78:79], v[138:139], v[90:91], v[78:79]
	s_nop 0
	v_pk_fma_f32 v[78:79], v[136:137], v[92:93], v[78:79]
	s_nop 0
	v_pk_fma_f32 v[78:79], v[142:143], v[86:87], v[78:79]
	s_nop 0
	v_pk_fma_f32 v[78:79], v[140:141], v[88:89], v[78:79]
	s_nop 0
	v_add_f32_e32 v97, v78, v79
	ds_read_b128 v[78:81], v70 offset:24576
	ds_read_b128 v[82:85], v70 offset:25600
	ds_read_b128 v[86:89], v70 offset:26624
	ds_read_b128 v[90:93], v70 offset:27648
	s_waitcnt lgkmcnt(3)
	v_pk_fma_f32 v[78:79], v[130:131], v[78:79], 0 op_sel_hi:[1,1,0]
	s_nop 0
	v_pk_fma_f32 v[78:79], v[128:129], v[80:81], v[78:79]
	s_waitcnt lgkmcnt(2)
	v_pk_fma_f32 v[78:79], v[134:135], v[82:83], v[78:79]
	s_nop 0
	v_pk_fma_f32 v[78:79], v[132:133], v[84:85], v[78:79]
	s_waitcnt lgkmcnt(1)
	v_pk_fma_f32 v[78:79], v[138:139], v[86:87], v[78:79]
	s_nop 0
	v_pk_fma_f32 v[78:79], v[136:137], v[88:89], v[78:79]
	s_waitcnt lgkmcnt(0)
	v_pk_fma_f32 v[86:87], v[142:143], v[90:91], v[78:79]
	ds_read_b128 v[78:81], v70 offset:29696
	ds_read_b128 v[82:85], v70 offset:28672
	v_pk_fma_f32 v[86:87], v[140:141], v[92:93], v[86:87]
	s_waitcnt lgkmcnt(0)
	v_pk_fma_f32 v[82:83], v[130:131], v[82:83], 0 op_sel_hi:[1,1,0]
	v_add_f32_e32 v98, v86, v87
	ds_read_b128 v[86:89], v70 offset:31744
	ds_read_b128 v[90:93], v70 offset:30720
	v_pk_fma_f32 v[82:83], v[128:129], v[84:85], v[82:83]
	s_nop 0
	v_pk_fma_f32 v[78:79], v[134:135], v[78:79], v[82:83]
	s_nop 0
	v_pk_fma_f32 v[78:79], v[132:133], v[80:81], v[78:79]
	s_waitcnt lgkmcnt(0)
	v_pk_fma_f32 v[78:79], v[138:139], v[90:91], v[78:79]
	s_nop 0
	v_pk_fma_f32 v[78:79], v[136:137], v[92:93], v[78:79]
	s_nop 0
	v_pk_fma_f32 v[78:79], v[142:143], v[86:87], v[78:79]
	s_nop 0
	v_pk_fma_f32 v[78:79], v[140:141], v[88:89], v[78:79]
	s_nop 0
	v_add_f32_e32 v78, v78, v79
	v_cndmask_b32_e64 v79, v94, v96, s[2:3]
	ds_bpermute_b32 v79, v69, v79
	v_cndmask_b32_e64 v80, v96, v94, s[2:3]
	v_cndmask_b32_e64 v81, v45, v97, s[2:3]
	v_cndmask_b32_e64 v82, v95, v78, s[2:3]
	ds_bpermute_b32 v81, v69, v81
	s_waitcnt lgkmcnt(1)
	v_add_f32_e32 v79, v80, v79
	v_cndmask_b32_e64 v80, v77, v98, s[2:3]
	ds_bpermute_b32 v80, v69, v80
	ds_bpermute_b32 v82, v69, v82
	v_cndmask_b32_e64 v45, v97, v45, s[2:3]
	v_cndmask_b32_e64 v77, v98, v77, s[2:3]
	v_cndmask_b32_e64 v78, v78, v95, s[2:3]
	s_waitcnt lgkmcnt(2)
	v_add_f32_e32 v45, v45, v81
	s_waitcnt lgkmcnt(1)
	v_add_f32_e32 v77, v77, v80
	s_waitcnt lgkmcnt(0)
	v_add_f32_e32 v78, v78, v82
	v_cndmask_b32_e64 v80, v79, v77, s[4:5]
	v_cndmask_b32_e64 v81, v45, v78, s[4:5]
	ds_bpermute_b32 v80, v68, v80
	ds_bpermute_b32 v81, v68, v81
	v_cndmask_b32_e64 v77, v77, v79, s[4:5]
	v_cndmask_b32_e64 v45, v78, v45, s[4:5]
	s_waitcnt lgkmcnt(1)
	v_add_f32_e32 v77, v77, v80
	s_waitcnt lgkmcnt(0)
	v_add_f32_e32 v45, v45, v81
	v_cndmask_b32_e64 v78, v77, v45, s[6:7]
	s_nop 1
	v_mov_b32_dpp v78, v78 row_ror:8 row_mask:0xf bank_mask:0xf
	v_cndmask_b32_e64 v45, v45, v77, s[6:7]
	s_waitcnt lgkmcnt(0)
	v_add_f32_e32 v45, v45, v78
	s_nop 1
	v_mov_b32_dpp v77, v45 quad_perm:[3,2,1,0] row_mask:0xf bank_mask:0xf
	s_nop 1
	v_mov_b32_dpp v77, v77 row_half_mirror row_mask:0xf bank_mask:0xf
	s_waitcnt lgkmcnt(0)
	v_add_f32_e32 v45, v45, v77
	s_nop 1
	v_mov_b32_dpp v77, v45 quad_perm:[2,3,0,1] row_mask:0xf bank_mask:0xf
	s_waitcnt lgkmcnt(0)
	v_add_f32_e32 v45, v45, v77
	s_nop 1
	v_mov_b32_dpp v77, v45 quad_perm:[1,0,3,2] row_mask:0xf bank_mask:0xf
	s_and_saveexec_b64 s[10:11], s[8:9]
	s_cbranch_execz .LBB0_105
	global_load_dword v78, v[42:43], off
	s_waitcnt lgkmcnt(0)
	v_add_f32_e32 v45, v45, v77
	s_add_i32 s20, s39, s40
	s_ashr_i32 s21, s20, 31
	s_waitcnt vmcnt(0)
	v_add_f32_e32 v45, v45, v78
	v_mul_f32_e64 v77, |v45|, s30
	v_exp_f32_e32 v77, v77
	v_min_f32_e32 v92, 0, v45
	v_add_f32_e32 v45, 1.0, v77
	v_add_f32_e32 v80, -1.0, v45
	v_frexp_mant_f32_e32 v81, v45
	v_cvt_f64_f32_e32 v[78:79], v45
	v_sub_f32_e32 v82, v80, v45
	v_frexp_exp_i32_f64_e32 v78, v[78:79]
	v_cmp_gt_f32_e32 vcc, s31, v81
	v_sub_f32_e32 v80, v77, v80
	v_add_f32_e32 v79, 1.0, v82
	v_subbrev_co_u32_e32 v78, vcc, 0, v78, vcc
	v_add_f32_e32 v79, v80, v79
	v_sub_u32_e32 v80, 0, v78
	v_ldexp_f32 v45, v45, v80
	v_ldexp_f32 v79, v79, v80
	v_add_f32_e32 v80, -1.0, v45
	v_add_f32_e32 v82, 1.0, v45
	v_add_f32_e32 v81, 1.0, v80
	v_add_f32_e32 v83, -1.0, v82
	v_sub_f32_e32 v81, v45, v81
	v_sub_f32_e32 v45, v45, v83
	v_add_f32_e32 v45, v79, v45
	v_add_f32_e32 v83, v79, v81
	v_add_f32_e32 v79, v82, v45
	v_rcp_f32_e32 v86, v79
	v_add_f32_e32 v81, v80, v83
	v_sub_f32_e32 v82, v79, v82
	v_sub_f32_e32 v45, v45, v82
	v_mul_f32_e32 v88, v81, v86
	v_mul_f32_e32 v82, v79, v88
	v_fma_f32 v84, v88, v79, -v82
	v_sub_f32_e32 v80, v81, v80
	v_fmac_f32_e32 v84, v88, v45
	v_sub_f32_e32 v87, v83, v80
	v_add_f32_e32 v80, v82, v84
	v_sub_f32_e32 v83, v81, v80
	v_mov_b32_e32 v85, v80
	v_pk_add_f32 v[80:81], v[80:81], v[82:83] neg_lo:[0,1] neg_hi:[0,1]
	v_cvt_f32_i32_e32 v78, v78
	v_pk_add_f32 v[80:81], v[80:81], v[84:85] neg_lo:[0,1] neg_hi:[0,1]
	v_cmp_neq_f32_e32 vcc, s34, v77
	v_add_f32_e32 v81, v87, v81
	v_add_f32_e32 v80, v80, v81
	v_add_f32_e32 v81, v83, v80
	v_mul_f32_e32 v85, v86, v81
	v_mul_f32_e32 v82, v79, v85
	v_fma_f32 v84, v85, v79, -v82
	v_sub_f32_e32 v83, v83, v81
	v_fmac_f32_e32 v84, v85, v45
	v_add_f32_e32 v87, v80, v83
	v_add_f32_e32 v89, v88, v85
	v_add_f32_e32 v80, v82, v84
	v_sub_f32_e32 v79, v89, v88
	v_sub_f32_e32 v83, v81, v80
	v_sub_f32_e32 v45, v85, v79
	v_mov_b32_e32 v85, v80
	v_pk_add_f32 v[80:81], v[80:81], v[82:83] neg_lo:[0,1] neg_hi:[0,1]
	s_nop 0
	v_pk_add_f32 v[80:81], v[80:81], v[84:85] neg_lo:[0,1] neg_hi:[0,1]
	s_nop 0
	v_add_f32_e32 v79, v87, v81
	v_add_f32_e32 v79, v80, v79
	v_add_f32_e32 v79, v83, v79
	v_mul_f32_e32 v79, v86, v79
	v_add_f32_e32 v45, v45, v79
	v_add_f32_e32 v79, v89, v45
	v_mul_f32_e32 v80, v79, v79
	v_sub_f32_e32 v82, v79, v89
	v_fmamk_f32 v83, v80, 0x3e9b6dac, v72
	v_ldexp_f32 v81, v79, 1
	v_sub_f32_e32 v82, v45, v82
	v_mul_f32_e32 v79, v79, v80
	v_fmaak_f32 v45, v80, v83, 0x3f2aaada
	v_ldexp_f32 v85, v82, 1
	v_pk_mul_f32 v[82:83], v[78:79], v[44:45]
	s_nop 0
	v_fma_f32 v80, v78, s33, -v82
	v_fmac_f32_e32 v80, 0xb102e308, v78
	v_pk_add_f32 v[78:79], v[82:83], v[80:81]
	v_mov_b32_e32 v84, v82
	v_sub_f32_e32 v45, v79, v81
	v_sub_f32_e32 v45, v83, v45
	v_add_f32_e32 v85, v85, v45
	v_pk_add_f32 v[86:87], v[78:79], v[82:83] neg_lo:[0,1] neg_hi:[0,1]
	v_pk_add_f32 v[82:83], v[78:79], v[84:85]
	v_mov_b32_e32 v81, v78
	v_mov_b32_e32 v87, v83
	v_pk_add_f32 v[90:91], v[80:81], v[86:87] neg_lo:[0,1] neg_hi:[0,1]
	v_pk_add_f32 v[80:81], v[80:81], v[86:87]
	v_mov_b32_e32 v89, v78
	v_pk_add_f32 v[86:87], v[80:81], v[78:79] op_sel:[1,0] op_sel_hi:[0,1] neg_lo:[0,1] neg_hi:[0,1]
	v_mov_b32_e32 v88, v85
	v_mov_b32_e32 v84, v83
	v_mov_b32_e32 v85, v81
	v_pk_mov_b32 v[78:79], v[78:79], v[86:87] op_sel:[1,0]
	v_pk_add_f32 v[82:83], v[82:83], v[86:87] op_sel_hi:[1,0] neg_lo:[0,1] neg_hi:[0,1]
	v_pk_add_f32 v[78:79], v[84:85], v[78:79] neg_lo:[0,1] neg_hi:[0,1]
	v_mov_b32_e32 v82, v90
	v_pk_add_f32 v[78:79], v[88:89], v[78:79] neg_lo:[0,1] neg_hi:[0,1]
	v_mov_b32_e32 v91, v81
	v_pk_add_f32 v[82:83], v[82:83], v[78:79]
	s_nop 0
	v_pk_add_f32 v[84:85], v[82:83], v[82:83] op_sel:[0,1] op_sel_hi:[1,0]
	s_nop 0
	v_pk_add_f32 v[80:81], v[80:81], v[84:85] op_sel:[1,0] op_sel_hi:[0,1]
	v_mov_b32_e32 v83, v80
	v_mov_b32_e32 v79, v84
	v_pk_add_f32 v[84:85], v[82:83], v[90:91] neg_lo:[0,1] neg_hi:[0,1]
	s_nop 0
	v_sub_f32_e32 v45, v82, v84
	v_pk_add_f32 v[78:79], v[78:79], v[84:85] neg_lo:[0,1] neg_hi:[0,1]
	v_sub_f32_e32 v45, v90, v45
	v_add_f32_e32 v45, v78, v45
	v_add_f32_e32 v45, v45, v79
	v_add_f32_e32 v45, v80, v45
	v_cndmask_b32_e32 v45, v74, v45, vcc
	v_cmp_ngt_f32_e32 vcc, -1.0, v77
	v_lshl_add_u64 v[78:79], s[20:21], 2, v[46:47]
	s_nop 0
	v_cndmask_b32_e32 v45, v75, v45, vcc
	v_cmp_neq_f32_e32 vcc, -1.0, v77
	s_nop 1
	v_cndmask_b32_e32 v45, v76, v45, vcc
	v_cmp_lt_f32_e64 vcc, |v77|, s35
	s_nop 1
	v_cndmask_b32_e32 v45, v45, v77, vcc
	v_sub_f32_e32 v45, v92, v45
	global_store_dword v[78:79], v45, off
.LBB0_105:
	s_or_b64 exec, exec, s[10:11]
	s_waitcnt vmcnt(7)
	v_pk_fma_f32 v[78:79], v[20:21], v[20:21], 0 op_sel_hi:[1,1,0]
	v_mov_b32_e32 v88, 0
	v_pk_fma_f32 v[78:79], v[22:23], v[22:23], v[78:79]
	s_lshl_b64 s[18:19], s[18:19], 10
	s_waitcnt vmcnt(6)
	v_pk_fma_f32 v[78:79], v[16:17], v[16:17], v[78:79]
	v_lshl_add_u64 v[82:83], v[40:41], 0, s[18:19]
	v_pk_fma_f32 v[78:79], v[18:19], v[18:19], v[78:79]
	s_waitcnt vmcnt(5)
	v_pk_fma_f32 v[78:79], v[28:29], v[28:29], v[78:79]
	s_nop 0
	v_pk_fma_f32 v[78:79], v[30:31], v[30:31], v[78:79]
	s_waitcnt vmcnt(4)
	v_pk_fma_f32 v[78:79], v[24:25], v[24:25], v[78:79]
	s_nop 0
	v_pk_fma_f32 v[78:79], v[26:27], v[26:27], v[78:79]
	s_nop 0
	v_add_f32_e32 v45, v78, v79
	s_waitcnt lgkmcnt(0)
	s_waitcnt lgkmcnt(0)
	s_nop 1
	v_add_f32_dpp v45, v45, v45 quad_perm:[1,0,3,2] row_mask:0xf bank_mask:0xf
	s_waitcnt lgkmcnt(0)
	s_nop 1
	v_add_f32_dpp v45, v45, v45 quad_perm:[2,3,0,1] row_mask:0xf bank_mask:0xf
	s_waitcnt lgkmcnt(0)
	s_nop 1
	v_add_f32_dpp v45, v45, v45 row_half_mirror row_mask:0xf bank_mask:0xf
	s_waitcnt lgkmcnt(0)
	s_nop 1
	v_add_f32_dpp v45, v45, v45 row_mirror row_mask:0xf bank_mask:0xf
	s_waitcnt lgkmcnt(0)
	v_mov_b32_e32 v77, v45
	s_nop 1
	v_permlane16_swap_b32_e32 v45, v77
	v_add_f32_e32 v45, v45, v77
	s_waitcnt lgkmcnt(0)
	v_mov_b32_e32 v77, v45
	s_nop 1
	v_permlane32_swap_b32_e32 v45, v77
	v_add_f32_e32 v45, v45, v77
	v_fmamk_f32 v45, v45, 0x3a800000, v35
	v_mul_f32_e32 v77, 0x4f800000, v45
	v_cmp_gt_f32_e32 vcc, s28, v45
	s_nop 1
	v_cndmask_b32_e32 v45, v45, v77, vcc
	v_sqrt_f32_e32 v77, v45
	s_nop 0
	v_add_u32_e32 v78, -1, v77
	v_add_u32_e32 v79, 1, v77
	v_fma_f32 v80, -v78, v77, v45
	v_fma_f32 v81, -v79, v77, v45
	v_cmp_ge_f32_e64 s[10:11], 0, v80
	s_nop 1
	v_cndmask_b32_e64 v77, v77, v78, s[10:11]
	v_cmp_lt_f32_e64 s[10:11], 0, v81
	s_nop 1
	v_cndmask_b32_e64 v77, v77, v79, s[10:11]
	v_mul_f32_e32 v78, 0x37800000, v77
	v_cndmask_b32_e32 v77, v77, v78, vcc
	v_cmp_class_f32_e32 vcc, v45, v71
	s_nop 1
	v_cndmask_b32_e32 v45, v77, v45, vcc
	v_div_scale_f32 v77, s[10:11], v45, v45, 1.0
	v_rcp_f32_e32 v78, v77
	v_div_scale_f32 v79, vcc, 1.0, v45, 1.0
	v_fma_f32 v80, -v77, v78, 1.0
	v_fmac_f32_e32 v78, v80, v78
	v_mul_f32_e32 v80, v79, v78
	v_fma_f32 v81, -v77, v80, v79
	v_fmac_f32_e32 v80, v81, v78
	v_fma_f32 v77, -v77, v80, v79
	v_div_fmas_f32 v77, v77, v78, v80
	v_div_fixup_f32 v78, v77, v45, 1.0
	v_pk_mul_f32 v[20:21], v[20:21], v[78:79] op_sel_hi:[1,0]
	v_pk_mul_f32 v[84:85], v[30:31], v[78:79] op_sel_hi:[1,0]
	v_pk_fma_f32 v[30:31], v[50:51], v[20:21], v[0:1]
	v_pk_mul_f32 v[22:23], v[22:23], v[78:79] op_sel_hi:[1,0]
	v_mul_f32_e32 v45, 0x41000000, v30
	v_mul_f32_e32 v77, 0x41000000, v31
	v_med3_f32 v45, v45, s29, v73
	v_med3_f32 v77, v77, s29, v73
	v_cvt_pk_fp8_f32 v88, v45, v77
	v_pk_mul_f32 v[16:17], v[16:17], v[78:79] op_sel_hi:[1,0]
	v_pk_mul_f32 v[18:19], v[18:19], v[78:79] op_sel_hi:[1,0]
	v_pk_mul_f32 v[80:81], v[28:29], v[78:79] op_sel_hi:[1,0]
	v_pk_mul_f32 v[86:87], v[24:25], v[78:79] op_sel_hi:[1,0]
	v_pk_mul_f32 v[78:79], v[26:27], v[78:79] op_sel_hi:[1,0]
	v_pk_fma_f32 v[24:25], v[48:49], v[22:23], v[2:3]
	v_pk_fma_f32 v[28:29], v[54:55], v[16:17], v[4:5]
	v_pk_fma_f32 v[16:17], v[60:61], v[78:79], v[14:15]
	v_mul_f32_e32 v78, 0x41000000, v24
	v_mul_f32_e32 v45, 0x41000000, v25
	v_med3_f32 v77, v78, s29, v73
	v_med3_f32 v45, v45, s29, v73
	v_cvt_pk_fp8_f32 v88, v77, v45 op_sel:[0,0,1]
	v_mul_f32_e32 v45, 0x41000000, v28
	v_mul_f32_e32 v77, 0x41000000, v29
	v_pk_fma_f32 v[20:21], v[52:53], v[18:19], v[6:7]
	v_pk_fma_f32 v[18:19], v[56:57], v[84:85], v[10:11]
	v_med3_f32 v45, v45, s29, v73
	v_med3_f32 v77, v77, s29, v73
	v_mov_b32_e32 v84, 0
	v_cvt_pk_fp8_f32 v84, v45, v77
	v_mul_f32_e32 v78, 0x41000000, v20
	v_mul_f32_e32 v45, 0x41000000, v21
	v_pk_fma_f32 v[26:27], v[58:59], v[80:81], v[8:9]
	v_med3_f32 v77, v78, s29, v73
	v_med3_f32 v45, v45, s29, v73
	v_cvt_pk_fp8_f32 v84, v77, v45 op_sel:[0,0,1]
	v_mul_f32_e32 v45, 0x41000000, v26
	v_mul_f32_e32 v77, 0x41000000, v27
	v_med3_f32 v45, v45, s29, v73
	v_med3_f32 v77, v77, s29, v73
	v_mov_b32_e32 v85, 0
	v_cvt_pk_fp8_f32 v85, v45, v77
	v_mul_f32_e32 v78, 0x41000000, v18
	v_mul_f32_e32 v45, 0x41000000, v19
	v_pk_fma_f32 v[22:23], v[62:63], v[86:87], v[12:13]
	v_med3_f32 v77, v78, s29, v73
	v_med3_f32 v45, v45, s29, v73
	v_cvt_pk_fp8_f32 v85, v77, v45 op_sel:[0,0,1]
	v_mul_f32_e32 v45, 0x41000000, v22
	v_mul_f32_e32 v77, 0x41000000, v23
	v_med3_f32 v45, v45, s29, v73
	v_med3_f32 v77, v77, s29, v73
	v_mov_b32_e32 v86, 0
	v_cvt_pk_fp8_f32 v86, v45, v77
	v_mul_f32_e32 v78, 0x41000000, v16
	v_mul_f32_e32 v45, 0x41000000, v17
	v_med3_f32 v77, v78, s29, v73
	v_med3_f32 v45, v45, s29, v73
	v_cvt_pk_fp8_f32 v86, v77, v45 op_sel:[0,0,1]
	ds_read_b128 v[78:81], v70
	global_store_dword v[82:83], v88, off
	global_store_dword v[82:83], v84, off offset:256
	global_store_dword v[82:83], v85, off offset:512
	global_store_dword v[82:83], v86, off offset:768
	ds_read_b128 v[82:85], v70 offset:1024
	ds_read_b128 v[86:89], v70 offset:2048
	s_waitcnt lgkmcnt(2)
	v_pk_fma_f32 v[78:79], v[30:31], v[78:79], 0 op_sel_hi:[1,1,0]
	s_nop 0
	v_pk_fma_f32 v[90:91], v[24:25], v[80:81], v[78:79]
	ds_read_b128 v[78:81], v70 offset:3072
	s_waitcnt lgkmcnt(2)
	v_pk_fma_f32 v[82:83], v[28:29], v[82:83], v[90:91]
	s_nop 0
	v_pk_fma_f32 v[82:83], v[20:21], v[84:85], v[82:83]
	s_waitcnt lgkmcnt(1)
	v_pk_fma_f32 v[82:83], v[26:27], v[86:87], v[82:83]
	s_nop 0
	v_pk_fma_f32 v[82:83], v[18:19], v[88:89], v[82:83]
	s_waitcnt lgkmcnt(0)
	v_pk_fma_f32 v[78:79], v[22:23], v[78:79], v[82:83]
	ds_read_b128 v[82:85], v70 offset:5120
	ds_read_b128 v[86:89], v70 offset:4096
	v_pk_fma_f32 v[78:79], v[16:17], v[80:81], v[78:79]
	s_waitcnt lgkmcnt(0)
	v_pk_fma_f32 v[86:87], v[30:31], v[86:87], 0 op_sel_hi:[1,1,0]
	v_add_f32_e32 v45, v78, v79
	ds_read_b128 v[78:81], v70 offset:7168
	ds_read_b128 v[90:93], v70 offset:6144
	v_pk_fma_f32 v[86:87], v[24:25], v[88:89], v[86:87]
	s_nop 0
	v_pk_fma_f32 v[82:83], v[28:29], v[82:83], v[86:87]
	s_nop 0
	v_pk_fma_f32 v[82:83], v[20:21], v[84:85], v[82:83]
	s_waitcnt lgkmcnt(0)
	v_pk_fma_f32 v[82:83], v[26:27], v[90:91], v[82:83]
	s_nop 0
	v_pk_fma_f32 v[82:83], v[18:19], v[92:93], v[82:83]
	s_nop 0
	v_pk_fma_f32 v[78:79], v[22:23], v[78:79], v[82:83]
	s_nop 0
	v_pk_fma_f32 v[78:79], v[16:17], v[80:81], v[78:79]
	s_nop 0
	v_add_f32_e32 v77, v78, v79
	ds_read_b128 v[78:81], v70 offset:8192
	ds_read_b128 v[82:85], v70 offset:9216
	ds_read_b128 v[86:89], v70 offset:10240
	ds_read_b128 v[90:93], v70 offset:11264
	s_waitcnt lgkmcnt(3)
	v_pk_fma_f32 v[78:79], v[30:31], v[78:79], 0 op_sel_hi:[1,1,0]
	s_nop 0
	v_pk_fma_f32 v[78:79], v[24:25], v[80:81], v[78:79]
	s_waitcnt lgkmcnt(2)
	v_pk_fma_f32 v[78:79], v[28:29], v[82:83], v[78:79]
	s_nop 0
	v_pk_fma_f32 v[78:79], v[20:21], v[84:85], v[78:79]
	s_waitcnt lgkmcnt(1)
	v_pk_fma_f32 v[78:79], v[26:27], v[86:87], v[78:79]
	s_nop 0
	v_pk_fma_f32 v[78:79], v[18:19], v[88:89], v[78:79]
	s_waitcnt lgkmcnt(0)
	v_pk_fma_f32 v[86:87], v[22:23], v[90:91], v[78:79]
	ds_read_b128 v[78:81], v70 offset:13312
	ds_read_b128 v[82:85], v70 offset:12288
	v_pk_fma_f32 v[86:87], v[16:17], v[92:93], v[86:87]
	s_waitcnt lgkmcnt(0)
	v_pk_fma_f32 v[82:83], v[30:31], v[82:83], 0 op_sel_hi:[1,1,0]
	v_add_f32_e32 v94, v86, v87
	ds_read_b128 v[86:89], v70 offset:15360
	ds_read_b128 v[90:93], v70 offset:14336
	v_pk_fma_f32 v[82:83], v[24:25], v[84:85], v[82:83]
	s_nop 0
	v_pk_fma_f32 v[78:79], v[28:29], v[78:79], v[82:83]
	s_nop 0
	v_pk_fma_f32 v[78:79], v[20:21], v[80:81], v[78:79]
	s_waitcnt lgkmcnt(0)
	v_pk_fma_f32 v[78:79], v[26:27], v[90:91], v[78:79]
	s_nop 0
	v_pk_fma_f32 v[78:79], v[18:19], v[92:93], v[78:79]
	s_nop 0
	v_pk_fma_f32 v[78:79], v[22:23], v[86:87], v[78:79]
	s_nop 0
	v_pk_fma_f32 v[78:79], v[16:17], v[88:89], v[78:79]
	s_nop 0
	v_add_f32_e32 v95, v78, v79
	ds_read_b128 v[78:81], v70 offset:16384
	ds_read_b128 v[82:85], v70 offset:17408
	ds_read_b128 v[86:89], v70 offset:18432
	ds_read_b128 v[90:93], v70 offset:19456
	s_waitcnt lgkmcnt(3)
	v_pk_fma_f32 v[78:79], v[30:31], v[78:79], 0 op_sel_hi:[1,1,0]
	s_nop 0
	v_pk_fma_f32 v[78:79], v[24:25], v[80:81], v[78:79]
	s_waitcnt lgkmcnt(2)
	v_pk_fma_f32 v[78:79], v[28:29], v[82:83], v[78:79]
	s_nop 0
	v_pk_fma_f32 v[78:79], v[20:21], v[84:85], v[78:79]
	s_waitcnt lgkmcnt(1)
	v_pk_fma_f32 v[78:79], v[26:27], v[86:87], v[78:79]
	s_nop 0
	v_pk_fma_f32 v[78:79], v[18:19], v[88:89], v[78:79]
	s_waitcnt lgkmcnt(0)
	v_pk_fma_f32 v[86:87], v[22:23], v[90:91], v[78:79]
	ds_read_b128 v[78:81], v70 offset:21504
	ds_read_b128 v[82:85], v70 offset:20480
	v_pk_fma_f32 v[86:87], v[16:17], v[92:93], v[86:87]
	s_waitcnt lgkmcnt(0)
	v_pk_fma_f32 v[82:83], v[30:31], v[82:83], 0 op_sel_hi:[1,1,0]
	v_add_f32_e32 v96, v86, v87
	ds_read_b128 v[86:89], v70 offset:23552
	ds_read_b128 v[90:93], v70 offset:22528
	v_pk_fma_f32 v[82:83], v[24:25], v[84:85], v[82:83]
	s_nop 0
	v_pk_fma_f32 v[78:79], v[28:29], v[78:79], v[82:83]
	s_nop 0
	v_pk_fma_f32 v[78:79], v[20:21], v[80:81], v[78:79]
	s_waitcnt lgkmcnt(0)
	v_pk_fma_f32 v[78:79], v[26:27], v[90:91], v[78:79]
	s_nop 0
	v_pk_fma_f32 v[78:79], v[18:19], v[92:93], v[78:79]
	s_nop 0
	v_pk_fma_f32 v[78:79], v[22:23], v[86:87], v[78:79]
	s_nop 0
	v_pk_fma_f32 v[78:79], v[16:17], v[88:89], v[78:79]
	s_nop 0
	v_add_f32_e32 v97, v78, v79
	ds_read_b128 v[78:81], v70 offset:24576
	ds_read_b128 v[82:85], v70 offset:25600
	ds_read_b128 v[86:89], v70 offset:26624
	ds_read_b128 v[90:93], v70 offset:27648
	s_waitcnt lgkmcnt(3)
	v_pk_fma_f32 v[78:79], v[30:31], v[78:79], 0 op_sel_hi:[1,1,0]
	s_nop 0
	v_pk_fma_f32 v[78:79], v[24:25], v[80:81], v[78:79]
	s_waitcnt lgkmcnt(2)
	v_pk_fma_f32 v[78:79], v[28:29], v[82:83], v[78:79]
	s_nop 0
	v_pk_fma_f32 v[78:79], v[20:21], v[84:85], v[78:79]
	s_waitcnt lgkmcnt(1)
	v_pk_fma_f32 v[78:79], v[26:27], v[86:87], v[78:79]
	s_nop 0
	v_pk_fma_f32 v[78:79], v[18:19], v[88:89], v[78:79]
	s_waitcnt lgkmcnt(0)
	v_pk_fma_f32 v[86:87], v[22:23], v[90:91], v[78:79]
	ds_read_b128 v[78:81], v70 offset:29696
	ds_read_b128 v[82:85], v70 offset:28672
	v_pk_fma_f32 v[86:87], v[16:17], v[92:93], v[86:87]
	s_waitcnt lgkmcnt(0)
	v_pk_fma_f32 v[30:31], v[30:31], v[82:83], 0 op_sel_hi:[1,1,0]
	v_add_f32_e32 v98, v86, v87
	ds_read_b128 v[86:89], v70 offset:31744
	ds_read_b128 v[90:93], v70 offset:30720
	v_pk_fma_f32 v[24:25], v[24:25], v[84:85], v[30:31]
	s_nop 0
	v_pk_fma_f32 v[24:25], v[28:29], v[78:79], v[24:25]
	s_nop 0
	v_pk_fma_f32 v[20:21], v[20:21], v[80:81], v[24:25]
	s_waitcnt lgkmcnt(0)
	v_pk_fma_f32 v[20:21], v[26:27], v[90:91], v[20:21]
	s_nop 0
	v_pk_fma_f32 v[18:19], v[18:19], v[92:93], v[20:21]
	s_nop 0
	v_pk_fma_f32 v[18:19], v[22:23], v[86:87], v[18:19]
	s_nop 0
	v_pk_fma_f32 v[16:17], v[16:17], v[88:89], v[18:19]
	s_nop 0
	v_add_f32_e32 v16, v16, v17
	v_cndmask_b32_e64 v17, v45, v96, s[2:3]
	ds_bpermute_b32 v17, v69, v17
	v_cndmask_b32_e64 v18, v96, v45, s[2:3]
	v_cndmask_b32_e64 v19, v77, v97, s[2:3]
	ds_bpermute_b32 v19, v69, v19
	v_cndmask_b32_e64 v21, v95, v16, s[2:3]
	s_waitcnt lgkmcnt(1)
	v_add_f32_e32 v17, v18, v17
	v_cndmask_b32_e64 v18, v94, v98, s[2:3]
	ds_bpermute_b32 v18, v69, v18
	ds_bpermute_b32 v21, v69, v21
	v_cndmask_b32_e64 v20, v97, v77, s[2:3]
	s_waitcnt lgkmcnt(2)
	v_add_f32_e32 v19, v20, v19
	v_cndmask_b32_e64 v20, v98, v94, s[2:3]
	v_cndmask_b32_e64 v16, v16, v95, s[2:3]
	s_waitcnt lgkmcnt(1)
	v_add_f32_e32 v18, v20, v18
	s_waitcnt lgkmcnt(0)
	v_add_f32_e32 v16, v16, v21
	v_cndmask_b32_e64 v20, v17, v18, s[4:5]
	v_cndmask_b32_e64 v21, v19, v16, s[4:5]
	ds_bpermute_b32 v20, v68, v20
	ds_bpermute_b32 v21, v68, v21
	v_cndmask_b32_e64 v17, v18, v17, s[4:5]
	v_cndmask_b32_e64 v16, v16, v19, s[4:5]
	s_waitcnt lgkmcnt(1)
	v_add_f32_e32 v17, v17, v20
	s_waitcnt lgkmcnt(0)
	v_add_f32_e32 v16, v16, v21
	v_cndmask_b32_e64 v18, v17, v16, s[6:7]
	s_nop 1
	v_mov_b32_dpp v18, v18 row_ror:8 row_mask:0xf bank_mask:0xf
	v_cndmask_b32_e64 v16, v16, v17, s[6:7]
	s_waitcnt lgkmcnt(0)
	v_add_f32_e32 v16, v16, v18
	s_nop 1
	v_mov_b32_dpp v17, v16 quad_perm:[3,2,1,0] row_mask:0xf bank_mask:0xf
	s_nop 1
	v_mov_b32_dpp v17, v17 row_half_mirror row_mask:0xf bank_mask:0xf
	s_waitcnt lgkmcnt(0)
	v_add_f32_e32 v16, v16, v17
	s_nop 1
	v_mov_b32_dpp v17, v16 quad_perm:[2,3,0,1] row_mask:0xf bank_mask:0xf
	s_waitcnt lgkmcnt(0)
	v_add_f32_e32 v16, v16, v17
	s_nop 1
	v_mov_b32_dpp v17, v16 quad_perm:[1,0,3,2] row_mask:0xf bank_mask:0xf
	s_and_saveexec_b64 s[10:11], s[8:9]
	s_cbranch_execz .LBB0_102
	global_load_dword v18, v[42:43], off
	s_waitcnt lgkmcnt(0)
	v_add_f32_e32 v16, v16, v17
	s_sub_u32 s16, s16, s37
	s_subb_u32 s17, s17, s38
	s_waitcnt vmcnt(0)
	v_add_f32_e32 v16, v16, v18
	v_mul_f32_e64 v17, |v16|, s30
	v_exp_f32_e32 v30, v17
	v_min_f32_e32 v31, 0, v16
	v_add_f32_e32 v18, 1.0, v30
	v_add_f32_e32 v19, -1.0, v18
	v_frexp_mant_f32_e32 v20, v18
	v_cvt_f64_f32_e32 v[16:17], v18
	v_sub_f32_e32 v21, v19, v18
	v_frexp_exp_i32_f64_e32 v16, v[16:17]
	v_cmp_gt_f32_e32 vcc, s31, v20
	v_sub_f32_e32 v19, v30, v19
	v_add_f32_e32 v17, 1.0, v21
	v_subbrev_co_u32_e32 v16, vcc, 0, v16, vcc
	v_add_f32_e32 v17, v19, v17
	v_sub_u32_e32 v19, 0, v16
	v_ldexp_f32 v18, v18, v19
	v_add_f32_e32 v20, -1.0, v18
	v_add_f32_e32 v21, 1.0, v18
	v_ldexp_f32 v17, v17, v19
	v_add_f32_e32 v19, 1.0, v20
	v_add_f32_e32 v22, -1.0, v21
	v_sub_f32_e32 v19, v18, v19
	v_sub_f32_e32 v18, v18, v22
	v_add_f32_e32 v22, v17, v19
	v_add_f32_e32 v17, v17, v18
	v_add_f32_e32 v24, v21, v17
	v_rcp_f32_e32 v25, v24
	v_add_f32_e32 v19, v20, v22
	v_sub_f32_e32 v20, v19, v20
	v_sub_f32_e32 v18, v24, v21
	v_mul_f32_e32 v27, v19, v25
	v_sub_f32_e32 v26, v22, v20
	v_mul_f32_e32 v20, v24, v27
	v_sub_f32_e32 v17, v17, v18
	v_fma_f32 v22, v27, v24, -v20
	v_fmac_f32_e32 v22, v27, v17
	v_add_f32_e32 v18, v20, v22
	v_sub_f32_e32 v21, v19, v18
	v_mov_b32_e32 v23, v18
	v_pk_add_f32 v[18:19], v[18:19], v[20:21] neg_lo:[0,1] neg_hi:[0,1]
	v_cvt_f32_i32_e32 v16, v16
	v_pk_add_f32 v[18:19], v[18:19], v[22:23] neg_lo:[0,1] neg_hi:[0,1]
	v_cmp_neq_f32_e32 vcc, s34, v30
	v_add_f32_e32 v19, v26, v19
	v_add_f32_e32 v18, v18, v19
	v_add_f32_e32 v19, v21, v18
	v_mul_f32_e32 v23, v25, v19
	v_mul_f32_e32 v20, v24, v23
	v_sub_f32_e32 v21, v21, v19
	v_add_f32_e32 v28, v27, v23
	v_fma_f32 v22, v23, v24, -v20
	v_add_f32_e32 v26, v18, v21
	v_sub_f32_e32 v18, v28, v27
	v_fmac_f32_e32 v22, v23, v17
	v_sub_f32_e32 v17, v23, v18
	v_add_f32_e32 v18, v20, v22
	v_sub_f32_e32 v21, v19, v18
	v_mov_b32_e32 v23, v18
	v_pk_add_f32 v[18:19], v[18:19], v[20:21] neg_lo:[0,1] neg_hi:[0,1]
	s_nop 0
	v_pk_add_f32 v[18:19], v[18:19], v[22:23] neg_lo:[0,1] neg_hi:[0,1]
	s_nop 0
	v_add_f32_e32 v19, v26, v19
	v_add_f32_e32 v18, v18, v19
	v_add_f32_e32 v18, v21, v18
	v_mul_f32_e32 v18, v25, v18
	v_add_f32_e32 v17, v17, v18
	v_add_f32_e32 v18, v28, v17
	v_mul_f32_e32 v20, v18, v18
	v_sub_f32_e32 v21, v18, v28
	v_fmamk_f32 v22, v20, 0x3e9b6dac, v72
	v_sub_f32_e32 v21, v17, v21
	v_mul_f32_e32 v17, v18, v20
	v_fmaak_f32 v45, v20, v22, 0x3f2aaada
	v_ldexp_f32 v23, v21, 1
	v_pk_mul_f32 v[20:21], v[16:17], v[44:45]
	v_ldexp_f32 v19, v18, 1
	v_fma_f32 v18, v16, s33, -v20
	v_fmac_f32_e32 v18, 0xb102e308, v16
	v_pk_add_f32 v[16:17], v[20:21], v[18:19]
	v_mov_b32_e32 v22, v20
	v_sub_f32_e32 v26, v17, v19
	v_pk_add_f32 v[24:25], v[16:17], v[20:21] neg_lo:[0,1] neg_hi:[0,1]
	v_sub_f32_e32 v20, v21, v26
	v_add_f32_e32 v23, v23, v20
	v_pk_add_f32 v[20:21], v[16:17], v[22:23]
	v_mov_b32_e32 v19, v16
	v_mov_b32_e32 v25, v21
	v_pk_add_f32 v[28:29], v[18:19], v[24:25] neg_lo:[0,1] neg_hi:[0,1]
	v_pk_add_f32 v[18:19], v[18:19], v[24:25]
	v_mov_b32_e32 v27, v16
	v_pk_add_f32 v[24:25], v[18:19], v[16:17] op_sel:[1,0] op_sel_hi:[0,1] neg_lo:[0,1] neg_hi:[0,1]
	v_mov_b32_e32 v26, v23
	v_mov_b32_e32 v22, v21
	v_mov_b32_e32 v23, v19
	v_pk_mov_b32 v[16:17], v[16:17], v[24:25] op_sel:[1,0]
	v_pk_add_f32 v[20:21], v[20:21], v[24:25] op_sel_hi:[1,0] neg_lo:[0,1] neg_hi:[0,1]
	v_pk_add_f32 v[16:17], v[22:23], v[16:17] neg_lo:[0,1] neg_hi:[0,1]
	v_mov_b32_e32 v20, v28
	v_pk_add_f32 v[16:17], v[26:27], v[16:17] neg_lo:[0,1] neg_hi:[0,1]
	v_mov_b32_e32 v29, v19
	v_pk_add_f32 v[20:21], v[20:21], v[16:17]
	s_nop 0
	v_pk_add_f32 v[22:23], v[20:21], v[20:21] op_sel:[0,1] op_sel_hi:[1,0]
	s_nop 0
	v_pk_add_f32 v[18:19], v[18:19], v[22:23] op_sel:[1,0] op_sel_hi:[0,1]
	v_mov_b32_e32 v21, v18
	v_mov_b32_e32 v17, v22
	v_pk_add_f32 v[22:23], v[20:21], v[28:29] neg_lo:[0,1] neg_hi:[0,1]
	s_nop 0
	v_sub_f32_e32 v19, v20, v22
	v_pk_add_f32 v[16:17], v[16:17], v[22:23] neg_lo:[0,1] neg_hi:[0,1]
	v_sub_f32_e32 v19, v28, v19
	v_add_f32_e32 v16, v16, v19
	v_add_f32_e32 v16, v16, v17
	v_add_f32_e32 v16, v18, v16
	v_cndmask_b32_e32 v16, v74, v16, vcc
	v_cmp_ngt_f32_e32 vcc, -1.0, v30
	s_nop 1
	v_cndmask_b32_e32 v16, v75, v16, vcc
	v_cmp_neq_f32_e32 vcc, -1.0, v30
	s_nop 1
	v_cndmask_b32_e32 v16, v76, v16, vcc
	v_cmp_lt_f32_e64 vcc, |v30|, s35
	s_nop 1
	v_cndmask_b32_e32 v16, v16, v30, vcc
	v_sub_f32_e32 v18, v31, v16
	v_lshl_add_u64 v[16:17], s[16:17], 2, v[46:47]
	global_store_dword v[16:17], v18, off offset:4
	s_branch .LBB0_102

.LBB0_250:
	s_or_b64 exec, exec, s[8:9]
	s_nop 1
	v_mov_b32_dpp v0, v34 quad_perm:[1,0,3,2] row_mask:0xf bank_mask:0xf
	v_max_f32_e32 v1, v34, v34
	s_ashr_i32 s45, s44, 31
	s_lshl_b32 s35, s75, 6
	s_waitcnt lgkmcnt(0)
	v_max_f32_e32 v0, v0, v0
	v_max_f32_e32 v0, v1, v0
	s_nop 1
	v_mov_b32_dpp v1, v0 quad_perm:[2,3,0,1] row_mask:0xf bank_mask:0xf
	s_waitcnt lgkmcnt(0)
	v_max_f32_e32 v1, v1, v1
	v_max_f32_e32 v0, v0, v1
	s_nop 1
	v_mov_b32_dpp v1, v0 quad_perm:[3,2,1,0] row_mask:0xf bank_mask:0xf
	s_nop 1
	v_mov_b32_dpp v1, v1 row_half_mirror row_mask:0xf bank_mask:0xf
	s_waitcnt lgkmcnt(0)
	v_max_f32_e32 v1, v1, v1
	v_max_f32_e32 v0, v0, v1
	s_nop 1
	v_mov_b32_dpp v1, v0 row_ror:8 row_mask:0xf bank_mask:0xf
	s_waitcnt lgkmcnt(0)
	v_max_f32_e32 v1, v1, v1
	v_max_f32_e32 v0, v0, v1
	ds_bpermute_b32 v1, v186, v0
	s_waitcnt lgkmcnt(0)
	v_max_f32_e32 v1, v1, v1
	v_max_f32_e32 v0, v0, v1
	ds_bpermute_b32 v1, v225, v0
	s_and_saveexec_b64 s[8:9], s[2:3]
	s_cbranch_execz .LBB0_252
	s_waitcnt lgkmcnt(0)
	v_max_f32_e32 v1, v1, v1
	v_max_f32_e32 v0, v0, v0
	v_max_f32_e32 v0, v0, v1
	v_mov_b32_e32 v1, s52
	ds_write_b32 v1, v0

.LBB0_273:
	s_or_b64 exec, exec, s[8:9]
	s_and_saveexec_b64 s[8:9], s[6:7]
	v_mov_b32_e32 v0, s66
	ds_write_b64 v0, v[110:111]
	s_or_b64 exec, exec, s[8:9]
	s_lshl_b32 s42, s51, 8
	s_add_u32 s50, s45, s42
	s_addc_u32 s35, s46, 0
	s_mul_i32 s43, s35, 0x1e00
	v_mad_u64_u32 v[0:1], s[8:9], s50, v233, v[126:127]
	v_add_u32_e32 v1, s43, v1
	global_load_dwordx4 v[64:67], v[0:1], off
	global_load_dwordx4 v[68:71], v[0:1], off offset:32
	global_load_dwordx4 v[72:75], v[0:1], off offset:64
	global_load_dwordx4 v[76:79], v[0:1], off offset:96
	v_add_u32_e32 v0, s42, v181
	v_mad_u64_u32 v[12:13], s[8:9], v0, s56, v[128:129]
	v_lshl_add_u32 v16, v0, 3, 0
	global_load_dwordx4 v[0:3], v[12:13], off offset:1024
	global_load_dwordx4 v[4:7], v[12:13], off offset:1056
	global_load_dwordx4 v[8:11], v[12:13], off offset:1088
	s_nop 0
	global_load_dwordx4 v[12:15], v[12:13], off offset:1120
	s_waitcnt vmcnt(4)
	v_and_b32_e32 v18, 0xffff0000, v64
	v_and_b32_e32 v20, 0xffff0000, v65
	v_lshlrev_b32_e32 v17, 16, v64
	v_lshlrev_b32_e32 v19, 16, v65
	v_and_b32_e32 v22, 0xffff0000, v66
	v_mul_f32_e32 v49, v18, v18
	v_mul_f32_e32 v50, v20, v20
	v_lshlrev_b32_e32 v21, 16, v66
	v_and_b32_e32 v24, 0xffff0000, v67
	v_mul_f32_e32 v51, v22, v22
	v_fmac_f32_e32 v49, v17, v17
	v_fmac_f32_e32 v50, v19, v19
	v_lshlrev_b32_e32 v23, 16, v67
	v_and_b32_e32 v26, 0xffff0000, v68
	v_mul_f32_e32 v52, v24, v24
	v_fmac_f32_e32 v51, v21, v21
	v_add_f32_e32 v49, v49, v50
	v_lshlrev_b32_e32 v25, 16, v68
	v_and_b32_e32 v28, 0xffff0000, v69
	v_mul_f32_e32 v53, v26, v26
	v_fmac_f32_e32 v52, v23, v23
	v_add_f32_e32 v49, v51, v49
	v_lshlrev_b32_e32 v27, 16, v69
	v_and_b32_e32 v30, 0xffff0000, v70
	v_mul_f32_e32 v54, v28, v28
	v_fmac_f32_e32 v53, v25, v25
	v_add_f32_e32 v49, v52, v49
	v_lshlrev_b32_e32 v29, 16, v70
	v_and_b32_e32 v32, 0xffff0000, v71
	v_mul_f32_e32 v55, v30, v30
	v_fmac_f32_e32 v54, v27, v27
	v_add_f32_e32 v49, v53, v49
	v_lshlrev_b32_e32 v31, 16, v71
	v_and_b32_e32 v34, 0xffff0000, v72
	v_mul_f32_e32 v56, v32, v32
	v_fmac_f32_e32 v55, v29, v29
	v_add_f32_e32 v49, v54, v49
	v_lshlrev_b32_e32 v33, 16, v72
	v_and_b32_e32 v36, 0xffff0000, v73
	v_mul_f32_e32 v57, v34, v34
	v_fmac_f32_e32 v56, v31, v31
	v_add_f32_e32 v49, v55, v49
	v_lshlrev_b32_e32 v35, 16, v73
	v_and_b32_e32 v38, 0xffff0000, v74
	v_mul_f32_e32 v58, v36, v36
	v_fmac_f32_e32 v57, v33, v33
	v_add_f32_e32 v49, v56, v49
	v_lshlrev_b32_e32 v37, 16, v74
	v_and_b32_e32 v40, 0xffff0000, v75
	v_mul_f32_e32 v59, v38, v38
	v_fmac_f32_e32 v58, v35, v35
	v_add_f32_e32 v49, v57, v49
	v_lshlrev_b32_e32 v39, 16, v75
	v_and_b32_e32 v42, 0xffff0000, v76
	v_mul_f32_e32 v60, v40, v40
	v_fmac_f32_e32 v59, v37, v37
	v_add_f32_e32 v49, v58, v49
	v_lshlrev_b32_e32 v41, 16, v76
	v_and_b32_e32 v44, 0xffff0000, v77
	v_mul_f32_e32 v61, v42, v42
	v_fmac_f32_e32 v60, v39, v39
	v_add_f32_e32 v49, v59, v49
	v_lshlrev_b32_e32 v43, 16, v77
	v_and_b32_e32 v46, 0xffff0000, v78
	v_mul_f32_e32 v62, v44, v44
	v_fmac_f32_e32 v61, v41, v41
	v_add_f32_e32 v49, v60, v49
	v_lshlrev_b32_e32 v45, 16, v78
	v_and_b32_e32 v48, 0xffff0000, v79
	v_mul_f32_e32 v63, v46, v46
	v_fmac_f32_e32 v62, v43, v43
	v_add_f32_e32 v49, v61, v49
	v_lshlrev_b32_e32 v47, 16, v79
	v_mul_f32_e32 v80, v48, v48
	v_fmac_f32_e32 v63, v45, v45
	v_add_f32_e32 v49, v62, v49
	v_fmac_f32_e32 v80, v47, v47
	v_add_f32_e32 v49, v63, v49
	v_add_f32_e32 v49, v80, v49
	v_mov_b32_e32 v50, v49
	s_nop 1
	v_permlane32_swap_b32_e32 v49, v50
	v_add_f32_e32 v49, v49, v50
	s_waitcnt vmcnt(3)
	v_lshlrev_b32_e32 v50, 16, v0
	v_and_b32_e32 v0, 0xffff0000, v0
	v_lshlrev_b32_e32 v51, 16, v1
	v_and_b32_e32 v1, 0xffff0000, v1
	v_mul_f32_e32 v0, v18, v0
	v_lshlrev_b32_e32 v52, 16, v2
	v_and_b32_e32 v2, 0xffff0000, v2
	v_mul_f32_e32 v1, v20, v1
	v_fmac_f32_e32 v0, v17, v50
	v_lshlrev_b32_e32 v53, 16, v3
	v_and_b32_e32 v3, 0xffff0000, v3
	v_mul_f32_e32 v2, v22, v2
	v_fmac_f32_e32 v1, v19, v51
	v_add_f32_e32 v0, 0, v0
	s_waitcnt vmcnt(2)
	v_lshlrev_b32_e32 v54, 16, v4
	v_and_b32_e32 v4, 0xffff0000, v4
	v_mul_f32_e32 v3, v24, v3
	v_fmac_f32_e32 v2, v21, v52
	v_add_f32_e32 v0, v1, v0
	v_lshlrev_b32_e32 v55, 16, v5
	v_and_b32_e32 v5, 0xffff0000, v5
	v_mul_f32_e32 v4, v26, v4
	v_fmac_f32_e32 v3, v23, v53
	v_add_f32_e32 v0, v2, v0
	v_lshlrev_b32_e32 v56, 16, v6
	v_and_b32_e32 v6, 0xffff0000, v6
	v_mul_f32_e32 v5, v28, v5
	v_fmac_f32_e32 v4, v25, v54
	v_add_f32_e32 v0, v3, v0
	v_lshlrev_b32_e32 v57, 16, v7
	v_and_b32_e32 v7, 0xffff0000, v7
	v_mul_f32_e32 v6, v30, v6
	v_fmac_f32_e32 v5, v27, v55
	v_add_f32_e32 v0, v4, v0
	s_waitcnt vmcnt(1)
	v_lshlrev_b32_e32 v58, 16, v8
	v_and_b32_e32 v8, 0xffff0000, v8
	v_mul_f32_e32 v7, v32, v7
	v_fmac_f32_e32 v6, v29, v56
	v_add_f32_e32 v0, v5, v0
	v_lshlrev_b32_e32 v59, 16, v9
	v_and_b32_e32 v9, 0xffff0000, v9
	v_mul_f32_e32 v8, v34, v8
	v_fmac_f32_e32 v7, v31, v57
	v_add_f32_e32 v0, v6, v0
	v_lshlrev_b32_e32 v60, 16, v10
	v_and_b32_e32 v10, 0xffff0000, v10
	v_mul_f32_e32 v9, v36, v9
	v_fmac_f32_e32 v8, v33, v58
	v_add_f32_e32 v0, v7, v0
	v_lshlrev_b32_e32 v61, 16, v11
	v_and_b32_e32 v11, 0xffff0000, v11
	v_mul_f32_e32 v10, v38, v10
	v_fmac_f32_e32 v9, v35, v59
	v_add_f32_e32 v0, v8, v0
	s_waitcnt vmcnt(0)
	v_lshlrev_b32_e32 v62, 16, v12
	v_and_b32_e32 v12, 0xffff0000, v12
	v_mul_f32_e32 v11, v40, v11
	v_fmac_f32_e32 v10, v37, v60
	v_add_f32_e32 v0, v9, v0
	v_lshlrev_b32_e32 v63, 16, v13
	v_and_b32_e32 v13, 0xffff0000, v13
	v_mul_f32_e32 v12, v42, v12
	v_fmac_f32_e32 v11, v39, v61
	v_add_f32_e32 v0, v10, v0
	v_lshlrev_b32_e32 v80, 16, v14
	v_and_b32_e32 v14, 0xffff0000, v14
	v_mul_f32_e32 v13, v44, v13
	v_fmac_f32_e32 v12, v41, v62
	v_add_f32_e32 v0, v11, v0
	v_lshlrev_b32_e32 v81, 16, v15
	v_and_b32_e32 v15, 0xffff0000, v15
	v_mul_f32_e32 v14, v46, v14
	v_fmac_f32_e32 v13, v43, v63
	v_add_f32_e32 v0, v12, v0
	v_mul_f32_e32 v15, v48, v15
	v_fmac_f32_e32 v14, v45, v80
	v_add_f32_e32 v0, v13, v0
	v_fmac_f32_e32 v15, v47, v81
	v_add_f32_e32 v0, v14, v0
	s_waitcnt vmcnt(0) lgkmcnt(0)
	s_barrier
	v_add_f32_e32 v2, v15, v0
	v_add_u32_e32 v0, 0x10000, v16
	ds_read_b64 v[0:1], v0
	v_mov_b32_e32 v3, v2
	s_nop 1
	v_permlane32_swap_b32_e32 v2, v3
	v_add_f32_e32 v2, v2, v3
	s_waitcnt lgkmcnt(0)
	v_lshlrev_b32_e32 v3, 16, v0
	v_and_b32_e32 v0, 0xffff0000, v0
	v_add_f32_e32 v0, v3, v0
	v_lshlrev_b32_e32 v1, 16, v1
	v_add_f32_e32 v0, v0, v1
	v_add_f32_e32 v0, v2, v0
	s_nop 1
	v_mov_b32_dpp v1, v49 quad_perm:[1,0,3,2] row_mask:0xf bank_mask:0xf
	s_nop 1
	v_mov_b32_dpp v2, v0 quad_perm:[1,0,3,2] row_mask:0xf bank_mask:0xf
	s_waitcnt lgkmcnt(0)
	v_max_f32_e32 v1, v1, v1
	s_waitcnt lgkmcnt(0)
	v_max_f32_e32 v2, v2, v2
	v_max_f32_e32 v1, v49, v1
	v_min_f32_e32 v0, v0, v2
	s_nop 1
	v_mov_b32_dpp v3, v1 quad_perm:[2,3,0,1] row_mask:0xf bank_mask:0xf
	s_nop 1
	v_mov_b32_dpp v2, v0 quad_perm:[2,3,0,1] row_mask:0xf bank_mask:0xf
	s_waitcnt lgkmcnt(0)
	v_max_f32_e32 v3, v3, v3
	s_waitcnt lgkmcnt(0)
	v_max_f32_e32 v2, v2, v2
	v_max_f32_e32 v1, v1, v3
	v_min_f32_e32 v0, v0, v2
	s_nop 1
	v_mov_b32_dpp v3, v1 quad_perm:[3,2,1,0] row_mask:0xf bank_mask:0xf
	s_nop 1
	v_mov_b32_dpp v3, v3 row_half_mirror row_mask:0xf bank_mask:0xf
	s_nop 1
	v_mov_b32_dpp v2, v0 quad_perm:[3,2,1,0] row_mask:0xf bank_mask:0xf
	s_nop 1
	v_mov_b32_dpp v2, v2 row_half_mirror row_mask:0xf bank_mask:0xf
	s_waitcnt lgkmcnt(0)
	v_max_f32_e32 v3, v3, v3
	s_waitcnt lgkmcnt(0)
	v_max_f32_e32 v2, v2, v2
	v_max_f32_e32 v1, v1, v3
	v_min_f32_e32 v0, v0, v2
	s_nop 1
	v_mov_b32_dpp v3, v1 row_ror:8 row_mask:0xf bank_mask:0xf
	s_nop 1
	v_mov_b32_dpp v2, v0 row_ror:8 row_mask:0xf bank_mask:0xf
	s_waitcnt lgkmcnt(0)
	v_max_f32_e32 v3, v3, v3
	s_waitcnt lgkmcnt(0)
	v_max_f32_e32 v2, v2, v2
	v_max_f32_e32 v1, v1, v3
	v_min_f32_e32 v0, v0, v2
	ds_bpermute_b32 v3, v186, v1
	ds_bpermute_b32 v2, v186, v0
	s_and_saveexec_b64 s[8:9], s[2:3]
	s_cbranch_execz .LBB0_277
	s_waitcnt lgkmcnt(0)
	v_max_f32_e32 v3, v3, v3
	v_max_f32_e32 v1, v1, v1
	s_waitcnt lgkmcnt(0)
	v_max_f32_e32 v2, v2, v2
	v_max_f32_e32 v0, v0, v0
	v_max_f32_e32 v1, v1, v3
	v_min_f32_e32 v0, v0, v2
	v_mov_b32_e32 v2, s59
	ds_write2_b32 v2, v1, v0 offset1:8

.LBB0_504:
	v_add_u32_e32 v126, 0, v235
	s_waitcnt lgkmcnt(0)
	ds_read_b128 v[0:3], v126
	ds_read_b128 v[4:7], v126 offset:1024
	ds_read_b128 v[8:11], v126 offset:2048
	ds_read_b128 v[12:15], v126 offset:3072
	ds_read_b128 v[16:19], v126 offset:4096
	s_waitcnt lgkmcnt(4)
	v_pk_fma_f32 v[20:21], v[146:147], v[0:1], 0 op_sel_hi:[1,1,0]
	ds_read_b128 v[24:27], v126 offset:6144
	v_pk_fma_f32 v[20:21], v[144:145], v[2:3], v[20:21]
	s_waitcnt lgkmcnt(1)
	v_pk_fma_f32 v[28:29], v[146:147], v[16:17], 0 op_sel_hi:[1,1,0]
	v_pk_fma_f32 v[20:21], v[150:151], v[4:5], v[20:21]
	v_pk_fma_f32 v[32:33], v[144:145], v[18:19], v[28:29]
	v_pk_fma_f32 v[20:21], v[148:149], v[6:7], v[20:21]
	ds_read_b128 v[28:31], v126 offset:7168
	v_pk_fma_f32 v[20:21], v[154:155], v[8:9], v[20:21]
	s_nop 0
	v_pk_fma_f32 v[20:21], v[152:153], v[10:11], v[20:21]
	s_nop 0
	v_pk_fma_f32 v[20:21], v[158:159], v[12:13], v[20:21]
	s_nop 0
	v_pk_fma_f32 v[208:209], v[156:157], v[14:15], v[20:21]
	ds_read_b128 v[20:23], v126 offset:5120
	s_waitcnt lgkmcnt(0)
	v_pk_fma_f32 v[32:33], v[150:151], v[20:21], v[32:33]
	s_nop 0
	v_pk_fma_f32 v[32:33], v[148:149], v[22:23], v[32:33]
	s_nop 0
	v_pk_fma_f32 v[32:33], v[154:155], v[24:25], v[32:33]
	s_nop 0
	v_pk_fma_f32 v[32:33], v[152:153], v[26:27], v[32:33]
	s_nop 0
	v_pk_fma_f32 v[32:33], v[158:159], v[28:29], v[32:33]
	s_nop 0
	v_pk_fma_f32 v[238:239], v[156:157], v[30:31], v[32:33]
	ds_read_b128 v[32:35], v126 offset:8192
	ds_read_b128 v[36:39], v126 offset:9216
	ds_read_b128 v[40:43], v126 offset:10240
	ds_read_b128 v[44:47], v126 offset:11264
	ds_read_b128 v[48:51], v126 offset:12288
	s_waitcnt lgkmcnt(4)
	v_pk_fma_f32 v[52:53], v[146:147], v[32:33], 0 op_sel_hi:[1,1,0]
	ds_read_b128 v[56:59], v126 offset:14336
	v_pk_fma_f32 v[52:53], v[144:145], v[34:35], v[52:53]
	s_waitcnt lgkmcnt(1)
	v_pk_fma_f32 v[60:61], v[146:147], v[48:49], 0 op_sel_hi:[1,1,0]
	v_pk_fma_f32 v[52:53], v[150:151], v[36:37], v[52:53]
	v_pk_fma_f32 v[64:65], v[144:145], v[50:51], v[60:61]
	v_pk_fma_f32 v[52:53], v[148:149], v[38:39], v[52:53]
	ds_read_b128 v[60:63], v126 offset:15360
	v_pk_fma_f32 v[52:53], v[154:155], v[40:41], v[52:53]
	s_nop 0
	v_pk_fma_f32 v[52:53], v[152:153], v[42:43], v[52:53]
	s_nop 0
	v_pk_fma_f32 v[52:53], v[158:159], v[44:45], v[52:53]
	s_nop 0
	v_pk_fma_f32 v[240:241], v[156:157], v[46:47], v[52:53]
	ds_read_b128 v[52:55], v126 offset:13312
	s_waitcnt lgkmcnt(0)
	v_pk_fma_f32 v[64:65], v[150:151], v[52:53], v[64:65]
	s_nop 0
	v_pk_fma_f32 v[64:65], v[148:149], v[54:55], v[64:65]
	s_nop 0
	v_pk_fma_f32 v[64:65], v[154:155], v[56:57], v[64:65]
	s_nop 0
	v_pk_fma_f32 v[64:65], v[152:153], v[58:59], v[64:65]
	s_nop 0
	v_pk_fma_f32 v[64:65], v[158:159], v[60:61], v[64:65]
	s_nop 0
	v_pk_fma_f32 v[242:243], v[156:157], v[62:63], v[64:65]
	ds_read_b128 v[64:67], v126 offset:16384
	ds_read_b128 v[68:71], v126 offset:17408
	ds_read_b128 v[72:75], v126 offset:18432
	ds_read_b128 v[76:79], v126 offset:19456
	ds_read_b128 v[80:83], v126 offset:20480
	s_waitcnt lgkmcnt(4)
	v_pk_fma_f32 v[84:85], v[146:147], v[64:65], 0 op_sel_hi:[1,1,0]
	ds_read_b128 v[88:91], v126 offset:22528
	v_pk_fma_f32 v[84:85], v[144:145], v[66:67], v[84:85]
	s_waitcnt lgkmcnt(1)
	v_pk_fma_f32 v[92:93], v[146:147], v[80:81], 0 op_sel_hi:[1,1,0]
	v_pk_fma_f32 v[84:85], v[150:151], v[68:69], v[84:85]
	v_pk_fma_f32 v[96:97], v[144:145], v[82:83], v[92:93]
	v_pk_fma_f32 v[84:85], v[148:149], v[70:71], v[84:85]
	ds_read_b128 v[92:95], v126 offset:23552
	v_pk_fma_f32 v[84:85], v[154:155], v[72:73], v[84:85]
	s_nop 0
	v_pk_fma_f32 v[84:85], v[152:153], v[74:75], v[84:85]
	s_nop 0
	v_pk_fma_f32 v[84:85], v[158:159], v[76:77], v[84:85]
	s_nop 0
	v_pk_fma_f32 v[244:245], v[156:157], v[78:79], v[84:85]
	ds_read_b128 v[84:87], v126 offset:21504
	s_waitcnt lgkmcnt(0)
	v_pk_fma_f32 v[96:97], v[150:151], v[84:85], v[96:97]
	s_nop 0
	v_pk_fma_f32 v[96:97], v[148:149], v[86:87], v[96:97]
	s_nop 0
	v_pk_fma_f32 v[96:97], v[154:155], v[88:89], v[96:97]
	s_nop 0
	v_pk_fma_f32 v[96:97], v[152:153], v[90:91], v[96:97]
	s_nop 0
	v_pk_fma_f32 v[96:97], v[158:159], v[92:93], v[96:97]
	s_nop 0
	v_pk_fma_f32 v[246:247], v[156:157], v[94:95], v[96:97]
	ds_read_b128 v[96:99], v126 offset:24576
	ds_read_b128 v[100:103], v126 offset:25600
	ds_read_b128 v[104:107], v126 offset:26624
	ds_read_b128 v[108:111], v126 offset:27648
	ds_read_b128 v[112:115], v126 offset:28672
	s_waitcnt lgkmcnt(4)
	v_pk_fma_f32 v[116:117], v[146:147], v[96:97], 0 op_sel_hi:[1,1,0]
	ds_read_b128 v[120:123], v126 offset:30720
	v_pk_fma_f32 v[116:117], v[144:145], v[98:99], v[116:117]
	s_waitcnt lgkmcnt(1)
	v_pk_fma_f32 v[124:125], v[146:147], v[112:113], 0 op_sel_hi:[1,1,0]
	v_pk_fma_f32 v[116:117], v[150:151], v[100:101], v[116:117]
	v_pk_fma_f32 v[250:251], v[144:145], v[114:115], v[124:125]
	v_pk_fma_f32 v[116:117], v[148:149], v[102:103], v[116:117]
	s_nop 0
	v_pk_fma_f32 v[116:117], v[154:155], v[104:105], v[116:117]
	s_nop 0
	v_pk_fma_f32 v[116:117], v[152:153], v[106:107], v[116:117]
	s_nop 0
	v_pk_fma_f32 v[116:117], v[158:159], v[108:109], v[116:117]
	s_nop 0
	v_pk_fma_f32 v[248:249], v[156:157], v[110:111], v[116:117]
	ds_read_b128 v[116:119], v126 offset:29696
	ds_read_b128 v[124:127], v126 offset:31744
	s_waitcnt lgkmcnt(1)
	v_pk_fma_f32 v[250:251], v[150:151], v[116:117], v[250:251]
	s_nop 0
	v_pk_fma_f32 v[250:251], v[148:149], v[118:119], v[250:251]
	s_nop 0
	v_pk_fma_f32 v[250:251], v[154:155], v[120:121], v[250:251]
	s_nop 0
	v_pk_fma_f32 v[250:251], v[152:153], v[122:123], v[250:251]
	s_waitcnt lgkmcnt(0)
	v_pk_fma_f32 v[250:251], v[158:159], v[124:125], v[250:251]
	s_nop 0
	v_pk_fma_f32 v[250:251], v[156:157], v[126:127], v[250:251]
	v_add_f32_e32 v208, v208, v209
	v_add_f32_e32 v209, v238, v239
	v_add_f32_e32 v239, v244, v245
	v_add_f32_e32 v237, v240, v241
	v_cndmask_b32_e64 v240, v208, v239, s[2:3]
	ds_bpermute_b32 v240, v220, v240
	v_add_f32_e32 v238, v242, v243
	v_add_f32_e32 v241, v246, v247
	v_add_f32_e32 v242, v248, v249
	v_add_f32_e32 v243, v250, v251
	v_cndmask_b32_e64 v208, v239, v208, s[2:3]
	s_waitcnt lgkmcnt(0)
	v_add_f32_e32 v208, v208, v240
	v_cndmask_b32_e64 v239, v209, v241, s[2:3]
	v_cndmask_b32_e64 v209, v241, v209, s[2:3]
	v_cndmask_b32_e64 v240, v237, v242, s[2:3]
	v_cndmask_b32_e64 v241, v238, v243, s[2:3]
	ds_bpermute_b32 v239, v220, v239
	ds_bpermute_b32 v240, v220, v240
	ds_bpermute_b32 v241, v220, v241
	v_cndmask_b32_e64 v237, v242, v237, s[2:3]
	v_cndmask_b32_e64 v238, v243, v238, s[2:3]
	s_waitcnt lgkmcnt(2)
	v_add_f32_e32 v209, v209, v239
	s_waitcnt lgkmcnt(1)
	v_add_f32_e32 v237, v237, v240
	s_waitcnt lgkmcnt(0)
	v_add_f32_e32 v238, v238, v241
	v_cndmask_b32_e64 v239, v208, v237, s[4:5]
	v_cndmask_b32_e64 v240, v209, v238, s[4:5]
	ds_bpermute_b32 v239, v219, v239
	ds_bpermute_b32 v240, v219, v240
	v_cndmask_b32_e64 v208, v237, v208, s[4:5]
	v_cndmask_b32_e64 v209, v238, v209, s[4:5]
	s_waitcnt lgkmcnt(1)
	v_add_f32_e32 v208, v208, v239
	s_waitcnt lgkmcnt(0)
	v_add_f32_e32 v209, v209, v240
	v_cndmask_b32_e64 v237, v208, v209, s[6:7]
	s_nop 1
	v_mov_b32_dpp v237, v237 row_ror:8 row_mask:0xf bank_mask:0xf
	v_cndmask_b32_e64 v208, v209, v208, s[6:7]
	s_waitcnt lgkmcnt(0)
	v_add_f32_e32 v208, v208, v237
	s_nop 1
	v_mov_b32_dpp v209, v208 quad_perm:[3,2,1,0] row_mask:0xf bank_mask:0xf
	s_nop 1
	v_mov_b32_dpp v209, v209 row_half_mirror row_mask:0xf bank_mask:0xf
	v_add_u32_e32 v237, 0, v236
	s_waitcnt lgkmcnt(0)
	v_add_f32_e32 v208, v208, v209
	s_nop 1
	v_mov_b32_dpp v209, v208 quad_perm:[2,3,0,1] row_mask:0xf bank_mask:0xf
	s_waitcnt lgkmcnt(0)
	v_add_f32_e32 v238, v208, v209
	s_nop 1
	v_mov_b32_dpp v239, v238 quad_perm:[1,0,3,2] row_mask:0xf bank_mask:0xf
	v_lshl_add_u64 v[208:209], v[138:139], 0, s[12:13]
	s_and_saveexec_b64 s[14:15], s[8:9]
	s_cbranch_execz .LBB0_506
	global_load_dword v240, v[208:209], off
	s_waitcnt lgkmcnt(0)
	v_add_f32_e32 v238, v238, v239
	v_add_u32_e32 v241, 0x20000, v237
	s_waitcnt vmcnt(0)
	v_add_f32_e32 v238, v238, v240
	ds_write_b32 v241, v238
.LBB0_506:
	s_or_b64 exec, exec, s[14:15]
	s_waitcnt lgkmcnt(0)
	v_pk_fma_f32 v[238:239], v[162:163], v[0:1], 0 op_sel_hi:[1,1,0]
	v_pk_fma_f32 v[240:241], v[162:163], v[16:17], 0 op_sel_hi:[1,1,0]
	v_pk_fma_f32 v[242:243], v[162:163], v[32:33], 0 op_sel_hi:[1,1,0]
	v_pk_fma_f32 v[246:247], v[162:163], v[64:65], 0 op_sel_hi:[1,1,0]
	v_pk_fma_f32 v[238:239], v[160:161], v[2:3], v[238:239]
	v_pk_fma_f32 v[240:241], v[160:161], v[18:19], v[240:241]
	v_pk_fma_f32 v[242:243], v[160:161], v[34:35], v[242:243]
	v_pk_fma_f32 v[246:247], v[160:161], v[66:67], v[246:247]
	v_pk_fma_f32 v[238:239], v[166:167], v[4:5], v[238:239]
	v_pk_fma_f32 v[240:241], v[166:167], v[20:21], v[240:241]
	v_pk_fma_f32 v[242:243], v[166:167], v[36:37], v[242:243]
	v_pk_fma_f32 v[246:247], v[166:167], v[68:69], v[246:247]
	v_pk_fma_f32 v[238:239], v[164:165], v[6:7], v[238:239]
	v_pk_fma_f32 v[240:241], v[164:165], v[22:23], v[240:241]
	v_pk_fma_f32 v[242:243], v[164:165], v[38:39], v[242:243]
	v_pk_fma_f32 v[246:247], v[164:165], v[70:71], v[246:247]
	v_pk_fma_f32 v[238:239], v[170:171], v[8:9], v[238:239]
	v_pk_fma_f32 v[240:241], v[170:171], v[24:25], v[240:241]
	v_pk_fma_f32 v[242:243], v[170:171], v[40:41], v[242:243]
	v_pk_fma_f32 v[246:247], v[170:171], v[72:73], v[246:247]
	v_pk_fma_f32 v[238:239], v[168:169], v[10:11], v[238:239]
	v_pk_fma_f32 v[240:241], v[168:169], v[26:27], v[240:241]
	v_pk_fma_f32 v[242:243], v[168:169], v[42:43], v[242:243]
	v_pk_fma_f32 v[246:247], v[168:169], v[74:75], v[246:247]
	v_pk_fma_f32 v[238:239], v[174:175], v[12:13], v[238:239]
	v_pk_fma_f32 v[240:241], v[174:175], v[28:29], v[240:241]
	v_pk_fma_f32 v[242:243], v[174:175], v[44:45], v[242:243]
	v_pk_fma_f32 v[244:245], v[162:163], v[48:49], 0 op_sel_hi:[1,1,0]
	v_pk_fma_f32 v[246:247], v[174:175], v[76:77], v[246:247]
	v_pk_fma_f32 v[248:249], v[162:163], v[80:81], 0 op_sel_hi:[1,1,0]
	v_pk_fma_f32 v[250:251], v[162:163], v[96:97], 0 op_sel_hi:[1,1,0]
	v_pk_fma_f32 v[252:253], v[162:163], v[112:113], 0 op_sel_hi:[1,1,0]
	v_pk_fma_f32 v[238:239], v[172:173], v[14:15], v[238:239]
	v_pk_fma_f32 v[240:241], v[172:173], v[30:31], v[240:241]
	v_pk_fma_f32 v[242:243], v[172:173], v[46:47], v[242:243]
	v_pk_fma_f32 v[244:245], v[160:161], v[50:51], v[244:245]
	v_pk_fma_f32 v[246:247], v[172:173], v[78:79], v[246:247]
	v_pk_fma_f32 v[248:249], v[160:161], v[82:83], v[248:249]
	v_pk_fma_f32 v[250:251], v[160:161], v[98:99], v[250:251]
	v_pk_fma_f32 v[252:253], v[160:161], v[114:115], v[252:253]
	v_pk_fma_f32 v[244:245], v[166:167], v[52:53], v[244:245]
	v_pk_fma_f32 v[248:249], v[166:167], v[84:85], v[248:249]
	v_pk_fma_f32 v[250:251], v[166:167], v[100:101], v[250:251]
	v_pk_fma_f32 v[252:253], v[166:167], v[116:117], v[252:253]
	v_add_f32_e32 v238, v238, v239
	v_add_f32_e32 v239, v240, v241
	v_add_f32_e32 v240, v242, v243
	v_add_f32_e32 v242, v246, v247
	v_pk_fma_f32 v[244:245], v[164:165], v[54:55], v[244:245]
	v_pk_fma_f32 v[248:249], v[164:165], v[86:87], v[248:249]
	v_pk_fma_f32 v[250:251], v[164:165], v[102:103], v[250:251]
	v_pk_fma_f32 v[252:253], v[164:165], v[118:119], v[252:253]
	v_cndmask_b32_e64 v243, v238, v242, s[2:3]
	v_pk_fma_f32 v[244:245], v[170:171], v[56:57], v[244:245]
	v_pk_fma_f32 v[248:249], v[170:171], v[88:89], v[248:249]
	v_pk_fma_f32 v[250:251], v[170:171], v[104:105], v[250:251]
	v_pk_fma_f32 v[252:253], v[170:171], v[120:121], v[252:253]
	ds_bpermute_b32 v243, v220, v243
	v_pk_fma_f32 v[244:245], v[168:169], v[58:59], v[244:245]
	v_pk_fma_f32 v[248:249], v[168:169], v[90:91], v[248:249]
	v_pk_fma_f32 v[250:251], v[168:169], v[106:107], v[250:251]
	v_pk_fma_f32 v[252:253], v[168:169], v[122:123], v[252:253]
	v_pk_fma_f32 v[244:245], v[174:175], v[60:61], v[244:245]
	v_pk_fma_f32 v[248:249], v[174:175], v[92:93], v[248:249]
	v_pk_fma_f32 v[250:251], v[174:175], v[108:109], v[250:251]
	v_pk_fma_f32 v[252:253], v[174:175], v[124:125], v[252:253]
	v_pk_fma_f32 v[244:245], v[172:173], v[62:63], v[244:245]
	v_pk_fma_f32 v[248:249], v[172:173], v[94:95], v[248:249]
	v_pk_fma_f32 v[250:251], v[172:173], v[110:111], v[250:251]
	v_pk_fma_f32 v[252:253], v[172:173], v[126:127], v[252:253]
	v_add_f32_e32 v241, v244, v245
	v_add_f32_e32 v244, v248, v249
	v_add_f32_e32 v245, v250, v251
	v_add_f32_e32 v246, v252, v253
	v_cndmask_b32_e64 v238, v242, v238, s[2:3]
	s_waitcnt lgkmcnt(0)
	v_add_f32_e32 v238, v238, v243
	v_cndmask_b32_e64 v242, v239, v244, s[2:3]
	v_cndmask_b32_e64 v239, v244, v239, s[2:3]
	v_cndmask_b32_e64 v243, v240, v245, s[2:3]
	v_cndmask_b32_e64 v244, v241, v246, s[2:3]
	ds_bpermute_b32 v242, v220, v242
	ds_bpermute_b32 v243, v220, v243
	ds_bpermute_b32 v244, v220, v244
	v_cndmask_b32_e64 v240, v245, v240, s[2:3]
	v_cndmask_b32_e64 v241, v246, v241, s[2:3]
	s_waitcnt lgkmcnt(2)
	v_add_f32_e32 v239, v239, v242
	s_waitcnt lgkmcnt(1)
	v_add_f32_e32 v240, v240, v243
	s_waitcnt lgkmcnt(0)
	v_add_f32_e32 v241, v241, v244
	v_cndmask_b32_e64 v242, v238, v240, s[4:5]
	v_cndmask_b32_e64 v243, v239, v241, s[4:5]
	ds_bpermute_b32 v242, v219, v242
	ds_bpermute_b32 v243, v219, v243
	v_cndmask_b32_e64 v238, v240, v238, s[4:5]
	v_cndmask_b32_e64 v239, v241, v239, s[4:5]
	s_waitcnt lgkmcnt(1)
	v_add_f32_e32 v238, v238, v242
	s_waitcnt lgkmcnt(0)
	v_add_f32_e32 v239, v239, v243
	v_cndmask_b32_e64 v240, v238, v239, s[6:7]
	s_nop 1
	v_mov_b32_dpp v240, v240 row_ror:8 row_mask:0xf bank_mask:0xf
	v_cndmask_b32_e64 v238, v239, v238, s[6:7]
	s_waitcnt lgkmcnt(0)
	v_add_f32_e32 v238, v238, v240
	s_nop 1
	v_mov_b32_dpp v239, v238 quad_perm:[3,2,1,0] row_mask:0xf bank_mask:0xf
	s_nop 1
	v_mov_b32_dpp v239, v239 row_half_mirror row_mask:0xf bank_mask:0xf
	s_waitcnt lgkmcnt(0)
	v_add_f32_e32 v238, v238, v239
	s_nop 1
	v_mov_b32_dpp v239, v238 quad_perm:[2,3,0,1] row_mask:0xf bank_mask:0xf
	s_waitcnt lgkmcnt(0)
	v_add_f32_e32 v238, v238, v239
	s_nop 1
	v_mov_b32_dpp v239, v238 quad_perm:[1,0,3,2] row_mask:0xf bank_mask:0xf
	s_and_saveexec_b64 s[14:15], s[8:9]
	s_cbranch_execz .LBB0_508
	global_load_dword v240, v[208:209], off
	s_waitcnt lgkmcnt(0)
	v_add_f32_e32 v238, v238, v239
	v_add_u32_e32 v241, 0x20080, v237
	s_waitcnt vmcnt(0)
	v_add_f32_e32 v238, v238, v240
	ds_write_b32 v241, v238
.LBB0_508:
	s_or_b64 exec, exec, s[14:15]
	s_waitcnt lgkmcnt(0)
	v_pk_fma_f32 v[238:239], v[178:179], v[0:1], 0 op_sel_hi:[1,1,0]
	v_pk_fma_f32 v[240:241], v[178:179], v[16:17], 0 op_sel_hi:[1,1,0]
	v_pk_fma_f32 v[242:243], v[178:179], v[32:33], 0 op_sel_hi:[1,1,0]
	v_pk_fma_f32 v[246:247], v[178:179], v[64:65], 0 op_sel_hi:[1,1,0]
	v_pk_fma_f32 v[238:239], v[176:177], v[2:3], v[238:239]
	v_pk_fma_f32 v[240:241], v[176:177], v[18:19], v[240:241]
	v_pk_fma_f32 v[242:243], v[176:177], v[34:35], v[242:243]
	v_pk_fma_f32 v[246:247], v[176:177], v[66:67], v[246:247]
	v_pk_fma_f32 v[238:239], v[182:183], v[4:5], v[238:239]
	v_pk_fma_f32 v[240:241], v[182:183], v[20:21], v[240:241]
	v_pk_fma_f32 v[242:243], v[182:183], v[36:37], v[242:243]
	v_pk_fma_f32 v[246:247], v[182:183], v[68:69], v[246:247]
	v_pk_fma_f32 v[238:239], v[180:181], v[6:7], v[238:239]
	v_pk_fma_f32 v[240:241], v[180:181], v[22:23], v[240:241]
	v_pk_fma_f32 v[242:243], v[180:181], v[38:39], v[242:243]
	v_pk_fma_f32 v[246:247], v[180:181], v[70:71], v[246:247]
	v_pk_fma_f32 v[238:239], v[186:187], v[8:9], v[238:239]
	v_pk_fma_f32 v[240:241], v[186:187], v[24:25], v[240:241]
	v_pk_fma_f32 v[242:243], v[186:187], v[40:41], v[242:243]
	v_pk_fma_f32 v[246:247], v[186:187], v[72:73], v[246:247]
	v_pk_fma_f32 v[238:239], v[184:185], v[10:11], v[238:239]
	v_pk_fma_f32 v[240:241], v[184:185], v[26:27], v[240:241]
	v_pk_fma_f32 v[242:243], v[184:185], v[42:43], v[242:243]
	v_pk_fma_f32 v[246:247], v[184:185], v[74:75], v[246:247]
	v_pk_fma_f32 v[238:239], v[190:191], v[12:13], v[238:239]
	v_pk_fma_f32 v[240:241], v[190:191], v[28:29], v[240:241]
	v_pk_fma_f32 v[242:243], v[190:191], v[44:45], v[242:243]
	v_pk_fma_f32 v[244:245], v[178:179], v[48:49], 0 op_sel_hi:[1,1,0]
	v_pk_fma_f32 v[246:247], v[190:191], v[76:77], v[246:247]
	v_pk_fma_f32 v[248:249], v[178:179], v[80:81], 0 op_sel_hi:[1,1,0]
	v_pk_fma_f32 v[250:251], v[178:179], v[96:97], 0 op_sel_hi:[1,1,0]
	v_pk_fma_f32 v[252:253], v[178:179], v[112:113], 0 op_sel_hi:[1,1,0]
	v_pk_fma_f32 v[238:239], v[188:189], v[14:15], v[238:239]
	v_pk_fma_f32 v[240:241], v[188:189], v[30:31], v[240:241]
	v_pk_fma_f32 v[242:243], v[188:189], v[46:47], v[242:243]
	v_pk_fma_f32 v[244:245], v[176:177], v[50:51], v[244:245]
	v_pk_fma_f32 v[246:247], v[188:189], v[78:79], v[246:247]
	v_pk_fma_f32 v[248:249], v[176:177], v[82:83], v[248:249]
	v_pk_fma_f32 v[250:251], v[176:177], v[98:99], v[250:251]
	v_pk_fma_f32 v[252:253], v[176:177], v[114:115], v[252:253]
	v_pk_fma_f32 v[244:245], v[182:183], v[52:53], v[244:245]
	v_pk_fma_f32 v[248:249], v[182:183], v[84:85], v[248:249]
	v_pk_fma_f32 v[250:251], v[182:183], v[100:101], v[250:251]
	v_pk_fma_f32 v[252:253], v[182:183], v[116:117], v[252:253]
	v_add_f32_e32 v238, v238, v239
	v_add_f32_e32 v239, v240, v241
	v_add_f32_e32 v240, v242, v243
	v_add_f32_e32 v242, v246, v247
	v_pk_fma_f32 v[244:245], v[180:181], v[54:55], v[244:245]
	v_pk_fma_f32 v[248:249], v[180:181], v[86:87], v[248:249]
	v_pk_fma_f32 v[250:251], v[180:181], v[102:103], v[250:251]
	v_pk_fma_f32 v[252:253], v[180:181], v[118:119], v[252:253]
	v_cndmask_b32_e64 v243, v238, v242, s[2:3]
	v_pk_fma_f32 v[244:245], v[186:187], v[56:57], v[244:245]
	v_pk_fma_f32 v[248:249], v[186:187], v[88:89], v[248:249]
	v_pk_fma_f32 v[250:251], v[186:187], v[104:105], v[250:251]
	v_pk_fma_f32 v[252:253], v[186:187], v[120:121], v[252:253]
	ds_bpermute_b32 v243, v220, v243
	v_pk_fma_f32 v[244:245], v[184:185], v[58:59], v[244:245]
	v_pk_fma_f32 v[248:249], v[184:185], v[90:91], v[248:249]
	v_pk_fma_f32 v[250:251], v[184:185], v[106:107], v[250:251]
	v_pk_fma_f32 v[252:253], v[184:185], v[122:123], v[252:253]
	v_pk_fma_f32 v[244:245], v[190:191], v[60:61], v[244:245]
	v_pk_fma_f32 v[248:249], v[190:191], v[92:93], v[248:249]
	v_pk_fma_f32 v[250:251], v[190:191], v[108:109], v[250:251]
	v_pk_fma_f32 v[252:253], v[190:191], v[124:125], v[252:253]
	v_pk_fma_f32 v[244:245], v[188:189], v[62:63], v[244:245]
	v_pk_fma_f32 v[248:249], v[188:189], v[94:95], v[248:249]
	v_pk_fma_f32 v[250:251], v[188:189], v[110:111], v[250:251]
	v_pk_fma_f32 v[252:253], v[188:189], v[126:127], v[252:253]
	v_add_f32_e32 v241, v244, v245
	v_add_f32_e32 v244, v248, v249
	v_add_f32_e32 v245, v250, v251
	v_add_f32_e32 v246, v252, v253
	v_cndmask_b32_e64 v238, v242, v238, s[2:3]
	s_waitcnt lgkmcnt(0)
	v_add_f32_e32 v238, v238, v243
	v_cndmask_b32_e64 v242, v239, v244, s[2:3]
	v_cndmask_b32_e64 v239, v244, v239, s[2:3]
	v_cndmask_b32_e64 v243, v240, v245, s[2:3]
	v_cndmask_b32_e64 v244, v241, v246, s[2:3]
	ds_bpermute_b32 v242, v220, v242
	ds_bpermute_b32 v243, v220, v243
	ds_bpermute_b32 v244, v220, v244
	v_cndmask_b32_e64 v240, v245, v240, s[2:3]
	v_cndmask_b32_e64 v241, v246, v241, s[2:3]
	s_waitcnt lgkmcnt(2)
	v_add_f32_e32 v239, v239, v242
	s_waitcnt lgkmcnt(1)
	v_add_f32_e32 v240, v240, v243
	s_waitcnt lgkmcnt(0)
	v_add_f32_e32 v241, v241, v244
	v_cndmask_b32_e64 v242, v238, v240, s[4:5]
	v_cndmask_b32_e64 v243, v239, v241, s[4:5]
	ds_bpermute_b32 v242, v219, v242
	ds_bpermute_b32 v243, v219, v243
	v_cndmask_b32_e64 v238, v240, v238, s[4:5]
	v_cndmask_b32_e64 v239, v241, v239, s[4:5]
	s_waitcnt lgkmcnt(1)
	v_add_f32_e32 v238, v238, v242
	s_waitcnt lgkmcnt(0)
	v_add_f32_e32 v239, v239, v243
	v_cndmask_b32_e64 v240, v238, v239, s[6:7]
	s_nop 1
	v_mov_b32_dpp v240, v240 row_ror:8 row_mask:0xf bank_mask:0xf
	v_cndmask_b32_e64 v238, v239, v238, s[6:7]
	s_waitcnt lgkmcnt(0)
	v_add_f32_e32 v238, v238, v240
	s_nop 1
	v_mov_b32_dpp v239, v238 quad_perm:[3,2,1,0] row_mask:0xf bank_mask:0xf
	s_nop 1
	v_mov_b32_dpp v239, v239 row_half_mirror row_mask:0xf bank_mask:0xf
	s_waitcnt lgkmcnt(0)
	v_add_f32_e32 v238, v238, v239
	s_nop 1
	v_mov_b32_dpp v239, v238 quad_perm:[2,3,0,1] row_mask:0xf bank_mask:0xf
	s_waitcnt lgkmcnt(0)
	v_add_f32_e32 v238, v238, v239
	s_nop 1
	v_mov_b32_dpp v239, v238 quad_perm:[1,0,3,2] row_mask:0xf bank_mask:0xf
	s_and_saveexec_b64 s[14:15], s[8:9]
	s_cbranch_execz .LBB0_510
	global_load_dword v240, v[208:209], off
	s_waitcnt lgkmcnt(0)
	v_add_f32_e32 v238, v238, v239
	v_add_u32_e32 v241, 0x20100, v237
	s_waitcnt vmcnt(0)
	v_add_f32_e32 v238, v238, v240
	ds_write_b32 v241, v238
.LBB0_510:
	s_or_b64 exec, exec, s[14:15]
	v_pk_fma_f32 v[0:1], v[194:195], v[0:1], 0 op_sel_hi:[1,1,0]
	s_nop 0
	v_pk_fma_f32 v[0:1], v[192:193], v[2:3], v[0:1]
	v_pk_fma_f32 v[2:3], v[194:195], v[16:17], 0 op_sel_hi:[1,1,0]
	v_pk_fma_f32 v[0:1], v[198:199], v[4:5], v[0:1]
	v_pk_fma_f32 v[4:5], v[194:195], v[32:33], 0 op_sel_hi:[1,1,0]
	v_pk_fma_f32 v[0:1], v[196:197], v[6:7], v[0:1]
	v_pk_fma_f32 v[2:3], v[192:193], v[18:19], v[2:3]
	v_pk_fma_f32 v[0:1], v[202:203], v[8:9], v[0:1]
	v_pk_fma_f32 v[8:9], v[194:195], v[64:65], 0 op_sel_hi:[1,1,0]
	v_pk_fma_f32 v[4:5], v[192:193], v[34:35], v[4:5]
	v_pk_fma_f32 v[8:9], v[192:193], v[66:67], v[8:9]
	v_pk_fma_f32 v[2:3], v[198:199], v[20:21], v[2:3]
	v_pk_fma_f32 v[4:5], v[198:199], v[36:37], v[4:5]
	v_pk_fma_f32 v[8:9], v[198:199], v[68:69], v[8:9]
	v_pk_fma_f32 v[2:3], v[196:197], v[22:23], v[2:3]
	v_pk_fma_f32 v[4:5], v[196:197], v[38:39], v[4:5]
	v_pk_fma_f32 v[8:9], v[196:197], v[70:71], v[8:9]
	v_pk_fma_f32 v[0:1], v[200:201], v[10:11], v[0:1]
	v_pk_fma_f32 v[2:3], v[202:203], v[24:25], v[2:3]
	v_pk_fma_f32 v[4:5], v[202:203], v[40:41], v[4:5]
	v_pk_fma_f32 v[8:9], v[202:203], v[72:73], v[8:9]
	v_pk_fma_f32 v[0:1], v[206:207], v[12:13], v[0:1]
	v_pk_fma_f32 v[2:3], v[200:201], v[26:27], v[2:3]
	v_pk_fma_f32 v[4:5], v[200:201], v[42:43], v[4:5]
	v_pk_fma_f32 v[8:9], v[200:201], v[74:75], v[8:9]
	v_pk_fma_f32 v[0:1], v[204:205], v[14:15], v[0:1]
	v_pk_fma_f32 v[2:3], v[206:207], v[28:29], v[2:3]
	v_pk_fma_f32 v[4:5], v[206:207], v[44:45], v[4:5]
	v_pk_fma_f32 v[6:7], v[194:195], v[48:49], 0 op_sel_hi:[1,1,0]
	v_pk_fma_f32 v[8:9], v[206:207], v[76:77], v[8:9]
	v_pk_fma_f32 v[10:11], v[194:195], v[80:81], 0 op_sel_hi:[1,1,0]
	v_pk_fma_f32 v[12:13], v[194:195], v[96:97], 0 op_sel_hi:[1,1,0]
	v_pk_fma_f32 v[14:15], v[194:195], v[112:113], 0 op_sel_hi:[1,1,0]
	v_pk_fma_f32 v[2:3], v[204:205], v[30:31], v[2:3]
	v_pk_fma_f32 v[4:5], v[204:205], v[46:47], v[4:5]
	v_pk_fma_f32 v[6:7], v[192:193], v[50:51], v[6:7]
	v_pk_fma_f32 v[8:9], v[204:205], v[78:79], v[8:9]
	v_pk_fma_f32 v[10:11], v[192:193], v[82:83], v[10:11]
	v_pk_fma_f32 v[12:13], v[192:193], v[98:99], v[12:13]
	v_pk_fma_f32 v[14:15], v[192:193], v[114:115], v[14:15]
	v_pk_fma_f32 v[6:7], v[198:199], v[52:53], v[6:7]
	v_pk_fma_f32 v[10:11], v[198:199], v[84:85], v[10:11]
	v_pk_fma_f32 v[12:13], v[198:199], v[100:101], v[12:13]
	v_pk_fma_f32 v[14:15], v[198:199], v[116:117], v[14:15]
	v_add_f32_e32 v0, v0, v1
	v_add_f32_e32 v1, v2, v3
	v_add_f32_e32 v2, v4, v5
	v_add_f32_e32 v4, v8, v9
	v_pk_fma_f32 v[6:7], v[196:197], v[54:55], v[6:7]
	v_pk_fma_f32 v[10:11], v[196:197], v[86:87], v[10:11]
	v_pk_fma_f32 v[12:13], v[196:197], v[102:103], v[12:13]
	v_pk_fma_f32 v[14:15], v[196:197], v[118:119], v[14:15]
	v_cndmask_b32_e64 v5, v0, v4, s[2:3]
	v_pk_fma_f32 v[6:7], v[202:203], v[56:57], v[6:7]
	v_pk_fma_f32 v[10:11], v[202:203], v[88:89], v[10:11]
	v_pk_fma_f32 v[12:13], v[202:203], v[104:105], v[12:13]
	v_pk_fma_f32 v[14:15], v[202:203], v[120:121], v[14:15]
	ds_bpermute_b32 v5, v220, v5
	v_pk_fma_f32 v[6:7], v[200:201], v[58:59], v[6:7]
	v_pk_fma_f32 v[10:11], v[200:201], v[90:91], v[10:11]
	v_pk_fma_f32 v[12:13], v[200:201], v[106:107], v[12:13]
	v_pk_fma_f32 v[14:15], v[200:201], v[122:123], v[14:15]
	v_pk_fma_f32 v[6:7], v[206:207], v[60:61], v[6:7]
	v_pk_fma_f32 v[10:11], v[206:207], v[92:93], v[10:11]
	v_pk_fma_f32 v[12:13], v[206:207], v[108:109], v[12:13]
	v_pk_fma_f32 v[14:15], v[206:207], v[124:125], v[14:15]
	v_pk_fma_f32 v[6:7], v[204:205], v[62:63], v[6:7]
	v_pk_fma_f32 v[10:11], v[204:205], v[94:95], v[10:11]
	v_pk_fma_f32 v[12:13], v[204:205], v[110:111], v[12:13]
	v_pk_fma_f32 v[14:15], v[204:205], v[126:127], v[14:15]
	v_add_f32_e32 v3, v6, v7
	v_add_f32_e32 v6, v10, v11
	v_add_f32_e32 v7, v12, v13
	v_add_f32_e32 v8, v14, v15
	v_cndmask_b32_e64 v0, v4, v0, s[2:3]
	s_waitcnt lgkmcnt(0)
	v_add_f32_e32 v0, v0, v5
	v_cndmask_b32_e64 v4, v1, v6, s[2:3]
	v_cndmask_b32_e64 v1, v6, v1, s[2:3]
	v_cndmask_b32_e64 v5, v2, v7, s[2:3]
	v_cndmask_b32_e64 v6, v3, v8, s[2:3]
	ds_bpermute_b32 v4, v220, v4
	ds_bpermute_b32 v5, v220, v5
	ds_bpermute_b32 v6, v220, v6
	v_cndmask_b32_e64 v2, v7, v2, s[2:3]
	v_cndmask_b32_e64 v3, v8, v3, s[2:3]
	s_waitcnt lgkmcnt(2)
	v_add_f32_e32 v1, v1, v4
	s_waitcnt lgkmcnt(1)
	v_add_f32_e32 v2, v2, v5
	s_waitcnt lgkmcnt(0)
	v_add_f32_e32 v3, v3, v6
	v_cndmask_b32_e64 v4, v0, v2, s[4:5]
	v_cndmask_b32_e64 v5, v1, v3, s[4:5]
	ds_bpermute_b32 v4, v219, v4
	ds_bpermute_b32 v5, v219, v5
	v_cndmask_b32_e64 v0, v2, v0, s[4:5]
	v_cndmask_b32_e64 v1, v3, v1, s[4:5]
	s_waitcnt lgkmcnt(1)
	v_add_f32_e32 v0, v0, v4
	s_waitcnt lgkmcnt(0)
	v_add_f32_e32 v1, v1, v5
	v_cndmask_b32_e64 v2, v0, v1, s[6:7]
	s_nop 1
	v_mov_b32_dpp v2, v2 row_ror:8 row_mask:0xf bank_mask:0xf
	v_cndmask_b32_e64 v0, v1, v0, s[6:7]
	s_waitcnt lgkmcnt(0)
	v_add_f32_e32 v0, v0, v2
	s_nop 1
	v_mov_b32_dpp v1, v0 quad_perm:[3,2,1,0] row_mask:0xf bank_mask:0xf
	s_nop 1
	v_mov_b32_dpp v1, v1 row_half_mirror row_mask:0xf bank_mask:0xf
	s_waitcnt lgkmcnt(0)
	v_add_f32_e32 v0, v0, v1
	s_nop 1
	v_mov_b32_dpp v1, v0 quad_perm:[2,3,0,1] row_mask:0xf bank_mask:0xf
	s_waitcnt lgkmcnt(0)
	v_add_f32_e32 v0, v0, v1
	s_nop 1
	v_mov_b32_dpp v1, v0 quad_perm:[1,0,3,2] row_mask:0xf bank_mask:0xf
	s_and_saveexec_b64 s[14:15], s[8:9]
	s_cbranch_execz .LBB0_503
	global_load_dword v2, v[208:209], off
	s_waitcnt lgkmcnt(0)
	v_add_f32_e32 v0, v0, v1
	v_add_u32_e32 v3, 0x20180, v237
	s_waitcnt vmcnt(0)
	v_add_f32_e32 v0, v0, v2
	ds_write_b32 v3, v0
	s_branch .LBB0_503
.LBB0_512:
	s_waitcnt lgkmcnt(0)
	ds_read2_b32 v[4:5], v212 offset1:16
	s_waitcnt lgkmcnt(0)
	v_cmp_gt_f32_e32 vcc, v5, v4
	s_nop 1
	v_cndmask_b32_e32 v0, v4, v5, vcc
	v_cndmask_b32_e32 v2, v211, v213, vcc
	s_nop 1
	v_mov_b32_dpp v1, v0 quad_perm:[1,0,3,2] row_mask:0xf bank_mask:0xf
	s_nop 1
	v_mov_b32_dpp v3, v2 quad_perm:[1,0,3,2] row_mask:0xf bank_mask:0xf
	s_waitcnt lgkmcnt(0)
	v_cmp_eq_f32_e64 s[12:13], v0, v1
	s_waitcnt lgkmcnt(0)
	v_cmp_lt_i32_e64 s[14:15], v3, v2
	v_cmp_lt_f32_e32 vcc, v0, v1
	s_and_b64 s[12:13], s[12:13], s[14:15]
	s_or_b64 vcc, vcc, s[12:13]
	v_cndmask_b32_e32 v0, v0, v1, vcc
	v_cndmask_b32_e32 v2, v2, v3, vcc
	s_nop 1
	v_mov_b32_dpp v1, v0 quad_perm:[2,3,0,1] row_mask:0xf bank_mask:0xf
	s_nop 1
	v_mov_b32_dpp v3, v2 quad_perm:[2,3,0,1] row_mask:0xf bank_mask:0xf
	s_waitcnt lgkmcnt(0)
	v_cmp_eq_f32_e64 s[12:13], v0, v1
	s_waitcnt lgkmcnt(0)
	v_cmp_lt_i32_e64 s[14:15], v3, v2
	v_cmp_lt_f32_e32 vcc, v0, v1
	s_and_b64 s[12:13], s[12:13], s[14:15]
	s_or_b64 vcc, vcc, s[12:13]
	v_cndmask_b32_e32 v0, v0, v1, vcc
	v_cndmask_b32_e32 v3, v2, v3, vcc
	s_nop 1
	v_mov_b32_dpp v1, v0 quad_perm:[3,2,1,0] row_mask:0xf bank_mask:0xf
	s_nop 1
	v_mov_b32_dpp v1, v1 row_half_mirror row_mask:0xf bank_mask:0xf
	s_nop 1
	v_mov_b32_dpp v6, v3 quad_perm:[3,2,1,0] row_mask:0xf bank_mask:0xf
	s_nop 1
	v_mov_b32_dpp v6, v6 row_half_mirror row_mask:0xf bank_mask:0xf
	s_waitcnt lgkmcnt(0)
	v_cmp_eq_f32_e64 s[12:13], v0, v1
	s_waitcnt lgkmcnt(0)
	v_cmp_lt_i32_e64 s[14:15], v6, v3
	v_cmp_lt_f32_e32 vcc, v0, v1
	s_and_b64 s[12:13], s[12:13], s[14:15]
	s_or_b64 vcc, vcc, s[12:13]
	v_cndmask_b32_e32 v1, v0, v1, vcc
	v_cndmask_b32_e32 v0, v3, v6, vcc
	s_nop 1
	v_mov_b32_dpp v2, v1 row_ror:8 row_mask:0xf bank_mask:0xf
	s_nop 1
	v_mov_b32_dpp v3, v0 row_ror:8 row_mask:0xf bank_mask:0xf
	s_waitcnt lgkmcnt(0)
	v_cmp_eq_f32_e64 s[12:13], v1, v2
	s_waitcnt lgkmcnt(0)
	v_cmp_lt_i32_e64 s[14:15], v3, v0
	v_cmp_lt_f32_e32 vcc, v1, v2
	s_and_b64 s[12:13], s[12:13], s[14:15]
	s_or_b64 vcc, vcc, s[12:13]
	v_cndmask_b32_e32 v0, v0, v3, vcc
	v_cmp_ne_u32_e64 s[12:13], v0, v211
	s_nop 1
	v_cndmask_b32_e64 v6, v233, v4, s[12:13]
	v_cmp_ne_u32_e64 s[12:13], v0, v213
	s_nop 1
	v_cndmask_b32_e64 v7, v233, v5, s[12:13]
	v_cmp_gt_f32_e64 s[12:13], v7, v6
	s_nop 1
	v_cndmask_b32_e64 v3, v6, v7, s[12:13]
	v_cndmask_b32_e64 v5, v211, v213, s[12:13]
	s_nop 1
	v_mov_b32_dpp v4, v3 quad_perm:[1,0,3,2] row_mask:0xf bank_mask:0xf
	s_nop 1
	v_mov_b32_dpp v8, v5 quad_perm:[1,0,3,2] row_mask:0xf bank_mask:0xf
	s_waitcnt lgkmcnt(0)
	v_cmp_eq_f32_e64 s[14:15], v3, v4
	s_waitcnt lgkmcnt(0)
	v_cmp_lt_i32_e64 s[16:17], v8, v5
	v_cmp_lt_f32_e64 s[12:13], v3, v4
	s_and_b64 s[14:15], s[14:15], s[16:17]
	s_or_b64 s[12:13], s[12:13], s[14:15]
	v_cndmask_b32_e64 v3, v3, v4, s[12:13]
	v_cndmask_b32_e64 v5, v5, v8, s[12:13]
	s_nop 1
	v_mov_b32_dpp v4, v3 quad_perm:[2,3,0,1] row_mask:0xf bank_mask:0xf
	s_nop 1
	v_mov_b32_dpp v8, v5 quad_perm:[2,3,0,1] row_mask:0xf bank_mask:0xf
	s_waitcnt lgkmcnt(0)
	v_cmp_eq_f32_e64 s[14:15], v3, v4
	s_waitcnt lgkmcnt(0)
	v_cmp_lt_i32_e64 s[16:17], v8, v5
	v_cmp_lt_f32_e64 s[12:13], v3, v4
	s_and_b64 s[14:15], s[14:15], s[16:17]
	s_or_b64 s[12:13], s[12:13], s[14:15]
	v_cndmask_b32_e64 v3, v3, v4, s[12:13]
	v_cndmask_b32_e64 v8, v5, v8, s[12:13]
	s_nop 1
	v_mov_b32_dpp v4, v3 quad_perm:[3,2,1,0] row_mask:0xf bank_mask:0xf
	s_nop 1
	v_mov_b32_dpp v4, v4 row_half_mirror row_mask:0xf bank_mask:0xf
	s_nop 1
	v_mov_b32_dpp v9, v8 quad_perm:[3,2,1,0] row_mask:0xf bank_mask:0xf
	s_nop 1
	v_mov_b32_dpp v9, v9 row_half_mirror row_mask:0xf bank_mask:0xf
	s_waitcnt lgkmcnt(0)
	v_cmp_eq_f32_e64 s[14:15], v3, v4
	s_waitcnt lgkmcnt(0)
	v_cmp_lt_i32_e64 s[16:17], v9, v8
	v_cmp_lt_f32_e64 s[12:13], v3, v4
	s_and_b64 s[14:15], s[14:15], s[16:17]
	s_or_b64 s[12:13], s[12:13], s[14:15]
	v_cndmask_b32_e64 v4, v3, v4, s[12:13]
	v_cndmask_b32_e64 v3, v8, v9, s[12:13]
	s_nop 1
	v_mov_b32_dpp v5, v4 row_ror:8 row_mask:0xf bank_mask:0xf
	s_nop 1
	v_mov_b32_dpp v8, v3 row_ror:8 row_mask:0xf bank_mask:0xf
	s_waitcnt lgkmcnt(0)
	v_cmp_eq_f32_e64 s[14:15], v4, v5
	s_waitcnt lgkmcnt(0)
	v_cmp_lt_i32_e64 s[16:17], v8, v3
	v_cmp_lt_f32_e64 s[12:13], v4, v5
	s_and_b64 s[14:15], s[14:15], s[16:17]
	s_or_b64 s[12:13], s[12:13], s[14:15]
	v_cndmask_b32_e64 v3, v3, v8, s[12:13]
	v_cmp_ne_u32_e64 s[14:15], v3, v211
	s_nop 1
	v_cndmask_b32_e64 v9, v233, v6, s[14:15]
	v_cmp_ne_u32_e64 s[14:15], v3, v213
	s_nop 1
	v_cndmask_b32_e64 v10, v233, v7, s[14:15]
	v_cmp_gt_f32_e64 s[14:15], v10, v9
	s_nop 1
	v_cndmask_b32_e64 v6, v9, v10, s[14:15]
	v_cndmask_b32_e64 v8, v211, v213, s[14:15]
	s_nop 1
	v_mov_b32_dpp v7, v6 quad_perm:[1,0,3,2] row_mask:0xf bank_mask:0xf
	s_nop 1
	v_mov_b32_dpp v11, v8 quad_perm:[1,0,3,2] row_mask:0xf bank_mask:0xf
	s_waitcnt lgkmcnt(0)
	v_cmp_eq_f32_e64 s[16:17], v6, v7
	s_waitcnt lgkmcnt(0)
	v_cmp_lt_i32_e64 s[18:19], v11, v8
	v_cmp_lt_f32_e64 s[14:15], v6, v7
	s_and_b64 s[16:17], s[16:17], s[18:19]
	s_or_b64 s[14:15], s[14:15], s[16:17]
	v_cndmask_b32_e64 v6, v6, v7, s[14:15]
	v_cndmask_b32_e64 v8, v8, v11, s[14:15]
	s_nop 1
	v_mov_b32_dpp v7, v6 quad_perm:[2,3,0,1] row_mask:0xf bank_mask:0xf
	s_nop 1
	v_mov_b32_dpp v11, v8 quad_perm:[2,3,0,1] row_mask:0xf bank_mask:0xf
	s_waitcnt lgkmcnt(0)
	v_cmp_eq_f32_e64 s[16:17], v6, v7
	s_waitcnt lgkmcnt(0)
	v_cmp_lt_i32_e64 s[18:19], v11, v8
	v_cmp_lt_f32_e64 s[14:15], v6, v7
	s_and_b64 s[16:17], s[16:17], s[18:19]
	s_or_b64 s[14:15], s[14:15], s[16:17]
	v_cndmask_b32_e64 v6, v6, v7, s[14:15]
	v_cndmask_b32_e64 v11, v8, v11, s[14:15]
	s_nop 1
	v_mov_b32_dpp v7, v6 quad_perm:[3,2,1,0] row_mask:0xf bank_mask:0xf
	s_nop 1
	v_mov_b32_dpp v7, v7 row_half_mirror row_mask:0xf bank_mask:0xf
	s_nop 1
	v_mov_b32_dpp v12, v11 quad_perm:[3,2,1,0] row_mask:0xf bank_mask:0xf
	s_nop 1
	v_mov_b32_dpp v12, v12 row_half_mirror row_mask:0xf bank_mask:0xf
	s_waitcnt lgkmcnt(0)
	v_cmp_eq_f32_e64 s[16:17], v6, v7
	s_waitcnt lgkmcnt(0)
	v_cmp_lt_i32_e64 s[18:19], v12, v11
	v_cmp_lt_f32_e64 s[14:15], v6, v7
	s_and_b64 s[16:17], s[16:17], s[18:19]
	s_or_b64 s[14:15], s[14:15], s[16:17]
	v_cndmask_b32_e64 v7, v6, v7, s[14:15]
	v_cndmask_b32_e64 v6, v11, v12, s[14:15]
	s_nop 1
	v_mov_b32_dpp v8, v7 row_ror:8 row_mask:0xf bank_mask:0xf
	s_nop 1
	v_mov_b32_dpp v11, v6 row_ror:8 row_mask:0xf bank_mask:0xf
	s_waitcnt lgkmcnt(0)
	v_cmp_eq_f32_e64 s[16:17], v7, v8
	s_waitcnt lgkmcnt(0)
	v_cmp_lt_i32_e64 s[18:19], v11, v6
	v_cmp_lt_f32_e64 s[14:15], v7, v8
	s_and_b64 s[16:17], s[16:17], s[18:19]
	s_or_b64 s[14:15], s[14:15], s[16:17]
	v_cndmask_b32_e64 v6, v6, v11, s[14:15]
	v_cmp_ne_u32_e64 s[16:17], v6, v211
	s_nop 1
	v_cndmask_b32_e64 v9, v233, v9, s[16:17]
	v_cmp_ne_u32_e64 s[16:17], v6, v213
	s_nop 1
	v_cndmask_b32_e64 v10, v233, v10, s[16:17]
	v_cmp_gt_f32_e64 s[16:17], v10, v9
	s_nop 1
	v_cndmask_b32_e64 v9, v9, v10, s[16:17]
	v_cndmask_b32_e64 v11, v211, v213, s[16:17]
	s_nop 1
	v_mov_b32_dpp v10, v9 quad_perm:[1,0,3,2] row_mask:0xf bank_mask:0xf
	s_nop 1
	v_mov_b32_dpp v12, v11 quad_perm:[1,0,3,2] row_mask:0xf bank_mask:0xf
	s_waitcnt lgkmcnt(0)
	v_cmp_eq_f32_e64 s[18:19], v9, v10
	s_waitcnt lgkmcnt(0)
	v_cmp_lt_i32_e64 s[20:21], v12, v11
	v_cmp_lt_f32_e64 s[16:17], v9, v10
	s_and_b64 s[18:19], s[18:19], s[20:21]
	s_or_b64 s[16:17], s[16:17], s[18:19]
	v_cndmask_b32_e64 v9, v9, v10, s[16:17]
	v_cndmask_b32_e64 v11, v11, v12, s[16:17]
	s_nop 1
	v_mov_b32_dpp v10, v9 quad_perm:[2,3,0,1] row_mask:0xf bank_mask:0xf
	s_nop 1
	v_mov_b32_dpp v12, v11 quad_perm:[2,3,0,1] row_mask:0xf bank_mask:0xf
	s_waitcnt lgkmcnt(0)
	v_cmp_eq_f32_e64 s[18:19], v9, v10
	s_waitcnt lgkmcnt(0)
	v_cmp_lt_i32_e64 s[20:21], v12, v11
	v_cmp_lt_f32_e64 s[16:17], v9, v10
	s_and_b64 s[18:19], s[18:19], s[20:21]
	s_or_b64 s[16:17], s[16:17], s[18:19]
	v_cndmask_b32_e64 v9, v9, v10, s[16:17]
	v_cndmask_b32_e64 v11, v11, v12, s[16:17]
	s_nop 1
	v_mov_b32_dpp v10, v9 quad_perm:[3,2,1,0] row_mask:0xf bank_mask:0xf
	s_nop 1
	v_mov_b32_dpp v10, v10 row_half_mirror row_mask:0xf bank_mask:0xf
	s_nop 1
	v_mov_b32_dpp v12, v11 quad_perm:[3,2,1,0] row_mask:0xf bank_mask:0xf
	s_nop 1
	v_mov_b32_dpp v12, v12 row_half_mirror row_mask:0xf bank_mask:0xf
	s_waitcnt lgkmcnt(0)
	v_cmp_eq_f32_e64 s[18:19], v9, v10
	s_waitcnt lgkmcnt(0)
	v_cmp_lt_i32_e64 s[20:21], v12, v11
	v_cmp_lt_f32_e64 s[16:17], v9, v10
	s_and_b64 s[18:19], s[18:19], s[20:21]
	s_or_b64 s[16:17], s[16:17], s[18:19]
	v_cndmask_b32_e64 v9, v9, v10, s[16:17]
	v_cndmask_b32_e64 v10, v11, v12, s[16:17]
	s_nop 1
	v_mov_b32_dpp v11, v9 row_ror:8 row_mask:0xf bank_mask:0xf
	s_nop 1
	v_mov_b32_dpp v12, v10 row_ror:8 row_mask:0xf bank_mask:0xf
	s_and_saveexec_b64 s[38:39], s[30:31]
	s_cbranch_execz .LBB0_501
	s_waitcnt lgkmcnt(0)
	v_cmp_eq_f32_e64 s[18:19], v9, v11
	s_waitcnt lgkmcnt(0)
	v_cmp_lt_i32_e64 s[20:21], v12, v10
	v_cndmask_b32_e64 v4, v4, v5, s[12:13]
	v_cndmask_b32_e32 v1, v1, v2, vcc
	v_cmp_lt_f32_e64 s[16:17], v9, v11
	s_and_b64 s[18:19], s[18:19], s[20:21]
	v_sub_f32_e32 v2, v4, v1
	s_or_b64 s[16:17], s[16:17], s[18:19]
	v_cndmask_b32_e64 v7, v7, v8, s[14:15]
	v_mul_f32_e32 v2, 0x3fb8aa3b, v2
	v_cndmask_b32_e64 v12, v10, v12, s[16:17]
	v_cndmask_b32_e64 v10, v9, v11, s[16:17]
	v_exp_f32_e32 v8, v2
	v_sub_f32_e32 v2, v7, v1
	v_mul_f32_e32 v2, 0x3fb8aa3b, v2
	v_sub_f32_e32 v1, v10, v1
	v_exp_f32_e32 v9, v2
	v_mul_f32_e32 v1, 0x3fb8aa3b, v1
	v_exp_f32_e32 v1, v1
	v_add_f32_e32 v2, 1.0, v8
	v_add_f32_e32 v2, v2, v9
	v_add_f32_e32 v2, v2, v1
	v_div_scale_f32 v4, s[12:13], v2, v2, 1.0
	v_rcp_f32_e32 v5, v4
	s_nop 0
	v_fma_f32 v7, -v4, v5, 1.0
	v_fmac_f32_e32 v5, v7, v5
	v_div_scale_f32 v7, vcc, 1.0, v2, 1.0
	v_mul_f32_e32 v10, v7, v5
	v_fma_f32 v11, -v4, v10, v7
	v_fmac_f32_e32 v10, v11, v5
	v_fma_f32 v4, -v4, v10, v7
	v_div_fmas_f32 v4, v4, v5, v10
	v_div_fixup_f32 v2, v4, v2, 1.0
	v_mul_f32_e32 v5, v1, v2
	v_lshl_add_u32 v1, v0, 2, s40
	ds_add_rtn_u32 v1, v1, v232
	v_add_lshl_u32 v4, v214, s48, 4
	v_add_u32_e32 v7, s41, v4
	ds_write_b32 v7, v0
	v_add_u32_e32 v0, s42, v4
	s_waitcnt lgkmcnt(1)
	ds_write_b32 v0, v1
	v_lshl_add_u32 v7, v3, 2, s40
	v_add_lshl_u32 v10, v234, s48, 2
	ds_add_rtn_u32 v7, v7, v232
	v_ashrrev_i32_e32 v11, 31, v10
	v_lshl_add_u64 v[0:1], v[10:11], 2, s[28:29]
	v_or_b32_e32 v10, 4, v4
	v_add_u32_e32 v11, s41, v10
	ds_write_b32 v11, v3
	v_add_u32_e32 v3, s42, v10
	s_waitcnt lgkmcnt(1)
	ds_write_b32 v3, v7
	v_lshl_add_u32 v3, v6, 2, s40
	ds_add_rtn_u32 v3, v3, v232
	v_or_b32_e32 v7, 8, v4
	v_add_u32_e32 v10, s41, v7
	ds_write_b32 v10, v6
	v_add_u32_e32 v6, s42, v7
	s_waitcnt lgkmcnt(1)
	ds_write_b32 v6, v3
	v_pk_mul_f32 v[6:7], v[8:9], v[2:3] op_sel_hi:[1,0]
	v_lshl_add_u32 v3, v12, 2, s40
	ds_add_rtn_u32 v3, v3, v232
	v_or_b32_e32 v4, 12, v4
	v_add_u32_e32 v8, s41, v4
	v_add_u32_e32 v4, s42, v4
	ds_write_b32 v8, v12
	s_waitcnt lgkmcnt(1)
	ds_write_b32 v4, v3
	v_mov_b32_e32 v3, v6
	v_mov_b32_e32 v4, v7
	global_store_dwordx4 v[0:1], v[2:5], off
	s_branch .LBB0_501

.LBB0_748:
	s_add_i32 s10, s40, s50
	s_add_i32 s24, s10, 2
	s_add_i32 s20, s10, 3
	s_add_i32 s10, s18, -7
	s_ashr_i32 s25, s24, 31
	s_ashr_i32 s21, s20, 31
	s_ashr_i32 s11, s10, 31
	s_lshl_b64 s[26:27], s[24:25], 11
	s_lshl_b64 s[22:23], s[20:21], 11
	s_lshl_b64 s[10:11], s[10:11], 2
	s_add_u32 s28, s33, s10
	s_addc_u32 s29, s34, s11
	s_add_u32 s10, s35, s10
	v_lshl_add_u64 v[72:73], v[34:35], 0, s[26:27]
	global_load_dword v82, v95, s[28:29]
	global_load_dwordx2 v[74:75], v[72:73], off nt
	s_addc_u32 s11, s36, s11
	s_add_i32 s28, s18, -6
	s_ashr_i32 s29, s28, 31
	s_lshl_b64 s[28:29], s[28:29], 2
	s_add_u32 s52, s33, s28
	s_addc_u32 s53, s34, s29
	global_load_dword v105, v95, s[52:53]
	s_add_u32 s28, s35, s28
	s_addc_u32 s29, s36, s29
	s_add_i32 s52, s18, -5
	s_ashr_i32 s53, s52, 31
	s_lshl_b64 s[52:53], s[52:53], 2
	s_add_u32 s54, s33, s52
	s_addc_u32 s55, s34, s53
	global_load_dword v113, v95, s[54:55]
	s_add_u32 s52, s35, s52
	s_addc_u32 s53, s36, s53
	s_add_i32 s54, s18, -4
	s_ashr_i32 s55, s54, 31
	s_lshl_b64 s[54:55], s[54:55], 2
	s_add_u32 s56, s33, s54
	s_addc_u32 s57, s34, s55
	s_add_u32 s54, s35, s54
	s_addc_u32 s55, s36, s55
	s_add_i32 s58, s18, -3
	s_ashr_i32 s59, s58, 31
	s_waitcnt lgkmcnt(0)
	v_lshl_add_u64 v[62:63], v[34:35], 0, s[22:23]
	global_load_dwordx2 v[76:77], v[72:73], off offset:512 nt
	global_load_dwordx2 v[78:79], v[72:73], off offset:1024 nt
	global_load_dwordx2 v[80:81], v[72:73], off offset:1536 nt
	global_load_dwordx2 v[70:71], v[62:63], off nt
	global_load_dwordx2 v[68:69], v[62:63], off offset:512 nt
	global_load_dwordx2 v[66:67], v[62:63], off offset:1024 nt
	global_load_dwordx2 v[64:65], v[62:63], off offset:1536 nt
	global_load_dword v112, v95, s[10:11]
	global_load_dword v126, v95, s[28:29]
	global_load_dword v127, v95, s[52:53]
	global_load_dword v114, v95, s[56:57]
	global_load_dword v128, v95, s[54:55]
	s_lshl_b64 s[10:11], s[58:59], 2
	s_add_u32 s28, s33, s10
	s_addc_u32 s29, s34, s11
	global_load_dword v115, v95, s[28:29]
	s_add_u32 s10, s35, s10
	s_addc_u32 s11, s36, s11
	s_add_i32 s28, s18, -2
	s_ashr_i32 s29, s28, 31
	s_lshl_b64 s[28:29], s[28:29], 2
	s_add_u32 s52, s33, s28
	s_addc_u32 s53, s34, s29
	s_add_u32 s28, s35, s28
	s_addc_u32 s29, s36, s29
	s_add_i32 s54, s18, -1
	s_ashr_i32 s55, s54, 31
	s_lshl_b64 s[54:55], s[54:55], 2
	s_add_u32 s56, s33, s54
	s_addc_u32 s57, s34, s55
	global_load_dword v116, v95, s[52:53]
	global_load_dword v132, v95, s[56:57]
	s_add_u32 s52, s35, s54
	s_addc_u32 s53, s36, s55
	s_ashr_i32 s19, s18, 31
	s_lshl_b64 s[54:55], s[18:19], 2
	s_add_u32 s56, s33, s54
	s_addc_u32 s57, s34, s55
	s_add_u32 s54, s35, s54
	s_addc_u32 s55, s36, s55
	s_waitcnt vmcnt(18)
	v_lshlrev_b32_sdwa v83, v98, v82 dst_sel:DWORD dst_unused:UNUSED_PAD src0_sel:DWORD src1_sel:BYTE_3
	v_add_u32_e32 v83, s45, v83
	ds_read_b32 v83, v83
	v_and_b32_e32 v82, 0xffffff, v82
	s_waitcnt vmcnt(17)
	v_and_b32_e32 v85, 0xffff0000, v74
	v_lshlrev_b32_e32 v86, 16, v75
	v_and_b32_e32 v87, 0xffff0000, v75
	s_waitcnt vmcnt(16)
	v_lshlrev_b32_sdwa v84, v98, v105 dst_sel:DWORD dst_unused:UNUSED_PAD src0_sel:DWORD src1_sel:BYTE_3
	v_add_u32_e32 v84, s45, v84
	ds_read_b32 v106, v84
	s_waitcnt lgkmcnt(1)
	v_add_u32_e32 v82, v83, v82
	v_ashrrev_i32_e32 v83, 31, v82
	v_lshlrev_b64 v[82:83], 10, v[82:83]
	v_lshl_add_u64 v[82:83], v[36:37], 0, v[82:83]
	global_load_dword v117, v[82:83], off nt
	global_load_dword v120, v[82:83], off offset:256 nt
	global_load_dword v124, v[82:83], off offset:512 nt
	global_load_dword v104, v95, s[10:11]
	global_load_dword v103, v95, s[28:29]
	global_load_dword v102, v95, s[52:53]
	global_load_dword v133, v95, s[56:57]
	global_load_dword v101, v95, s[54:55]
	v_lshlrev_b32_e32 v84, 16, v74
	v_and_b32_e32 v74, 0xffffff, v105
	global_load_dword v105, v[82:83], off offset:768 nt
	s_waitcnt vmcnt(24)
	v_lshlrev_b32_sdwa v75, v98, v113 dst_sel:DWORD dst_unused:UNUSED_PAD src0_sel:DWORD src1_sel:BYTE_3
	v_add_u32_e32 v75, s45, v75
	s_waitcnt lgkmcnt(0)
	v_add_u32_e32 v74, v106, v74
	ds_read_b32 v118, v75
	v_ashrrev_i32_e32 v75, 31, v74
	v_lshlrev_b64 v[74:75], 10, v[74:75]
	v_lshl_add_u64 v[74:75], v[36:37], 0, v[74:75]
	global_load_dword v129, v[74:75], off nt
	global_load_dword v130, v[74:75], off offset:256 nt
	global_load_dword v131, v[74:75], off offset:512 nt
	global_load_dword v134, v[74:75], off offset:768 nt
	s_waitcnt vmcnt(27)
	v_lshlrev_b32_e32 v82, 16, v76
	v_and_b32_e32 v83, 0xffff0000, v76
	v_and_b32_e32 v76, 0xffffff, v113
	s_waitcnt vmcnt(17)
	v_lshlrev_b32_sdwa v74, v98, v114 dst_sel:DWORD dst_unused:UNUSED_PAD src0_sel:DWORD src1_sel:BYTE_3
	s_waitcnt vmcnt(15)
	v_lshlrev_b32_sdwa v113, v98, v115 dst_sel:DWORD dst_unused:UNUSED_PAD src0_sel:DWORD src1_sel:BYTE_3
	v_add_u32_e32 v74, s45, v74
	v_add_u32_e32 v113, s45, v113
	v_lshlrev_b32_e32 v106, 16, v77
	v_and_b32_e32 v107, 0xffff0000, v77
	ds_read_b32 v77, v74
	ds_read_b32 v113, v113
	s_waitcnt lgkmcnt(2)
	v_add_u32_e32 v74, v118, v76
	v_ashrrev_i32_e32 v75, 31, v74
	v_lshlrev_b64 v[74:75], 10, v[74:75]
	v_lshl_add_u64 v[74:75], v[36:37], 0, v[74:75]
	global_load_dword v135, v[74:75], off nt
	global_load_dword v136, v[74:75], off offset:256 nt
	v_and_b32_e32 v76, 0xffffff, v114
	s_waitcnt lgkmcnt(1)
	v_add_u32_e32 v76, v77, v76
	v_ashrrev_i32_e32 v77, 31, v76
	v_lshlrev_b64 v[76:77], 10, v[76:77]
	v_lshl_add_u64 v[76:77], v[36:37], 0, v[76:77]
	global_load_dword v137, v[74:75], off offset:512 nt
	global_load_dword v138, v[74:75], off offset:768 nt
	global_load_dword v139, v[76:77], off nt
	global_load_dword v140, v[76:77], off offset:256 nt
	global_load_dword v141, v[76:77], off offset:512 nt
	global_load_dword v142, v[76:77], off offset:768 nt
	s_waitcnt vmcnt(22)
	v_lshlrev_b32_sdwa v74, v98, v116 dst_sel:DWORD dst_unused:UNUSED_PAD src0_sel:DWORD src1_sel:BYTE_3
	v_and_b32_e32 v114, 0xffffff, v115
	v_add_u32_e32 v74, s45, v74
	ds_read_b32 v77, v74
	s_waitcnt lgkmcnt(1)
	v_add_u32_e32 v74, v113, v114
	s_waitcnt vmcnt(21)
	v_lshlrev_b32_sdwa v113, v98, v132 dst_sel:DWORD dst_unused:UNUSED_PAD src0_sel:DWORD src1_sel:BYTE_3
	v_mul_f32_e32 v112, 0x3d000000, v112
	v_add_u32_e32 v113, s45, v113
	v_and_b32_e32 v76, 0xffffff, v116
	v_lshlrev_b32_e32 v108, 16, v78
	v_and_b32_e32 v109, 0xffff0000, v78
	v_lshlrev_b32_e32 v78, 16, v79
	v_and_b32_e32 v79, 0xffff0000, v79
	v_lshlrev_b32_e32 v110, 16, v80
	v_and_b32_e32 v111, 0xffff0000, v80
	ds_read_b32 v143, v113
	v_lshlrev_b32_e32 v80, 16, v81
	v_and_b32_e32 v81, 0xffff0000, v81
	v_ashrrev_i32_e32 v75, 31, v74
	s_waitcnt lgkmcnt(1)
	v_add_u32_e32 v76, v77, v76
	v_lshlrev_b64 v[74:75], 10, v[74:75]
	v_ashrrev_i32_e32 v77, 31, v76
	v_lshl_add_u64 v[74:75], v[36:37], 0, v[74:75]
	v_lshlrev_b64 v[76:77], 10, v[76:77]
	v_lshl_add_u64 v[76:77], v[36:37], 0, v[76:77]
	s_lshl_b64 s[28:29], s[24:25], 10
	s_waitcnt vmcnt(18)
	v_cvt_pk_f32_fp8_e32 v[122:123], v124
	v_cvt_pk_f32_fp8_sdwa v[124:125], v124 src0_sel:WORD_1
	v_cvt_pk_f32_fp8_e32 v[114:115], v117
	v_cvt_pk_f32_fp8_e32 v[118:119], v120
	v_cvt_pk_f32_fp8_sdwa v[120:121], v120 src0_sel:WORD_1
	v_cvt_pk_f32_fp8_sdwa v[116:117], v117 src0_sel:WORD_1
	v_pk_mul_f32 v[114:115], v[112:113], v[114:115] op_sel_hi:[0,1]
	v_pk_mul_f32 v[118:119], v[112:113], v[118:119] op_sel_hi:[0,1]
	v_pk_mul_f32 v[120:121], v[112:113], v[120:121] op_sel_hi:[0,1]
	v_pk_fma_f32 v[82:83], v[12:13], v[118:119], v[82:83]
	v_pk_fma_f32 v[106:107], v[14:15], v[120:121], v[106:107]
	s_waitcnt vmcnt(12)
	v_cvt_pk_f32_fp8_sdwa v[118:119], v105 src0_sel:WORD_1
	v_cvt_pk_f32_fp8_e32 v[120:121], v105
	v_pk_mul_f32 v[116:117], v[112:113], v[116:117] op_sel_hi:[0,1]
	v_pk_fma_f32 v[84:85], v[0:1], v[114:115], v[84:85]
	v_pk_mul_f32 v[114:115], v[112:113], v[124:125] op_sel_hi:[0,1]
	v_pk_fma_f32 v[86:87], v[2:3], v[116:117], v[86:87]
	v_pk_mul_f32 v[116:117], v[112:113], v[122:123] op_sel_hi:[0,1]
	v_pk_fma_f32 v[78:79], v[26:27], v[114:115], v[78:79]
	v_pk_mul_f32 v[114:115], v[112:113], v[118:119] op_sel_hi:[0,1]
	v_pk_mul_f32 v[112:113], v[112:113], v[120:121] op_sel_hi:[0,1]
	v_pk_fma_f32 v[108:109], v[24:25], v[116:117], v[108:109]
	v_pk_fma_f32 v[110:111], v[28:29], v[112:113], v[110:111]
	s_waitcnt vmcnt(11)
	v_cvt_pk_f32_fp8_e32 v[112:113], v129
	v_cvt_pk_f32_fp8_sdwa v[116:117], v129 src0_sel:WORD_1
	s_waitcnt vmcnt(10)
	v_cvt_pk_f32_fp8_e32 v[118:119], v130
	v_cvt_pk_f32_fp8_sdwa v[120:121], v130 src0_sel:WORD_1
	v_pk_fma_f32 v[80:81], v[30:31], v[114:115], v[80:81]
	v_mul_f32_e32 v114, 0x3d000000, v126
	v_pk_mul_f32 v[112:113], v[114:115], v[112:113] op_sel_hi:[0,1]
	v_pk_mul_f32 v[116:117], v[114:115], v[116:117] op_sel_hi:[0,1]
	v_pk_fma_f32 v[86:87], v[2:3], v[116:117], v[86:87]
	v_pk_fma_f32 v[84:85], v[0:1], v[112:113], v[84:85]
	v_pk_mul_f32 v[112:113], v[114:115], v[118:119] op_sel_hi:[0,1]
	v_pk_mul_f32 v[116:117], v[114:115], v[120:121] op_sel_hi:[0,1]
	s_waitcnt vmcnt(9)
	v_cvt_pk_f32_fp8_e32 v[118:119], v131
	v_cvt_pk_f32_fp8_sdwa v[120:121], v131 src0_sel:WORD_1
	v_pk_fma_f32 v[106:107], v[14:15], v[116:117], v[106:107]
	v_pk_fma_f32 v[82:83], v[12:13], v[112:113], v[82:83]
	v_pk_mul_f32 v[112:113], v[114:115], v[118:119] op_sel_hi:[0,1]
	v_pk_mul_f32 v[116:117], v[114:115], v[120:121] op_sel_hi:[0,1]
	s_waitcnt vmcnt(8)
	v_cvt_pk_f32_fp8_e32 v[118:119], v134
	v_cvt_pk_f32_fp8_sdwa v[120:121], v134 src0_sel:WORD_1
	v_pk_fma_f32 v[108:109], v[24:25], v[112:113], v[108:109]
	v_pk_fma_f32 v[78:79], v[26:27], v[116:117], v[78:79]
	v_pk_mul_f32 v[112:113], v[114:115], v[118:119] op_sel_hi:[0,1]
	v_pk_mul_f32 v[114:115], v[114:115], v[120:121] op_sel_hi:[0,1]
	v_pk_fma_f32 v[80:81], v[30:31], v[114:115], v[80:81]
	s_waitcnt vmcnt(7)
	v_cvt_pk_f32_fp8_sdwa v[114:115], v135 src0_sel:WORD_1
	v_cvt_pk_f32_fp8_e32 v[116:117], v135
	s_waitcnt vmcnt(6)
	v_cvt_pk_f32_fp8_sdwa v[118:119], v136 src0_sel:WORD_1
	v_cvt_pk_f32_fp8_e32 v[120:121], v136
	v_pk_fma_f32 v[110:111], v[28:29], v[112:113], v[110:111]
	v_mul_f32_e32 v112, 0x3d000000, v127
	v_pk_mul_f32 v[114:115], v[112:113], v[114:115] op_sel_hi:[0,1]
	v_pk_mul_f32 v[116:117], v[112:113], v[116:117] op_sel_hi:[0,1]
	v_pk_fma_f32 v[84:85], v[0:1], v[116:117], v[84:85]
	v_pk_fma_f32 v[86:87], v[2:3], v[114:115], v[86:87]
	v_pk_mul_f32 v[114:115], v[112:113], v[118:119] op_sel_hi:[0,1]
	v_pk_mul_f32 v[116:117], v[112:113], v[120:121] op_sel_hi:[0,1]
	s_waitcnt vmcnt(5)
	v_cvt_pk_f32_fp8_sdwa v[118:119], v137 src0_sel:WORD_1
	v_cvt_pk_f32_fp8_e32 v[120:121], v137
	v_pk_fma_f32 v[82:83], v[12:13], v[116:117], v[82:83]
	v_pk_fma_f32 v[106:107], v[14:15], v[114:115], v[106:107]
	v_pk_mul_f32 v[114:115], v[112:113], v[118:119] op_sel_hi:[0,1]
	v_pk_mul_f32 v[116:117], v[112:113], v[120:121] op_sel_hi:[0,1]
	s_waitcnt vmcnt(4)
	v_cvt_pk_f32_fp8_sdwa v[118:119], v138 src0_sel:WORD_1
	v_cvt_pk_f32_fp8_e32 v[120:121], v138
	v_pk_fma_f32 v[78:79], v[26:27], v[114:115], v[78:79]
	v_pk_fma_f32 v[108:109], v[24:25], v[116:117], v[108:109]
	v_pk_mul_f32 v[114:115], v[112:113], v[118:119] op_sel_hi:[0,1]
	v_pk_mul_f32 v[112:113], v[112:113], v[120:121] op_sel_hi:[0,1]
	v_pk_fma_f32 v[110:111], v[28:29], v[112:113], v[110:111]
	s_waitcnt vmcnt(3)
	v_cvt_pk_f32_fp8_e32 v[112:113], v139
	s_waitcnt vmcnt(2)
	v_cvt_pk_f32_fp8_e32 v[118:119], v140
	v_cvt_pk_f32_fp8_sdwa v[116:117], v139 src0_sel:WORD_1
	v_pk_fma_f32 v[80:81], v[30:31], v[114:115], v[80:81]
	v_mul_f32_e32 v114, 0x3d000000, v128
	v_cvt_pk_f32_fp8_sdwa v[120:121], v140 src0_sel:WORD_1
	v_pk_mul_f32 v[112:113], v[114:115], v[112:113] op_sel_hi:[0,1]
	v_pk_fma_f32 v[84:85], v[0:1], v[112:113], v[84:85]
	v_pk_mul_f32 v[112:113], v[114:115], v[118:119] op_sel_hi:[0,1]
	s_waitcnt vmcnt(1)
	v_cvt_pk_f32_fp8_e32 v[118:119], v141
	v_pk_mul_f32 v[116:117], v[114:115], v[116:117] op_sel_hi:[0,1]
	v_pk_fma_f32 v[86:87], v[2:3], v[116:117], v[86:87]
	v_pk_mul_f32 v[116:117], v[114:115], v[120:121] op_sel_hi:[0,1]
	v_cvt_pk_f32_fp8_sdwa v[120:121], v141 src0_sel:WORD_1
	v_pk_fma_f32 v[82:83], v[12:13], v[112:113], v[82:83]
	v_pk_mul_f32 v[112:113], v[114:115], v[118:119] op_sel_hi:[0,1]
	s_waitcnt vmcnt(0)
	v_cvt_pk_f32_fp8_e32 v[118:119], v142
	v_pk_fma_f32 v[106:107], v[14:15], v[116:117], v[106:107]
	v_pk_mul_f32 v[116:117], v[114:115], v[120:121] op_sel_hi:[0,1]
	v_cvt_pk_f32_fp8_sdwa v[120:121], v142 src0_sel:WORD_1
	v_pk_fma_f32 v[108:109], v[24:25], v[112:113], v[108:109]
	v_pk_mul_f32 v[112:113], v[114:115], v[118:119] op_sel_hi:[0,1]
	v_and_b32_sdwa v105, v85, v99 dst_sel:DWORD dst_unused:UNUSED_PAD src0_sel:WORD_1 src1_sel:DWORD
	v_pk_fma_f32 v[110:111], v[28:29], v[112:113], v[110:111]
	v_and_b32_sdwa v112, v84, v99 dst_sel:DWORD dst_unused:UNUSED_PAD src0_sel:WORD_1 src1_sel:DWORD
	v_add3_u32 v85, v85, v105, s46
	v_and_b32_sdwa v105, v87, v99 dst_sel:DWORD dst_unused:UNUSED_PAD src0_sel:WORD_1 src1_sel:DWORD
	v_pk_mul_f32 v[114:115], v[114:115], v[120:121] op_sel_hi:[0,1]
	v_add3_u32 v121, v84, v112, s46
	v_and_b32_sdwa v112, v86, v99 dst_sel:DWORD dst_unused:UNUSED_PAD src0_sel:WORD_1 src1_sel:DWORD
	v_add3_u32 v87, v87, v105, s46
	v_and_b32_sdwa v105, v83, v99 dst_sel:DWORD dst_unused:UNUSED_PAD src0_sel:WORD_1 src1_sel:DWORD
	v_add3_u32 v134, v86, v112, s46
	v_and_b32_sdwa v112, v82, v99 dst_sel:DWORD dst_unused:UNUSED_PAD src0_sel:WORD_1 src1_sel:DWORD
	v_add3_u32 v83, v83, v105, s46
	v_and_b32_sdwa v105, v107, v99 dst_sel:DWORD dst_unused:UNUSED_PAD src0_sel:WORD_1 src1_sel:DWORD
	v_add3_u32 v135, v82, v112, s46
	v_and_b32_sdwa v112, v106, v99 dst_sel:DWORD dst_unused:UNUSED_PAD src0_sel:WORD_1 src1_sel:DWORD
	v_add3_u32 v105, v107, v105, s46
	v_pk_fma_f32 v[78:79], v[26:27], v[116:117], v[78:79]
	v_add3_u32 v136, v106, v112, s46
	v_and_b32_e32 v123, 0xffff0000, v105
	v_and_b32_sdwa v105, v109, v99 dst_sel:DWORD dst_unused:UNUSED_PAD src0_sel:WORD_1 src1_sel:DWORD
	v_and_b32_sdwa v106, v108, v99 dst_sel:DWORD dst_unused:UNUSED_PAD src0_sel:WORD_1 src1_sel:DWORD
	v_add3_u32 v105, v109, v105, s46
	v_add3_u32 v137, v108, v106, s46
	v_and_b32_sdwa v106, v78, v99 dst_sel:DWORD dst_unused:UNUSED_PAD src0_sel:WORD_1 src1_sel:DWORD
	v_and_b32_e32 v125, 0xffff0000, v105
	v_and_b32_sdwa v105, v79, v99 dst_sel:DWORD dst_unused:UNUSED_PAD src0_sel:WORD_1 src1_sel:DWORD
	v_add3_u32 v138, v78, v106, s46
	v_and_b32_sdwa v78, v111, v99 dst_sel:DWORD dst_unused:UNUSED_PAD src0_sel:WORD_1 src1_sel:DWORD
	v_pk_fma_f32 v[80:81], v[30:31], v[114:115], v[80:81]
	v_add3_u32 v79, v79, v105, s46
	v_add3_u32 v78, v111, v78, s46
	v_and_b32_e32 v127, 0xffff0000, v79
	v_and_b32_sdwa v79, v110, v99 dst_sel:DWORD dst_unused:UNUSED_PAD src0_sel:WORD_1 src1_sel:DWORD
	v_and_b32_e32 v129, 0xffff0000, v78
	v_and_b32_sdwa v78, v81, v99 dst_sel:DWORD dst_unused:UNUSED_PAD src0_sel:WORD_1 src1_sel:DWORD
	v_and_b32_e32 v85, 0xffff0000, v85
	v_and_b32_e32 v84, 0xffff0000, v121
	v_add3_u32 v139, v110, v79, s46
	v_and_b32_sdwa v79, v80, v99 dst_sel:DWORD dst_unused:UNUSED_PAD src0_sel:WORD_1 src1_sel:DWORD
	v_add3_u32 v78, v81, v78, s46
	v_and_b32_e32 v87, 0xffff0000, v87
	v_and_b32_e32 v86, 0xffff0000, v134
	v_add3_u32 v80, v80, v79, s46
	v_and_b32_e32 v131, 0xffff0000, v78
	v_pk_fma_f32 v[78:79], v[84:85], v[84:85], 0 op_sel_hi:[1,1,0]
	v_and_b32_e32 v83, 0xffff0000, v83
	v_and_b32_e32 v82, 0xffff0000, v135
	v_pk_fma_f32 v[78:79], v[86:87], v[86:87], v[78:79]
	v_and_b32_e32 v122, 0xffff0000, v136
	v_pk_fma_f32 v[78:79], v[82:83], v[82:83], v[78:79]
	v_and_b32_e32 v124, 0xffff0000, v137
	v_pk_fma_f32 v[78:79], v[122:123], v[122:123], v[78:79]
	v_and_b32_e32 v126, 0xffff0000, v138
	v_pk_fma_f32 v[78:79], v[124:125], v[124:125], v[78:79]
	v_and_b32_e32 v128, 0xffff0000, v139
	v_pk_fma_f32 v[78:79], v[126:127], v[126:127], v[78:79]
	v_and_b32_e32 v130, 0xffff0000, v80
	v_pk_fma_f32 v[78:79], v[128:129], v[128:129], v[78:79]
	global_load_dword v120, v[74:75], off nt
	global_load_dword v119, v[74:75], off offset:256 nt
	global_load_dword v118, v[74:75], off offset:512 nt
	global_load_dword v117, v[74:75], off offset:768 nt
	global_load_dword v116, v[76:77], off nt
	global_load_dword v115, v[76:77], off offset:256 nt
	global_load_dword v113, v[76:77], off offset:512 nt
	global_load_dword v111, v[76:77], off offset:768 nt
	v_pk_fma_f32 v[78:79], v[130:131], v[130:131], v[78:79]
	v_lshlrev_b32_sdwa v77, v98, v133 dst_sel:DWORD dst_unused:UNUSED_PAD src0_sel:DWORD src1_sel:BYTE_3
	v_add_f32_e32 v78, v78, v79
	v_add_u32_e32 v77, s45, v77
	ds_read_b32 v77, v77
	v_and_b32_e32 v74, 0xffffff, v132
	s_waitcnt lgkmcnt(0)
	v_add_u32_e32 v74, v143, v74
	s_waitcnt lgkmcnt(0)
	s_nop 1
	v_add_f32_dpp v75, v78, v78 quad_perm:[1,0,3,2] row_mask:0xf bank_mask:0xf
	v_and_b32_e32 v79, 0xffffff, v133
	s_waitcnt lgkmcnt(0)
	s_nop 1
	v_add_f32_dpp v76, v75, v75 quad_perm:[2,3,0,1] row_mask:0xf bank_mask:0xf
	v_ashrrev_i32_e32 v75, 31, v74
	v_lshlrev_b64 v[74:75], 10, v[74:75]
	v_lshl_add_u64 v[74:75], v[36:37], 0, v[74:75]
	s_waitcnt lgkmcnt(0)
	s_nop 1
	v_add_f32_dpp v78, v76, v76 row_half_mirror row_mask:0xf bank_mask:0xf
	v_add_u32_e32 v76, v77, v79
	v_ashrrev_i32_e32 v77, 31, v76
	v_lshlrev_b64 v[76:77], 10, v[76:77]
	v_lshl_add_u64 v[76:77], v[36:37], 0, v[76:77]
	s_waitcnt lgkmcnt(0)
	s_nop 1
	v_add_f32_dpp v78, v78, v78 row_mirror row_mask:0xf bank_mask:0xf
	global_load_dword v114, v[74:75], off nt
	global_load_dword v112, v[74:75], off offset:256 nt
	global_load_dword v110, v[74:75], off offset:512 nt
	global_load_dword v109, v[74:75], off offset:768 nt
	global_load_dword v108, v[76:77], off nt
	global_load_dword v107, v[76:77], off offset:256 nt
	global_load_dword v106, v[76:77], off offset:512 nt
	global_load_dword v105, v[76:77], off offset:768 nt
	v_or_b32_sdwa v74, v85, v121 dst_sel:DWORD dst_unused:UNUSED_PAD src0_sel:DWORD src1_sel:WORD_1
	v_or_b32_sdwa v75, v87, v134 dst_sel:DWORD dst_unused:UNUSED_PAD src0_sel:DWORD src1_sel:WORD_1
	global_store_dwordx2 v[72:73], v[74:75], off
	s_waitcnt lgkmcnt(0)
	v_mov_b32_e32 v76, v78
	v_mov_b32_e32 v79, v78
	s_nop 1
	v_permlane16_swap_b32_e32 v76, v79
	v_add_f32_e32 v76, v76, v79
	v_or_b32_sdwa v74, v83, v135 dst_sel:DWORD dst_unused:UNUSED_PAD src0_sel:DWORD src1_sel:WORD_1
	v_or_b32_sdwa v75, v123, v136 dst_sel:DWORD dst_unused:UNUSED_PAD src0_sel:DWORD src1_sel:WORD_1
	global_store_dwordx2 v[72:73], v[74:75], off offset:512
	s_waitcnt lgkmcnt(0)
	v_mov_b32_e32 v74, v76
	v_mov_b32_e32 v77, v76
	s_nop 1
	v_permlane32_swap_b32_e32 v74, v77
	v_add_f32_e32 v74, v74, v77
	v_fmamk_f32 v74, v74, 0x3a800000, v96
	v_mul_f32_e32 v75, 0x4f800000, v74
	v_cmp_gt_f32_e32 vcc, s47, v74
	s_nop 1
	v_cndmask_b32_e32 v76, v74, v75, vcc
	v_sqrt_f32_e32 v77, v76
	v_or_b32_sdwa v74, v125, v137 dst_sel:DWORD dst_unused:UNUSED_PAD src0_sel:DWORD src1_sel:WORD_1
	v_or_b32_sdwa v75, v127, v138 dst_sel:DWORD dst_unused:UNUSED_PAD src0_sel:DWORD src1_sel:WORD_1
	global_store_dwordx2 v[72:73], v[74:75], off offset:1024
	v_add_u32_e32 v74, -1, v77
	v_fma_f32 v75, -v74, v77, v76
	v_cmp_ge_f32_e64 s[10:11], 0, v75
	v_add_u32_e32 v75, 1, v77
	s_nop 0
	v_cndmask_b32_e64 v74, v77, v74, s[10:11]
	v_fma_f32 v77, -v75, v77, v76
	v_cmp_lt_f32_e64 s[10:11], 0, v77
	s_nop 1
	v_cndmask_b32_e64 v74, v74, v75, s[10:11]
	v_mul_f32_e32 v75, 0x37800000, v74
	v_cndmask_b32_e32 v74, v74, v75, vcc
	v_cmp_class_f32_e32 vcc, v76, v97
	v_or_b32_sdwa v75, v131, v80 dst_sel:DWORD dst_unused:UNUSED_PAD src0_sel:DWORD src1_sel:WORD_1
	s_nop 0
	v_cndmask_b32_e32 v76, v74, v76, vcc
	v_div_scale_f32 v77, s[10:11], v76, v76, 1.0
	v_rcp_f32_e32 v78, v77
	v_or_b32_sdwa v74, v129, v139 dst_sel:DWORD dst_unused:UNUSED_PAD src0_sel:DWORD src1_sel:WORD_1
	global_store_dwordx2 v[72:73], v[74:75], off offset:1536
	v_fma_f32 v72, -v77, v78, 1.0
	v_fmac_f32_e32 v78, v72, v78
	v_div_scale_f32 v72, vcc, 1.0, v76, 1.0
	v_mul_f32_e32 v73, v72, v78
	v_fma_f32 v74, -v77, v73, v72
	v_fmac_f32_e32 v73, v74, v78
	v_fma_f32 v72, -v77, v73, v72
	v_div_fmas_f32 v72, v72, v78, v73
	v_div_fixup_f32 v132, v72, v76, 1.0
	v_pk_mul_f32 v[74:75], v[132:133], v[84:85] op_sel_hi:[0,1]
	v_pk_fma_f32 v[74:75], v[48:49], v[74:75], v[4:5]
	v_pk_mul_f32 v[72:73], v[132:133], v[86:87] op_sel_hi:[0,1]
	v_bfe_u32 v121, v74, 16, 1
	v_pk_mul_f32 v[78:79], v[132:133], v[82:83] op_sel_hi:[0,1]
	v_pk_mul_f32 v[82:83], v[132:133], v[124:125] op_sel_hi:[0,1]
	v_add3_u32 v121, v74, v121, s46
	v_bfe_u32 v124, v75, 16, 1
	v_pk_fma_f32 v[72:73], v[46:47], v[72:73], v[6:7]
	v_lshrrev_b32_e32 v121, 16, v121
	v_add3_u32 v124, v75, v124, s46
	v_and_or_b32 v124, v124, s44, v121
	v_bfe_u32 v121, v72, 16, 1
	v_add3_u32 v121, v72, v121, s46
	v_bfe_u32 v125, v73, 16, 1
	v_pk_fma_f32 v[78:79], v[52:53], v[78:79], v[8:9]
	v_lshrrev_b32_e32 v121, 16, v121
	v_add3_u32 v125, v73, v125, s46
	v_pk_mul_f32 v[76:77], v[132:133], v[122:123] op_sel_hi:[0,1]
	v_lshl_add_u64 v[122:123], v[38:39], 0, s[26:27]
	v_and_or_b32 v125, v125, s44, v121
	v_bfe_u32 v121, v78, 16, 1
	global_store_dwordx2 v[122:123], v[124:125], off
	v_add3_u32 v121, v78, v121, s46
	v_bfe_u32 v124, v79, 16, 1
	v_pk_fma_f32 v[76:77], v[50:51], v[76:77], v[10:11]
	v_lshrrev_b32_e32 v121, 16, v121
	v_add3_u32 v124, v79, v124, s46
	v_and_or_b32 v124, v124, s44, v121
	v_bfe_u32 v121, v76, 16, 1
	v_add3_u32 v121, v76, v121, s46
	v_bfe_u32 v125, v77, 16, 1
	v_pk_fma_f32 v[82:83], v[56:57], v[82:83], v[16:17]
	v_lshrrev_b32_e32 v121, 16, v121
	v_add3_u32 v125, v77, v125, s46
	v_and_or_b32 v125, v125, s44, v121
	v_bfe_u32 v121, v82, 16, 1
	v_pk_mul_f32 v[80:81], v[132:133], v[126:127] op_sel_hi:[0,1]
	global_store_dwordx2 v[122:123], v[124:125], off offset:512
	v_add3_u32 v121, v82, v121, s46
	v_bfe_u32 v124, v83, 16, 1
	v_pk_fma_f32 v[80:81], v[54:55], v[80:81], v[18:19]
	v_lshrrev_b32_e32 v121, 16, v121
	v_add3_u32 v124, v83, v124, s46
	v_and_or_b32 v124, v124, s44, v121
	v_bfe_u32 v121, v80, 16, 1
	v_pk_mul_f32 v[86:87], v[132:133], v[128:129] op_sel_hi:[0,1]
	v_add3_u32 v121, v80, v121, s46
	v_bfe_u32 v125, v81, 16, 1
	v_pk_fma_f32 v[86:87], v[60:61], v[86:87], v[20:21]
	v_lshrrev_b32_e32 v121, 16, v121
	v_add3_u32 v125, v81, v125, s46
	v_and_or_b32 v125, v125, s44, v121
	v_bfe_u32 v121, v86, 16, 1
	v_pk_mul_f32 v[84:85], v[132:133], v[130:131] op_sel_hi:[0,1]
	global_store_dwordx2 v[122:123], v[124:125], off offset:1024
	v_add3_u32 v121, v86, v121, s46
	v_bfe_u32 v124, v87, 16, 1
	v_pk_fma_f32 v[84:85], v[58:59], v[84:85], v[22:23]
	v_lshrrev_b32_e32 v121, 16, v121
	v_add3_u32 v124, v87, v124, s46
	v_and_or_b32 v124, v124, s44, v121
	v_bfe_u32 v121, v84, 16, 1
	v_add3_u32 v121, v84, v121, s46
	v_bfe_u32 v125, v85, 16, 1
	v_mul_f32_e32 v126, 0x41000000, v74
	v_mul_f32_e32 v127, 0x41000000, v75
	v_lshrrev_b32_e32 v121, 16, v121
	v_add3_u32 v125, v85, v125, s46
	v_med3_f32 v126, v126, s48, v100
	v_med3_f32 v127, v127, s48, v100
	v_mov_b32_e32 v129, 0
	v_cvt_pk_fp8_f32 v129, v126, v127
	v_and_or_b32 v125, v125, s44, v121
	v_mul_f32_e32 v128, 0x41000000, v72
	global_store_dwordx2 v[122:123], v[124:125], off offset:1536
	v_mul_f32_e32 v121, 0x41000000, v78
	v_mul_f32_e32 v122, 0x41000000, v79
	v_mul_f32_e32 v126, 0x41000000, v73
	v_med3_f32 v127, v128, s48, v100
	v_med3_f32 v121, v121, s48, v100
	v_med3_f32 v122, v122, s48, v100
	v_mov_b32_e32 v128, 0
	v_med3_f32 v126, v126, s48, v100
	v_cvt_pk_fp8_f32 v128, v121, v122
	v_cvt_pk_fp8_f32 v129, v127, v126 op_sel:[0,0,1]
	v_mul_f32_e32 v123, 0x41000000, v76
	v_mul_f32_e32 v121, 0x41000000, v77
	v_med3_f32 v122, v123, s48, v100
	v_med3_f32 v121, v121, s48, v100
	v_lshl_add_u64 v[126:127], v[40:41], 0, s[28:29]
	v_cvt_pk_fp8_f32 v128, v122, v121 op_sel:[0,0,1]
	v_mul_f32_e32 v121, 0x41000000, v82
	v_mul_f32_e32 v122, 0x41000000, v83
	global_store_dword v[126:127], v129, off
	v_med3_f32 v121, v121, s48, v100
	v_med3_f32 v122, v122, s48, v100
	v_mov_b32_e32 v129, 0
	v_cvt_pk_fp8_f32 v129, v121, v122
	v_mul_f32_e32 v123, 0x41000000, v80
	v_mul_f32_e32 v121, 0x41000000, v81
	v_med3_f32 v122, v123, s48, v100
	v_med3_f32 v121, v121, s48, v100
	v_cvt_pk_fp8_f32 v129, v122, v121 op_sel:[0,0,1]
	v_mul_f32_e32 v121, 0x41000000, v86
	v_mul_f32_e32 v122, 0x41000000, v87
	v_med3_f32 v121, v121, s48, v100
	v_med3_f32 v122, v122, s48, v100
	v_mov_b32_e32 v130, 0
	v_cvt_pk_fp8_f32 v130, v121, v122
	v_mul_f32_e32 v123, 0x41000000, v84
	v_mul_f32_e32 v121, 0x41000000, v85
	v_med3_f32 v122, v123, s48, v100
	v_med3_f32 v121, v121, s48, v100
	v_cvt_pk_fp8_f32 v130, v122, v121 op_sel:[0,0,1]
	ds_read_b128 v[122:125], v94
	global_store_dword v[126:127], v128, off offset:256
	global_store_dword v[126:127], v129, off offset:512
	global_store_dword v[126:127], v130, off offset:768
	ds_read_b128 v[126:129], v94 offset:1024
	ds_read_b128 v[130:133], v94 offset:2048
	s_waitcnt lgkmcnt(2)
	v_pk_fma_f32 v[122:123], v[74:75], v[122:123], 0 op_sel_hi:[1,1,0]
	s_nop 0
	v_pk_fma_f32 v[134:135], v[72:73], v[124:125], v[122:123]
	ds_read_b128 v[122:125], v94 offset:3072
	s_waitcnt lgkmcnt(2)
	v_pk_fma_f32 v[126:127], v[78:79], v[126:127], v[134:135]
	s_nop 0
	v_pk_fma_f32 v[126:127], v[76:77], v[128:129], v[126:127]
	s_waitcnt lgkmcnt(1)
	v_pk_fma_f32 v[126:127], v[82:83], v[130:131], v[126:127]
	s_nop 0
	v_pk_fma_f32 v[126:127], v[80:81], v[132:133], v[126:127]
	s_waitcnt lgkmcnt(0)
	v_pk_fma_f32 v[122:123], v[86:87], v[122:123], v[126:127]
	ds_read_b128 v[126:129], v94 offset:5120
	ds_read_b128 v[130:133], v94 offset:4096
	v_pk_fma_f32 v[122:123], v[84:85], v[124:125], v[122:123]
	s_waitcnt lgkmcnt(0)
	v_pk_fma_f32 v[130:131], v[74:75], v[130:131], 0 op_sel_hi:[1,1,0]
	v_add_f32_e32 v121, v122, v123
	ds_read_b128 v[122:125], v94 offset:7168
	ds_read_b128 v[134:137], v94 offset:6144
	v_pk_fma_f32 v[130:131], v[72:73], v[132:133], v[130:131]
	s_nop 0
	v_pk_fma_f32 v[126:127], v[78:79], v[126:127], v[130:131]
	s_nop 0
	v_pk_fma_f32 v[126:127], v[76:77], v[128:129], v[126:127]
	s_waitcnt lgkmcnt(0)
	v_pk_fma_f32 v[126:127], v[82:83], v[134:135], v[126:127]
	s_nop 0
	v_pk_fma_f32 v[126:127], v[80:81], v[136:137], v[126:127]
	s_nop 0
	v_pk_fma_f32 v[122:123], v[86:87], v[122:123], v[126:127]
	s_nop 0
	v_pk_fma_f32 v[122:123], v[84:85], v[124:125], v[122:123]
	s_nop 0
	v_add_f32_e32 v138, v122, v123
	ds_read_b128 v[122:125], v94 offset:8192
	ds_read_b128 v[126:129], v94 offset:9216
	ds_read_b128 v[130:133], v94 offset:10240
	ds_read_b128 v[134:137], v94 offset:11264
	s_waitcnt lgkmcnt(3)
	v_pk_fma_f32 v[122:123], v[74:75], v[122:123], 0 op_sel_hi:[1,1,0]
	s_nop 0
	v_pk_fma_f32 v[122:123], v[72:73], v[124:125], v[122:123]
	s_waitcnt lgkmcnt(2)
	v_pk_fma_f32 v[122:123], v[78:79], v[126:127], v[122:123]
	s_nop 0
	v_pk_fma_f32 v[122:123], v[76:77], v[128:129], v[122:123]
	s_waitcnt lgkmcnt(1)
	v_pk_fma_f32 v[122:123], v[82:83], v[130:131], v[122:123]
	s_nop 0
	v_pk_fma_f32 v[122:123], v[80:81], v[132:133], v[122:123]
	s_waitcnt lgkmcnt(0)
	v_pk_fma_f32 v[130:131], v[86:87], v[134:135], v[122:123]
	ds_read_b128 v[122:125], v94 offset:13312
	ds_read_b128 v[126:129], v94 offset:12288
	v_pk_fma_f32 v[130:131], v[84:85], v[136:137], v[130:131]
	s_waitcnt lgkmcnt(0)
	v_pk_fma_f32 v[126:127], v[74:75], v[126:127], 0 op_sel_hi:[1,1,0]
	v_add_f32_e32 v139, v130, v131
	ds_read_b128 v[130:133], v94 offset:15360
	ds_read_b128 v[134:137], v94 offset:14336
	v_pk_fma_f32 v[126:127], v[72:73], v[128:129], v[126:127]
	s_nop 0
	v_pk_fma_f32 v[122:123], v[78:79], v[122:123], v[126:127]
	s_nop 0
	v_pk_fma_f32 v[122:123], v[76:77], v[124:125], v[122:123]
	s_waitcnt lgkmcnt(0)
	v_pk_fma_f32 v[122:123], v[82:83], v[134:135], v[122:123]
	s_nop 0
	v_pk_fma_f32 v[122:123], v[80:81], v[136:137], v[122:123]
	s_nop 0
	v_pk_fma_f32 v[122:123], v[86:87], v[130:131], v[122:123]
	s_nop 0
	v_pk_fma_f32 v[122:123], v[84:85], v[132:133], v[122:123]
	s_nop 0
	v_add_f32_e32 v140, v122, v123
	ds_read_b128 v[122:125], v94 offset:16384
	ds_read_b128 v[126:129], v94 offset:17408
	ds_read_b128 v[130:133], v94 offset:18432
	ds_read_b128 v[134:137], v94 offset:19456
	s_waitcnt lgkmcnt(3)
	v_pk_fma_f32 v[122:123], v[74:75], v[122:123], 0 op_sel_hi:[1,1,0]
	s_nop 0
	v_pk_fma_f32 v[122:123], v[72:73], v[124:125], v[122:123]
	s_waitcnt lgkmcnt(2)
	v_pk_fma_f32 v[122:123], v[78:79], v[126:127], v[122:123]
	s_nop 0
	v_pk_fma_f32 v[122:123], v[76:77], v[128:129], v[122:123]
	s_waitcnt lgkmcnt(1)
	v_pk_fma_f32 v[122:123], v[82:83], v[130:131], v[122:123]
	s_nop 0
	v_pk_fma_f32 v[122:123], v[80:81], v[132:133], v[122:123]
	s_waitcnt lgkmcnt(0)
	v_pk_fma_f32 v[130:131], v[86:87], v[134:135], v[122:123]
	ds_read_b128 v[122:125], v94 offset:21504
	ds_read_b128 v[126:129], v94 offset:20480
	v_pk_fma_f32 v[130:131], v[84:85], v[136:137], v[130:131]
	s_waitcnt lgkmcnt(0)
	v_pk_fma_f32 v[126:127], v[74:75], v[126:127], 0 op_sel_hi:[1,1,0]
	v_add_f32_e32 v141, v130, v131
	ds_read_b128 v[130:133], v94 offset:23552
	ds_read_b128 v[134:137], v94 offset:22528
	v_pk_fma_f32 v[126:127], v[72:73], v[128:129], v[126:127]
	s_nop 0
	v_pk_fma_f32 v[122:123], v[78:79], v[122:123], v[126:127]
	s_nop 0
	v_pk_fma_f32 v[122:123], v[76:77], v[124:125], v[122:123]
	s_waitcnt lgkmcnt(0)
	v_pk_fma_f32 v[122:123], v[82:83], v[134:135], v[122:123]
	s_nop 0
	v_pk_fma_f32 v[122:123], v[80:81], v[136:137], v[122:123]
	s_nop 0
	v_pk_fma_f32 v[122:123], v[86:87], v[130:131], v[122:123]
	s_nop 0
	v_pk_fma_f32 v[122:123], v[84:85], v[132:133], v[122:123]
	s_nop 0
	v_add_f32_e32 v142, v122, v123
	ds_read_b128 v[122:125], v94 offset:24576
	ds_read_b128 v[126:129], v94 offset:25600
	ds_read_b128 v[130:133], v94 offset:26624
	ds_read_b128 v[134:137], v94 offset:27648
	s_waitcnt lgkmcnt(3)
	v_pk_fma_f32 v[122:123], v[74:75], v[122:123], 0 op_sel_hi:[1,1,0]
	s_nop 0
	v_pk_fma_f32 v[122:123], v[72:73], v[124:125], v[122:123]
	s_waitcnt lgkmcnt(2)
	v_pk_fma_f32 v[122:123], v[78:79], v[126:127], v[122:123]
	s_nop 0
	v_pk_fma_f32 v[122:123], v[76:77], v[128:129], v[122:123]
	s_waitcnt lgkmcnt(1)
	v_pk_fma_f32 v[122:123], v[82:83], v[130:131], v[122:123]
	s_nop 0
	v_pk_fma_f32 v[122:123], v[80:81], v[132:133], v[122:123]
	s_waitcnt lgkmcnt(0)
	v_pk_fma_f32 v[130:131], v[86:87], v[134:135], v[122:123]
	ds_read_b128 v[122:125], v94 offset:29696
	ds_read_b128 v[126:129], v94 offset:28672
	v_pk_fma_f32 v[130:131], v[84:85], v[136:137], v[130:131]
	s_waitcnt lgkmcnt(0)
	v_pk_fma_f32 v[74:75], v[74:75], v[126:127], 0 op_sel_hi:[1,1,0]
	v_add_f32_e32 v143, v130, v131
	ds_read_b128 v[130:133], v94 offset:31744
	ds_read_b128 v[134:137], v94 offset:30720
	v_pk_fma_f32 v[72:73], v[72:73], v[128:129], v[74:75]
	s_nop 0
	v_pk_fma_f32 v[72:73], v[78:79], v[122:123], v[72:73]
	s_nop 0
	v_pk_fma_f32 v[72:73], v[76:77], v[124:125], v[72:73]
	s_waitcnt lgkmcnt(0)
	v_pk_fma_f32 v[72:73], v[82:83], v[134:135], v[72:73]
	s_nop 0
	v_pk_fma_f32 v[72:73], v[80:81], v[136:137], v[72:73]
	s_nop 0
	v_pk_fma_f32 v[72:73], v[86:87], v[130:131], v[72:73]
	s_nop 0
	v_pk_fma_f32 v[72:73], v[84:85], v[132:133], v[72:73]
	s_nop 0
	v_add_f32_e32 v72, v72, v73
	v_cndmask_b32_e64 v73, v121, v141, s[2:3]
	ds_bpermute_b32 v73, v93, v73
	v_cndmask_b32_e64 v74, v141, v121, s[2:3]
	v_cndmask_b32_e64 v75, v138, v142, s[2:3]
	ds_bpermute_b32 v75, v93, v75
	v_cndmask_b32_e64 v77, v140, v72, s[2:3]
	s_waitcnt lgkmcnt(1)
	v_add_f32_e32 v73, v74, v73
	v_cndmask_b32_e64 v74, v139, v143, s[2:3]
	ds_bpermute_b32 v74, v93, v74
	ds_bpermute_b32 v77, v93, v77
	v_cndmask_b32_e64 v76, v142, v138, s[2:3]
	s_waitcnt lgkmcnt(2)
	v_add_f32_e32 v75, v76, v75
	v_cndmask_b32_e64 v76, v143, v139, s[2:3]
	v_cndmask_b32_e64 v72, v72, v140, s[2:3]
	s_waitcnt lgkmcnt(1)
	v_add_f32_e32 v74, v76, v74
	s_waitcnt lgkmcnt(0)
	v_add_f32_e32 v72, v72, v77
	v_cndmask_b32_e64 v76, v73, v74, s[4:5]
	v_cndmask_b32_e64 v77, v75, v72, s[4:5]
	ds_bpermute_b32 v76, v92, v76
	ds_bpermute_b32 v77, v92, v77
	v_cndmask_b32_e64 v73, v74, v73, s[4:5]
	v_cndmask_b32_e64 v72, v72, v75, s[4:5]
	s_waitcnt lgkmcnt(1)
	v_add_f32_e32 v73, v73, v76
	s_waitcnt lgkmcnt(0)
	v_add_f32_e32 v72, v72, v77
	v_cndmask_b32_e64 v74, v73, v72, s[6:7]
	s_nop 1
	v_mov_b32_dpp v74, v74 row_ror:8 row_mask:0xf bank_mask:0xf
	v_cndmask_b32_e64 v72, v72, v73, s[6:7]
	s_waitcnt lgkmcnt(0)
	v_add_f32_e32 v72, v72, v74
	s_nop 1
	v_mov_b32_dpp v73, v72 quad_perm:[3,2,1,0] row_mask:0xf bank_mask:0xf
	s_nop 1
	v_mov_b32_dpp v73, v73 row_half_mirror row_mask:0xf bank_mask:0xf
	s_waitcnt lgkmcnt(0)
	v_add_f32_e32 v72, v72, v73
	s_nop 1
	v_mov_b32_dpp v73, v72 quad_perm:[2,3,0,1] row_mask:0xf bank_mask:0xf
	s_waitcnt lgkmcnt(0)
	v_add_f32_e32 v72, v72, v73
	s_nop 1
	v_mov_b32_dpp v73, v72 quad_perm:[1,0,3,2] row_mask:0xf bank_mask:0xf
	s_and_saveexec_b64 s[10:11], s[8:9]
	s_cbranch_execz .LBB0_750
	s_lshl_b64 s[24:25], s[24:25], 5
	v_lshl_add_u64 v[74:75], v[42:43], 0, s[24:25]
	s_waitcnt lgkmcnt(0)
	v_add_f32_e32 v72, v72, v73
	global_store_dword v[74:75], v72, off
.LBB0_750:
	s_or_b64 exec, exec, s[10:11]
	s_waitcnt vmcnt(27)
	v_cvt_pk_f32_fp8_sdwa v[80:81], v120 src0_sel:WORD_1
	s_waitcnt vmcnt(26)
	v_cvt_pk_f32_fp8_sdwa v[86:87], v119 src0_sel:WORD_1
	v_cvt_pk_f32_fp8_e32 v[82:83], v120
	v_mul_f32_e32 v84, 0x3d000000, v104
	v_lshlrev_b32_e32 v72, 16, v70
	s_waitcnt lgkmcnt(0)
	v_and_b32_e32 v73, 0xffff0000, v70
	v_lshlrev_b32_e32 v70, 16, v71
	v_and_b32_e32 v71, 0xffff0000, v71
	v_pk_mul_f32 v[80:81], v[84:85], v[80:81] op_sel_hi:[0,1]
	v_cvt_pk_f32_fp8_e32 v[120:121], v119
	v_pk_fma_f32 v[70:71], v[2:3], v[80:81], v[70:71]
	v_pk_mul_f32 v[80:81], v[84:85], v[86:87] op_sel_hi:[0,1]
	s_waitcnt vmcnt(25)
	v_cvt_pk_f32_fp8_sdwa v[86:87], v118 src0_sel:WORD_1
	v_cvt_pk_f32_fp8_e32 v[118:119], v118
	v_pk_mul_f32 v[82:83], v[84:85], v[82:83] op_sel_hi:[0,1]
	v_lshlrev_b32_e32 v74, 16, v68
	v_and_b32_e32 v75, 0xffff0000, v68
	v_pk_fma_f32 v[72:73], v[0:1], v[82:83], v[72:73]
	v_pk_mul_f32 v[82:83], v[84:85], v[120:121] op_sel_hi:[0,1]
	v_lshlrev_b32_e32 v68, 16, v69
	v_and_b32_e32 v69, 0xffff0000, v69
	v_pk_fma_f32 v[74:75], v[12:13], v[82:83], v[74:75]
	v_pk_mul_f32 v[82:83], v[84:85], v[118:119] op_sel_hi:[0,1]
	s_waitcnt vmcnt(24)
	v_cvt_pk_f32_fp8_e32 v[118:119], v117
	v_pk_fma_f32 v[68:69], v[14:15], v[80:81], v[68:69]
	v_pk_mul_f32 v[80:81], v[84:85], v[86:87] op_sel_hi:[0,1]
	v_cvt_pk_f32_fp8_sdwa v[86:87], v117 src0_sel:WORD_1
	v_lshlrev_b32_e32 v76, 16, v66
	v_and_b32_e32 v77, 0xffff0000, v66
	v_lshlrev_b32_e32 v66, 16, v67
	v_and_b32_e32 v67, 0xffff0000, v67
	v_lshlrev_b32_e32 v78, 16, v64
	v_and_b32_e32 v79, 0xffff0000, v64
	v_pk_fma_f32 v[76:77], v[24:25], v[82:83], v[76:77]
	v_pk_mul_f32 v[82:83], v[84:85], v[118:119] op_sel_hi:[0,1]
	v_pk_fma_f32 v[66:67], v[26:27], v[80:81], v[66:67]
	v_pk_mul_f32 v[80:81], v[84:85], v[86:87] op_sel_hi:[0,1]
	v_pk_fma_f32 v[78:79], v[28:29], v[82:83], v[78:79]
	s_waitcnt vmcnt(23)
	v_cvt_pk_f32_fp8_e32 v[82:83], v116
	v_cvt_pk_f32_fp8_sdwa v[84:85], v116 src0_sel:WORD_1
	s_waitcnt vmcnt(22)
	v_cvt_pk_f32_fp8_e32 v[86:87], v115
	v_cvt_pk_f32_fp8_sdwa v[116:117], v115 src0_sel:WORD_1
	v_lshlrev_b32_e32 v64, 16, v65
	v_and_b32_e32 v65, 0xffff0000, v65
	v_pk_fma_f32 v[64:65], v[30:31], v[80:81], v[64:65]
	v_mul_f32_e32 v80, 0x3d000000, v103
	v_pk_mul_f32 v[82:83], v[80:81], v[82:83] op_sel_hi:[0,1]
	v_pk_mul_f32 v[84:85], v[80:81], v[84:85] op_sel_hi:[0,1]
	v_pk_fma_f32 v[70:71], v[2:3], v[84:85], v[70:71]
	v_pk_fma_f32 v[72:73], v[0:1], v[82:83], v[72:73]
	v_pk_mul_f32 v[82:83], v[80:81], v[86:87] op_sel_hi:[0,1]
	v_pk_mul_f32 v[84:85], v[80:81], v[116:117] op_sel_hi:[0,1]
	s_waitcnt vmcnt(21)
	v_cvt_pk_f32_fp8_e32 v[86:87], v113
	v_cvt_pk_f32_fp8_sdwa v[116:117], v113 src0_sel:WORD_1
	v_pk_fma_f32 v[68:69], v[14:15], v[84:85], v[68:69]
	v_pk_fma_f32 v[74:75], v[12:13], v[82:83], v[74:75]
	v_pk_mul_f32 v[82:83], v[80:81], v[86:87] op_sel_hi:[0,1]
	v_pk_mul_f32 v[84:85], v[80:81], v[116:117] op_sel_hi:[0,1]
	s_waitcnt vmcnt(20)
	v_cvt_pk_f32_fp8_e32 v[86:87], v111
	v_cvt_pk_f32_fp8_sdwa v[116:117], v111 src0_sel:WORD_1
	v_pk_fma_f32 v[76:77], v[24:25], v[82:83], v[76:77]
	v_pk_fma_f32 v[66:67], v[26:27], v[84:85], v[66:67]
	v_pk_mul_f32 v[82:83], v[80:81], v[86:87] op_sel_hi:[0,1]
	v_pk_mul_f32 v[80:81], v[80:81], v[116:117] op_sel_hi:[0,1]
	v_pk_fma_f32 v[64:65], v[30:31], v[80:81], v[64:65]
	s_waitcnt vmcnt(19)
	v_cvt_pk_f32_fp8_sdwa v[80:81], v114 src0_sel:WORD_1
	v_cvt_pk_f32_fp8_e32 v[84:85], v114
	v_pk_fma_f32 v[78:79], v[28:29], v[82:83], v[78:79]
	v_mul_f32_e32 v82, 0x3d000000, v102
	s_waitcnt vmcnt(18)
	v_cvt_pk_f32_fp8_sdwa v[86:87], v112 src0_sel:WORD_1
	v_cvt_pk_f32_fp8_e32 v[102:103], v112
	v_pk_mul_f32 v[80:81], v[82:83], v[80:81] op_sel_hi:[0,1]
	v_pk_mul_f32 v[84:85], v[82:83], v[84:85] op_sel_hi:[0,1]
	v_pk_fma_f32 v[72:73], v[0:1], v[84:85], v[72:73]
	v_pk_fma_f32 v[70:71], v[2:3], v[80:81], v[70:71]
	v_pk_mul_f32 v[80:81], v[82:83], v[86:87] op_sel_hi:[0,1]
	v_pk_mul_f32 v[84:85], v[82:83], v[102:103] op_sel_hi:[0,1]
	s_waitcnt vmcnt(17)
	v_cvt_pk_f32_fp8_sdwa v[86:87], v110 src0_sel:WORD_1
	v_cvt_pk_f32_fp8_e32 v[102:103], v110
	v_pk_fma_f32 v[74:75], v[12:13], v[84:85], v[74:75]
	v_pk_fma_f32 v[68:69], v[14:15], v[80:81], v[68:69]
	v_pk_mul_f32 v[80:81], v[82:83], v[86:87] op_sel_hi:[0,1]
	v_pk_mul_f32 v[84:85], v[82:83], v[102:103] op_sel_hi:[0,1]
	s_waitcnt vmcnt(16)
	v_cvt_pk_f32_fp8_sdwa v[86:87], v109 src0_sel:WORD_1
	v_cvt_pk_f32_fp8_e32 v[102:103], v109
	v_pk_fma_f32 v[66:67], v[26:27], v[80:81], v[66:67]
	v_pk_fma_f32 v[76:77], v[24:25], v[84:85], v[76:77]
	v_pk_mul_f32 v[80:81], v[82:83], v[86:87] op_sel_hi:[0,1]
	v_pk_mul_f32 v[82:83], v[82:83], v[102:103] op_sel_hi:[0,1]
	v_pk_fma_f32 v[78:79], v[28:29], v[82:83], v[78:79]
	s_waitcnt vmcnt(15)
	v_cvt_pk_f32_fp8_e32 v[82:83], v108
	v_cvt_pk_f32_fp8_sdwa v[84:85], v108 src0_sel:WORD_1
	s_waitcnt vmcnt(14)
	v_cvt_pk_f32_fp8_e32 v[86:87], v107
	v_cvt_pk_f32_fp8_sdwa v[102:103], v107 src0_sel:WORD_1
	v_pk_fma_f32 v[64:65], v[30:31], v[80:81], v[64:65]
	v_mul_f32_e32 v80, 0x3d000000, v101
	v_pk_mul_f32 v[82:83], v[80:81], v[82:83] op_sel_hi:[0,1]
	v_pk_mul_f32 v[84:85], v[80:81], v[84:85] op_sel_hi:[0,1]
	v_pk_fma_f32 v[70:71], v[2:3], v[84:85], v[70:71]
	v_pk_fma_f32 v[72:73], v[0:1], v[82:83], v[72:73]
	v_pk_mul_f32 v[82:83], v[80:81], v[86:87] op_sel_hi:[0,1]
	v_pk_mul_f32 v[84:85], v[80:81], v[102:103] op_sel_hi:[0,1]
	s_waitcnt vmcnt(13)
	v_cvt_pk_f32_fp8_e32 v[86:87], v106
	v_cvt_pk_f32_fp8_sdwa v[102:103], v106 src0_sel:WORD_1
	v_pk_fma_f32 v[68:69], v[14:15], v[84:85], v[68:69]
	v_pk_fma_f32 v[74:75], v[12:13], v[82:83], v[74:75]
	v_pk_mul_f32 v[82:83], v[80:81], v[86:87] op_sel_hi:[0,1]
	v_pk_mul_f32 v[84:85], v[80:81], v[102:103] op_sel_hi:[0,1]
	s_waitcnt vmcnt(12)
	v_cvt_pk_f32_fp8_e32 v[86:87], v105
	v_cvt_pk_f32_fp8_sdwa v[102:103], v105 src0_sel:WORD_1
	v_pk_fma_f32 v[76:77], v[24:25], v[82:83], v[76:77]
	v_pk_fma_f32 v[66:67], v[26:27], v[84:85], v[66:67]
	v_pk_mul_f32 v[82:83], v[80:81], v[86:87] op_sel_hi:[0,1]
	v_pk_mul_f32 v[80:81], v[80:81], v[102:103] op_sel_hi:[0,1]
	v_pk_fma_f32 v[64:65], v[30:31], v[80:81], v[64:65]
	v_and_b32_sdwa v80, v73, v99 dst_sel:DWORD dst_unused:UNUSED_PAD src0_sel:WORD_1 src1_sel:DWORD
	v_and_b32_sdwa v81, v72, v99 dst_sel:DWORD dst_unused:UNUSED_PAD src0_sel:WORD_1 src1_sel:DWORD
	v_add3_u32 v73, v73, v80, s46
	v_and_b32_sdwa v80, v71, v99 dst_sel:DWORD dst_unused:UNUSED_PAD src0_sel:WORD_1 src1_sel:DWORD
	v_pk_fma_f32 v[78:79], v[28:29], v[82:83], v[78:79]
	v_add3_u32 v82, v72, v81, s46
	v_and_b32_sdwa v81, v70, v99 dst_sel:DWORD dst_unused:UNUSED_PAD src0_sel:WORD_1 src1_sel:DWORD
	v_add3_u32 v71, v71, v80, s46
	v_and_b32_sdwa v80, v75, v99 dst_sel:DWORD dst_unused:UNUSED_PAD src0_sel:WORD_1 src1_sel:DWORD
	v_add3_u32 v83, v70, v81, s46
	v_and_b32_sdwa v81, v74, v99 dst_sel:DWORD dst_unused:UNUSED_PAD src0_sel:WORD_1 src1_sel:DWORD
	v_add3_u32 v75, v75, v80, s46
	v_and_b32_sdwa v80, v69, v99 dst_sel:DWORD dst_unused:UNUSED_PAD src0_sel:WORD_1 src1_sel:DWORD
	v_add3_u32 v84, v74, v81, s46
	v_and_b32_sdwa v81, v68, v99 dst_sel:DWORD dst_unused:UNUSED_PAD src0_sel:WORD_1 src1_sel:DWORD
	v_add3_u32 v69, v69, v80, s46
	v_and_b32_sdwa v80, v77, v99 dst_sel:DWORD dst_unused:UNUSED_PAD src0_sel:WORD_1 src1_sel:DWORD
	v_add3_u32 v85, v68, v81, s46
	v_and_b32_sdwa v81, v76, v99 dst_sel:DWORD dst_unused:UNUSED_PAD src0_sel:WORD_1 src1_sel:DWORD
	v_add3_u32 v77, v77, v80, s46
	v_and_b32_sdwa v80, v67, v99 dst_sel:DWORD dst_unused:UNUSED_PAD src0_sel:WORD_1 src1_sel:DWORD
	v_add3_u32 v86, v76, v81, s46
	v_and_b32_sdwa v81, v66, v99 dst_sel:DWORD dst_unused:UNUSED_PAD src0_sel:WORD_1 src1_sel:DWORD
	v_add3_u32 v67, v67, v80, s46
	v_and_b32_sdwa v80, v79, v99 dst_sel:DWORD dst_unused:UNUSED_PAD src0_sel:WORD_1 src1_sel:DWORD
	v_add3_u32 v87, v66, v81, s46
	v_and_b32_sdwa v81, v78, v99 dst_sel:DWORD dst_unused:UNUSED_PAD src0_sel:WORD_1 src1_sel:DWORD
	v_add3_u32 v79, v79, v80, s46
	v_and_b32_sdwa v80, v65, v99 dst_sel:DWORD dst_unused:UNUSED_PAD src0_sel:WORD_1 src1_sel:DWORD
	v_and_b32_e32 v73, 0xffff0000, v73
	v_and_b32_e32 v72, 0xffff0000, v82
	v_add3_u32 v101, v78, v81, s46
	v_and_b32_sdwa v81, v64, v99 dst_sel:DWORD dst_unused:UNUSED_PAD src0_sel:WORD_1 src1_sel:DWORD
	v_add3_u32 v65, v65, v80, s46
	v_and_b32_e32 v71, 0xffff0000, v71
	v_and_b32_e32 v70, 0xffff0000, v83
	v_add3_u32 v102, v64, v81, s46
	v_and_b32_e32 v81, 0xffff0000, v65
	v_pk_fma_f32 v[64:65], v[72:73], v[72:73], 0 op_sel_hi:[1,1,0]
	v_and_b32_e32 v75, 0xffff0000, v75
	v_and_b32_e32 v74, 0xffff0000, v84
	v_pk_fma_f32 v[64:65], v[70:71], v[70:71], v[64:65]
	v_and_b32_e32 v69, 0xffff0000, v69
	v_and_b32_e32 v68, 0xffff0000, v85
	v_pk_fma_f32 v[64:65], v[74:75], v[74:75], v[64:65]
	v_and_b32_e32 v77, 0xffff0000, v77
	v_and_b32_e32 v76, 0xffff0000, v86
	v_pk_fma_f32 v[64:65], v[68:69], v[68:69], v[64:65]
	v_and_b32_e32 v67, 0xffff0000, v67
	v_and_b32_e32 v66, 0xffff0000, v87
	v_pk_fma_f32 v[64:65], v[76:77], v[76:77], v[64:65]
	v_and_b32_e32 v79, 0xffff0000, v79
	v_and_b32_e32 v78, 0xffff0000, v101
	v_pk_fma_f32 v[64:65], v[66:67], v[66:67], v[64:65]
	v_and_b32_e32 v80, 0xffff0000, v102
	v_pk_fma_f32 v[64:65], v[78:79], v[78:79], v[64:65]
	s_lshl_b64 s[24:25], s[20:21], 10
	v_pk_fma_f32 v[64:65], v[80:81], v[80:81], v[64:65]
	s_nop 0
	v_add_f32_e32 v64, v64, v65
	s_waitcnt lgkmcnt(0)
	s_nop 1
	v_add_f32_dpp v64, v64, v64 quad_perm:[1,0,3,2] row_mask:0xf bank_mask:0xf
	s_waitcnt lgkmcnt(0)
	s_nop 1
	v_add_f32_dpp v64, v64, v64 quad_perm:[2,3,0,1] row_mask:0xf bank_mask:0xf
	s_waitcnt lgkmcnt(0)
	s_nop 1
	v_add_f32_dpp v64, v64, v64 row_half_mirror row_mask:0xf bank_mask:0xf
	s_waitcnt lgkmcnt(0)
	s_nop 1
	v_add_f32_dpp v103, v64, v64 row_mirror row_mask:0xf bank_mask:0xf
	v_or_b32_sdwa v64, v73, v82 dst_sel:DWORD dst_unused:UNUSED_PAD src0_sel:DWORD src1_sel:WORD_1
	v_or_b32_sdwa v65, v71, v83 dst_sel:DWORD dst_unused:UNUSED_PAD src0_sel:DWORD src1_sel:WORD_1
	global_store_dwordx2 v[62:63], v[64:65], off
	v_or_b32_sdwa v64, v75, v84 dst_sel:DWORD dst_unused:UNUSED_PAD src0_sel:DWORD src1_sel:WORD_1
	s_waitcnt lgkmcnt(0)
	v_mov_b32_e32 v82, v103
	v_mov_b32_e32 v104, v103
	s_nop 1
	v_permlane16_swap_b32_e32 v82, v104
	v_add_f32_e32 v82, v82, v104
	v_or_b32_sdwa v65, v69, v85 dst_sel:DWORD dst_unused:UNUSED_PAD src0_sel:DWORD src1_sel:WORD_1
	global_store_dwordx2 v[62:63], v[64:65], off offset:512
	s_waitcnt lgkmcnt(0)
	v_mov_b32_e32 v64, v82
	v_mov_b32_e32 v83, v82
	s_nop 1
	v_permlane32_swap_b32_e32 v64, v83
	v_add_f32_e32 v64, v64, v83
	v_fmamk_f32 v64, v64, 0x3a800000, v96
	v_mul_f32_e32 v65, 0x4f800000, v64
	v_cmp_gt_f32_e32 vcc, s47, v64
	s_nop 1
	v_cndmask_b32_e32 v82, v64, v65, vcc
	v_sqrt_f32_e32 v83, v82
	v_or_b32_sdwa v64, v77, v86 dst_sel:DWORD dst_unused:UNUSED_PAD src0_sel:DWORD src1_sel:WORD_1
	v_or_b32_sdwa v65, v67, v87 dst_sel:DWORD dst_unused:UNUSED_PAD src0_sel:DWORD src1_sel:WORD_1
	global_store_dwordx2 v[62:63], v[64:65], off offset:1024
	v_add_u32_e32 v64, -1, v83
	v_fma_f32 v65, -v64, v83, v82
	v_cmp_ge_f32_e64 s[10:11], 0, v65
	v_add_u32_e32 v65, 1, v83
	v_mov_b32_e32 v86, 0
	v_cndmask_b32_e64 v64, v83, v64, s[10:11]
	v_fma_f32 v83, -v65, v83, v82
	v_cmp_lt_f32_e64 s[10:11], 0, v83
	s_nop 1
	v_cndmask_b32_e64 v64, v64, v65, s[10:11]
	v_mul_f32_e32 v65, 0x37800000, v64
	v_cndmask_b32_e32 v64, v64, v65, vcc
	v_cmp_class_f32_e32 vcc, v82, v97
	v_or_b32_sdwa v65, v81, v102 dst_sel:DWORD dst_unused:UNUSED_PAD src0_sel:DWORD src1_sel:WORD_1
	s_nop 0
	v_cndmask_b32_e32 v82, v64, v82, vcc
	v_div_scale_f32 v83, s[10:11], v82, v82, 1.0
	v_rcp_f32_e32 v84, v83
	v_or_b32_sdwa v64, v79, v101 dst_sel:DWORD dst_unused:UNUSED_PAD src0_sel:DWORD src1_sel:WORD_1
	global_store_dwordx2 v[62:63], v[64:65], off offset:1536
	v_fma_f32 v62, -v83, v84, 1.0
	v_fmac_f32_e32 v84, v62, v84
	v_div_scale_f32 v62, vcc, 1.0, v82, 1.0
	v_mul_f32_e32 v63, v62, v84
	v_fma_f32 v64, -v83, v63, v62
	v_fmac_f32_e32 v63, v64, v84
	v_fma_f32 v62, -v83, v63, v62
	v_div_fmas_f32 v62, v62, v84, v63
	v_div_fixup_f32 v82, v62, v82, 1.0
	v_pk_mul_f32 v[64:65], v[82:83], v[72:73] op_sel_hi:[0,1]
	v_pk_mul_f32 v[62:63], v[82:83], v[70:71] op_sel_hi:[0,1]
	v_pk_fma_f32 v[70:71], v[48:49], v[64:65], v[4:5]
	v_pk_mul_f32 v[64:65], v[82:83], v[68:69] op_sel_hi:[0,1]
	v_pk_mul_f32 v[68:69], v[82:83], v[76:77] op_sel_hi:[0,1]
	v_pk_mul_f32 v[72:73], v[82:83], v[74:75] op_sel_hi:[0,1]
	v_pk_fma_f32 v[74:75], v[56:57], v[68:69], v[16:17]
	v_pk_mul_f32 v[68:69], v[82:83], v[80:81] op_sel_hi:[0,1]
	v_bfe_u32 v80, v70, 16, 1
	v_add3_u32 v80, v70, v80, s46
	v_bfe_u32 v81, v71, 16, 1
	v_pk_fma_f32 v[62:63], v[46:47], v[62:63], v[6:7]
	v_lshrrev_b32_e32 v80, 16, v80
	v_add3_u32 v81, v71, v81, s46
	v_and_or_b32 v80, v81, s44, v80
	v_bfe_u32 v81, v62, 16, 1
	v_pk_mul_f32 v[66:67], v[82:83], v[66:67] op_sel_hi:[0,1]
	v_pk_mul_f32 v[76:77], v[82:83], v[78:79] op_sel_hi:[0,1]
	v_add3_u32 v81, v62, v81, s46
	v_bfe_u32 v82, v63, 16, 1
	v_lshrrev_b32_e32 v81, 16, v81
	v_add3_u32 v82, v63, v82, s46
	v_pk_fma_f32 v[72:73], v[52:53], v[72:73], v[8:9]
	v_lshl_add_u64 v[78:79], v[38:39], 0, s[22:23]
	v_and_or_b32 v81, v82, s44, v81
	global_store_dwordx2 v[78:79], v[80:81], off
	v_bfe_u32 v80, v72, 16, 1
	v_add3_u32 v80, v72, v80, s46
	v_bfe_u32 v81, v73, 16, 1
	v_pk_fma_f32 v[64:65], v[50:51], v[64:65], v[10:11]
	v_lshrrev_b32_e32 v80, 16, v80
	v_add3_u32 v81, v73, v81, s46
	v_and_or_b32 v80, v81, s44, v80
	v_bfe_u32 v81, v64, 16, 1
	v_add3_u32 v81, v64, v81, s46
	v_bfe_u32 v82, v65, 16, 1
	v_lshrrev_b32_e32 v81, 16, v81
	v_add3_u32 v82, v65, v82, s46
	v_and_or_b32 v81, v82, s44, v81
	global_store_dwordx2 v[78:79], v[80:81], off offset:512
	v_bfe_u32 v80, v74, 16, 1
	v_add3_u32 v80, v74, v80, s46
	v_bfe_u32 v81, v75, 16, 1
	v_pk_fma_f32 v[66:67], v[54:55], v[66:67], v[18:19]
	v_lshrrev_b32_e32 v80, 16, v80
	v_add3_u32 v81, v75, v81, s46
	v_and_or_b32 v80, v81, s44, v80
	v_bfe_u32 v81, v66, 16, 1
	v_add3_u32 v81, v66, v81, s46
	v_bfe_u32 v82, v67, 16, 1
	v_lshrrev_b32_e32 v81, 16, v81
	v_add3_u32 v82, v67, v82, s46
	v_pk_fma_f32 v[76:77], v[60:61], v[76:77], v[20:21]
	v_and_or_b32 v81, v82, s44, v81
	global_store_dwordx2 v[78:79], v[80:81], off offset:1024
	v_bfe_u32 v80, v76, 16, 1
	v_add3_u32 v80, v76, v80, s46
	v_bfe_u32 v81, v77, 16, 1
	v_pk_fma_f32 v[68:69], v[58:59], v[68:69], v[22:23]
	v_lshrrev_b32_e32 v80, 16, v80
	v_add3_u32 v81, v77, v81, s46
	v_mul_f32_e32 v83, 0x41000000, v70
	v_mul_f32_e32 v84, 0x41000000, v71
	v_and_or_b32 v80, v81, s44, v80
	v_bfe_u32 v81, v68, 16, 1
	v_med3_f32 v83, v83, s48, v100
	v_med3_f32 v84, v84, s48, v100
	v_add3_u32 v81, v68, v81, s46
	v_bfe_u32 v82, v69, 16, 1
	v_cvt_pk_fp8_f32 v86, v83, v84
	v_lshrrev_b32_e32 v81, 16, v81
	v_add3_u32 v82, v69, v82, s46
	v_mul_f32_e32 v85, 0x41000000, v62
	v_mul_f32_e32 v83, 0x41000000, v63
	v_and_or_b32 v81, v82, s44, v81
	v_med3_f32 v84, v85, s48, v100
	v_med3_f32 v83, v83, s48, v100
	global_store_dwordx2 v[78:79], v[80:81], off offset:1536
	v_mul_f32_e32 v78, 0x41000000, v72
	v_mul_f32_e32 v79, 0x41000000, v73
	v_cvt_pk_fp8_f32 v86, v84, v83 op_sel:[0,0,1]
	v_med3_f32 v78, v78, s48, v100
	v_med3_f32 v79, v79, s48, v100
	v_mov_b32_e32 v84, 0
	v_cvt_pk_fp8_f32 v84, v78, v79
	v_mul_f32_e32 v80, 0x41000000, v64
	v_mul_f32_e32 v78, 0x41000000, v65
	v_med3_f32 v79, v80, s48, v100
	v_med3_f32 v78, v78, s48, v100
	v_cvt_pk_fp8_f32 v84, v79, v78 op_sel:[0,0,1]
	v_mul_f32_e32 v78, 0x41000000, v74
	v_mul_f32_e32 v79, 0x41000000, v75
	v_med3_f32 v78, v78, s48, v100
	v_med3_f32 v79, v79, s48, v100
	v_mov_b32_e32 v85, 0
	v_cvt_pk_fp8_f32 v85, v78, v79
	v_mul_f32_e32 v80, 0x41000000, v66
	v_mul_f32_e32 v78, 0x41000000, v67
	v_med3_f32 v79, v80, s48, v100
	v_med3_f32 v78, v78, s48, v100
	v_lshl_add_u64 v[82:83], v[40:41], 0, s[24:25]
	v_cvt_pk_fp8_f32 v85, v79, v78 op_sel:[0,0,1]
	v_mul_f32_e32 v78, 0x41000000, v76
	v_mul_f32_e32 v79, 0x41000000, v77
	global_store_dword v[82:83], v86, off
	v_med3_f32 v78, v78, s48, v100
	v_med3_f32 v79, v79, s48, v100
	v_mov_b32_e32 v86, 0
	v_cvt_pk_fp8_f32 v86, v78, v79
	v_mul_f32_e32 v80, 0x41000000, v68
	v_mul_f32_e32 v78, 0x41000000, v69
	v_med3_f32 v79, v80, s48, v100
	v_med3_f32 v78, v78, s48, v100
	v_cvt_pk_fp8_f32 v86, v79, v78 op_sel:[0,0,1]
	ds_read_b128 v[78:81], v94
	global_store_dword v[82:83], v84, off offset:256
	global_store_dword v[82:83], v85, off offset:512
	global_store_dword v[82:83], v86, off offset:768
	ds_read_b128 v[82:85], v94 offset:1024
	ds_read_b128 v[102:105], v94 offset:2048
	s_waitcnt lgkmcnt(2)
	v_pk_fma_f32 v[78:79], v[70:71], v[78:79], 0 op_sel_hi:[1,1,0]
	s_nop 0
	v_pk_fma_f32 v[86:87], v[62:63], v[80:81], v[78:79]
	ds_read_b128 v[78:81], v94 offset:3072
	s_waitcnt lgkmcnt(2)
	v_pk_fma_f32 v[82:83], v[72:73], v[82:83], v[86:87]
	s_nop 0
	v_pk_fma_f32 v[82:83], v[64:65], v[84:85], v[82:83]
	s_waitcnt lgkmcnt(1)
	v_pk_fma_f32 v[82:83], v[74:75], v[102:103], v[82:83]
	s_nop 0
	v_pk_fma_f32 v[82:83], v[66:67], v[104:105], v[82:83]
	s_waitcnt lgkmcnt(0)
	v_pk_fma_f32 v[78:79], v[76:77], v[78:79], v[82:83]
	ds_read_b128 v[82:85], v94 offset:5120
	ds_read_b128 v[102:105], v94 offset:4096
	v_pk_fma_f32 v[78:79], v[68:69], v[80:81], v[78:79]
	s_waitcnt lgkmcnt(0)
	v_pk_fma_f32 v[86:87], v[70:71], v[102:103], 0 op_sel_hi:[1,1,0]
	v_add_f32_e32 v101, v78, v79
	ds_read_b128 v[78:81], v94 offset:7168
	ds_read_b128 v[106:109], v94 offset:6144
	v_pk_fma_f32 v[86:87], v[62:63], v[104:105], v[86:87]
	s_nop 0
	v_pk_fma_f32 v[82:83], v[72:73], v[82:83], v[86:87]
	s_nop 0
	v_pk_fma_f32 v[82:83], v[64:65], v[84:85], v[82:83]
	s_waitcnt lgkmcnt(0)
	v_pk_fma_f32 v[82:83], v[74:75], v[106:107], v[82:83]
	s_nop 0
	v_pk_fma_f32 v[82:83], v[66:67], v[108:109], v[82:83]
	s_nop 0
	v_pk_fma_f32 v[78:79], v[76:77], v[78:79], v[82:83]
	s_nop 0
	v_pk_fma_f32 v[78:79], v[68:69], v[80:81], v[78:79]
	s_nop 0
	v_add_f32_e32 v110, v78, v79
	ds_read_b128 v[78:81], v94 offset:8192
	ds_read_b128 v[82:85], v94 offset:9216
	ds_read_b128 v[102:105], v94 offset:10240
	ds_read_b128 v[106:109], v94 offset:11264
	s_waitcnt lgkmcnt(3)
	v_pk_fma_f32 v[78:79], v[70:71], v[78:79], 0 op_sel_hi:[1,1,0]
	s_nop 0
	v_pk_fma_f32 v[78:79], v[62:63], v[80:81], v[78:79]
	s_waitcnt lgkmcnt(2)
	v_pk_fma_f32 v[78:79], v[72:73], v[82:83], v[78:79]
	s_nop 0
	v_pk_fma_f32 v[78:79], v[64:65], v[84:85], v[78:79]
	s_waitcnt lgkmcnt(1)
	v_pk_fma_f32 v[78:79], v[74:75], v[102:103], v[78:79]
	s_nop 0
	v_pk_fma_f32 v[78:79], v[66:67], v[104:105], v[78:79]
	s_waitcnt lgkmcnt(0)
	v_pk_fma_f32 v[86:87], v[76:77], v[106:107], v[78:79]
	ds_read_b128 v[78:81], v94 offset:13312
	ds_read_b128 v[82:85], v94 offset:12288
	v_pk_fma_f32 v[86:87], v[68:69], v[108:109], v[86:87]
	ds_read_b128 v[102:105], v94 offset:15360
	ds_read_b128 v[106:109], v94 offset:14336
	v_add_f32_e32 v111, v86, v87
	s_waitcnt lgkmcnt(2)
	v_pk_fma_f32 v[82:83], v[70:71], v[82:83], 0 op_sel_hi:[1,1,0]
	s_nop 0
	v_pk_fma_f32 v[82:83], v[62:63], v[84:85], v[82:83]
	s_nop 0
	v_pk_fma_f32 v[78:79], v[72:73], v[78:79], v[82:83]
	s_nop 0
	v_pk_fma_f32 v[78:79], v[64:65], v[80:81], v[78:79]
	s_waitcnt lgkmcnt(0)
	v_pk_fma_f32 v[78:79], v[74:75], v[106:107], v[78:79]
	s_nop 0
	v_pk_fma_f32 v[78:79], v[66:67], v[108:109], v[78:79]
	s_nop 0
	v_pk_fma_f32 v[78:79], v[76:77], v[102:103], v[78:79]
	s_nop 0
	v_pk_fma_f32 v[78:79], v[68:69], v[104:105], v[78:79]
	s_nop 0
	v_add_f32_e32 v112, v78, v79
	ds_read_b128 v[78:81], v94 offset:16384
	ds_read_b128 v[82:85], v94 offset:17408
	ds_read_b128 v[102:105], v94 offset:18432
	ds_read_b128 v[106:109], v94 offset:19456
	s_waitcnt lgkmcnt(3)
	v_pk_fma_f32 v[78:79], v[70:71], v[78:79], 0 op_sel_hi:[1,1,0]
	s_nop 0
	v_pk_fma_f32 v[78:79], v[62:63], v[80:81], v[78:79]
	s_waitcnt lgkmcnt(2)
	v_pk_fma_f32 v[78:79], v[72:73], v[82:83], v[78:79]
	s_nop 0
	v_pk_fma_f32 v[78:79], v[64:65], v[84:85], v[78:79]
	s_waitcnt lgkmcnt(1)
	v_pk_fma_f32 v[78:79], v[74:75], v[102:103], v[78:79]
	s_nop 0
	v_pk_fma_f32 v[78:79], v[66:67], v[104:105], v[78:79]
	s_waitcnt lgkmcnt(0)
	v_pk_fma_f32 v[86:87], v[76:77], v[106:107], v[78:79]
	ds_read_b128 v[78:81], v94 offset:21504
	ds_read_b128 v[82:85], v94 offset:20480
	v_pk_fma_f32 v[86:87], v[68:69], v[108:109], v[86:87]
	ds_read_b128 v[102:105], v94 offset:23552
	ds_read_b128 v[106:109], v94 offset:22528
	v_add_f32_e32 v113, v86, v87
	s_waitcnt lgkmcnt(2)
	v_pk_fma_f32 v[82:83], v[70:71], v[82:83], 0 op_sel_hi:[1,1,0]
	s_nop 0
	v_pk_fma_f32 v[82:83], v[62:63], v[84:85], v[82:83]
	s_nop 0
	v_pk_fma_f32 v[78:79], v[72:73], v[78:79], v[82:83]
	s_nop 0
	v_pk_fma_f32 v[78:79], v[64:65], v[80:81], v[78:79]
	s_waitcnt lgkmcnt(0)
	v_pk_fma_f32 v[78:79], v[74:75], v[106:107], v[78:79]
	s_nop 0
	v_pk_fma_f32 v[78:79], v[66:67], v[108:109], v[78:79]
	s_nop 0
	v_pk_fma_f32 v[78:79], v[76:77], v[102:103], v[78:79]
	s_nop 0
	v_pk_fma_f32 v[78:79], v[68:69], v[104:105], v[78:79]
	s_nop 0
	v_add_f32_e32 v114, v78, v79
	ds_read_b128 v[78:81], v94 offset:24576
	ds_read_b128 v[82:85], v94 offset:25600
	ds_read_b128 v[102:105], v94 offset:26624
	ds_read_b128 v[106:109], v94 offset:27648
	s_waitcnt lgkmcnt(3)
	v_pk_fma_f32 v[78:79], v[70:71], v[78:79], 0 op_sel_hi:[1,1,0]
	s_nop 0
	v_pk_fma_f32 v[78:79], v[62:63], v[80:81], v[78:79]
	s_waitcnt lgkmcnt(2)
	v_pk_fma_f32 v[78:79], v[72:73], v[82:83], v[78:79]
	s_nop 0
	v_pk_fma_f32 v[78:79], v[64:65], v[84:85], v[78:79]
	s_waitcnt lgkmcnt(1)
	v_pk_fma_f32 v[78:79], v[74:75], v[102:103], v[78:79]
	s_nop 0
	v_pk_fma_f32 v[78:79], v[66:67], v[104:105], v[78:79]
	s_waitcnt lgkmcnt(0)
	v_pk_fma_f32 v[86:87], v[76:77], v[106:107], v[78:79]
	ds_read_b128 v[78:81], v94 offset:29696
	ds_read_b128 v[82:85], v94 offset:28672
	v_pk_fma_f32 v[86:87], v[68:69], v[108:109], v[86:87]
	ds_read_b128 v[102:105], v94 offset:31744
	ds_read_b128 v[106:109], v94 offset:30720
	v_add_f32_e32 v86, v86, v87
	s_waitcnt lgkmcnt(2)
	v_pk_fma_f32 v[70:71], v[70:71], v[82:83], 0 op_sel_hi:[1,1,0]
	s_nop 0
	v_pk_fma_f32 v[62:63], v[62:63], v[84:85], v[70:71]
	s_nop 0
	v_pk_fma_f32 v[62:63], v[72:73], v[78:79], v[62:63]
	s_nop 0
	v_pk_fma_f32 v[62:63], v[64:65], v[80:81], v[62:63]
	s_waitcnt lgkmcnt(0)
	v_pk_fma_f32 v[62:63], v[74:75], v[106:107], v[62:63]
	s_nop 0
	v_pk_fma_f32 v[62:63], v[66:67], v[108:109], v[62:63]
	s_nop 0
	v_pk_fma_f32 v[62:63], v[76:77], v[102:103], v[62:63]
	s_nop 0
	v_pk_fma_f32 v[62:63], v[68:69], v[104:105], v[62:63]
	s_nop 0
	v_add_f32_e32 v62, v62, v63
	v_cndmask_b32_e64 v63, v101, v113, s[2:3]
	ds_bpermute_b32 v63, v93, v63
	v_cndmask_b32_e64 v64, v113, v101, s[2:3]
	v_cndmask_b32_e64 v65, v110, v114, s[2:3]
	ds_bpermute_b32 v65, v93, v65
	v_cndmask_b32_e64 v67, v112, v62, s[2:3]
	s_waitcnt lgkmcnt(1)
	v_add_f32_e32 v63, v64, v63
	v_cndmask_b32_e64 v64, v111, v86, s[2:3]
	ds_bpermute_b32 v64, v93, v64
	ds_bpermute_b32 v67, v93, v67
	v_cndmask_b32_e64 v66, v114, v110, s[2:3]
	s_waitcnt lgkmcnt(2)
	v_add_f32_e32 v65, v66, v65
	v_cndmask_b32_e64 v66, v86, v111, s[2:3]
	v_cndmask_b32_e64 v62, v62, v112, s[2:3]
	s_waitcnt lgkmcnt(1)
	v_add_f32_e32 v64, v66, v64
	s_waitcnt lgkmcnt(0)
	v_add_f32_e32 v62, v62, v67
	v_cndmask_b32_e64 v66, v63, v64, s[4:5]
	v_cndmask_b32_e64 v67, v65, v62, s[4:5]
	ds_bpermute_b32 v66, v92, v66
	ds_bpermute_b32 v67, v92, v67
	v_cndmask_b32_e64 v63, v64, v63, s[4:5]
	v_cndmask_b32_e64 v62, v62, v65, s[4:5]
	s_waitcnt lgkmcnt(1)
	v_add_f32_e32 v63, v63, v66
	s_waitcnt lgkmcnt(0)
	v_add_f32_e32 v62, v62, v67
	v_cndmask_b32_e64 v64, v63, v62, s[6:7]
	s_nop 1
	v_mov_b32_dpp v64, v64 row_ror:8 row_mask:0xf bank_mask:0xf
	v_cndmask_b32_e64 v62, v62, v63, s[6:7]
	s_waitcnt lgkmcnt(0)
	v_add_f32_e32 v62, v62, v64
	s_nop 1
	v_mov_b32_dpp v63, v62 quad_perm:[3,2,1,0] row_mask:0xf bank_mask:0xf
	s_nop 1
	v_mov_b32_dpp v63, v63 row_half_mirror row_mask:0xf bank_mask:0xf
	s_waitcnt lgkmcnt(0)
	v_add_f32_e32 v62, v62, v63
	s_nop 1
	v_mov_b32_dpp v63, v62 quad_perm:[2,3,0,1] row_mask:0xf bank_mask:0xf
	s_waitcnt lgkmcnt(0)
	v_add_f32_e32 v62, v62, v63
	s_nop 1
	v_mov_b32_dpp v63, v62 quad_perm:[1,0,3,2] row_mask:0xf bank_mask:0xf
	s_and_saveexec_b64 s[10:11], s[8:9]
	s_cbranch_execz .LBB0_747
	s_lshl_b64 s[20:21], s[20:21], 5
	v_lshl_add_u64 v[64:65], v[42:43], 0, s[20:21]
	s_waitcnt lgkmcnt(0)
	v_add_f32_e32 v62, v62, v63
	global_store_dword v[64:65], v62, off
	s_branch .LBB0_747

.LBB0_1111:
	s_or_b64 exec, exec, s[50:51]
	s_nop 1
	v_mov_b32_dpp v0, v19 quad_perm:[1,0,3,2] row_mask:0xf bank_mask:0xf
	v_max_f32_e32 v1, v19, v19
	v_cmp_eq_u32_e32 vcc, 0, v150
	s_waitcnt lgkmcnt(0)
	v_max_f32_e32 v0, v0, v0
	v_max_f32_e32 v0, v1, v0
	s_nop 1
	v_mov_b32_dpp v1, v0 quad_perm:[2,3,0,1] row_mask:0xf bank_mask:0xf
	s_waitcnt lgkmcnt(0)
	v_max_f32_e32 v1, v1, v1
	v_max_f32_e32 v0, v0, v1
	s_nop 1
	v_mov_b32_dpp v1, v0 quad_perm:[3,2,1,0] row_mask:0xf bank_mask:0xf
	s_nop 1
	v_mov_b32_dpp v1, v1 row_half_mirror row_mask:0xf bank_mask:0xf
	s_waitcnt lgkmcnt(0)
	v_max_f32_e32 v1, v1, v1
	v_max_f32_e32 v0, v0, v1
	s_nop 1
	v_mov_b32_dpp v1, v0 row_ror:8 row_mask:0xf bank_mask:0xf
	s_waitcnt lgkmcnt(0)
	v_max_f32_e32 v1, v1, v1
	v_max_f32_e32 v0, v0, v1
	ds_bpermute_b32 v1, v159, v0
	s_waitcnt lgkmcnt(0)
	v_max_f32_e32 v1, v1, v1
	v_max_f32_e32 v0, v0, v1
	ds_bpermute_b32 v1, v160, v0
	s_and_saveexec_b64 s[0:1], vcc
	s_cbranch_execz .LBB0_1113
	s_waitcnt lgkmcnt(0)
	v_max_f32_e32 v1, v1, v1
	v_max_f32_e32 v0, v0, v0
	v_readlane_b32 s14, v254, 20
	v_max_f32_e32 v0, v0, v1
	s_nop 0
	v_mov_b32_e32 v1, s14
	ds_write_b32 v1, v0

.LBB0_1116:
	s_or_b64 exec, exec, s[50:51]
	v_cmp_gt_i32_e32 vcc, 64, v16
	s_and_saveexec_b64 s[0:1], vcc
	v_lshl_add_u32 v0, v16, 2, 0
	v_add_u32_e32 v0, 0x26900, v0
	ds_write_b32 v0, v53
	s_or_b64 exec, exec, s[0:1]
	v_readlane_b32 s24, v255, 10
	s_add_i32 s0, 0, 0x26800
	s_or_b32 s1, s24, s87
	v_ashrrev_i32_e32 v152, 3, v150
	v_readlane_b32 s25, v255, 11
	s_add_u32 s82, s1, s47
	s_addc_u32 s83, s25, 0
	v_ashrrev_i32_e32 v153, 31, v152
	v_lshl_add_u64 v[6:7], s[82:83], 0, v[152:153]
	v_and_b32_e32 v147, 7, v150
	s_waitcnt lgkmcnt(0)
	v_lshlrev_b64 v[0:1], 10, v[6:7]
	v_lshl_add_u64 v[0:1], s[38:39], 0, v[0:1]
	v_lshlrev_b32_e32 v52, 7, v147
	v_lshl_add_u64 v[4:5], v[0:1], 0, v[52:53]
	s_barrier
	global_load_dwordx4 v[0:3], v[4:5], off
	v_readlane_b32 s24, v254, 14
	v_lshlrev_b64 v[6:7], 5, v[6:7]
	v_readlane_b32 s25, v254, 15
	v_lshlrev_b32_e32 v52, 2, v147
	s_mov_b32 s14, 0xf800000
	v_lshl_add_u64 v[6:7], s[24:25], 0, v[6:7]
	v_lshl_add_u64 v[6:7], v[6:7], 0, v[52:53]
	global_load_dword v40, v[6:7], off
	global_load_dwordx4 v[28:31], v[4:5], off offset:16
	global_load_dwordx4 v[24:27], v[4:5], off offset:32
	global_load_dwordx4 v[20:23], v[4:5], off offset:48
	global_load_dwordx4 v[16:19], v[4:5], off offset:64
	global_load_dwordx4 v[12:15], v[4:5], off offset:80
	global_load_dwordx4 v[8:11], v[4:5], off offset:96
	v_mov_b32_e32 v6, s0
	v_readlane_b32 s0, v254, 61
	ds_read_b128 v[32:35], v6
	s_mov_b32 s1, 0xb3000000
	v_mov_b32_e32 v6, s0
	ds_read_b128 v[36:39], v6
	global_load_dwordx4 v[4:7], v[4:5], off offset:112
	s_waitcnt lgkmcnt(1)
	v_max_f32_e32 v33, v33, v33
	v_max_f32_e32 v32, v32, v32
	v_max_f32_e32 v32, v32, v33
	v_max3_f32 v32, v32, v34, v35
	s_waitcnt lgkmcnt(0)
	v_max3_f32 v32, v32, v36, v37
	v_max3_f32 v32, v32, v38, v39
	v_mul_f32_e32 v33, 0x4f800000, v32
	v_cmp_gt_f32_e32 vcc, s14, v32
	s_mov_b32 s0, 0x33000000
	v_add_u32_e32 v153, s47, v152
	v_cndmask_b32_e32 v32, v32, v33, vcc
	v_sqrt_f32_e32 v33, v32
	s_nop 0
	v_add_u32_e32 v34, -1, v33
	v_fma_f32 v36, -v34, v33, v32
	v_add_u32_e32 v35, 1, v33
	v_cmp_ge_f32_e64 s[50:51], 0, v36
	v_fma_f32 v37, -v35, v33, v32
	s_nop 0
	v_cndmask_b32_e64 v33, v33, v34, s[50:51]
	v_cmp_lt_f32_e64 s[50:51], 0, v37
	s_waitcnt vmcnt(8)
	v_cvt_f32_f16_sdwa v34, v0 dst_sel:DWORD dst_unused:UNUSED_PAD src0_sel:WORD_1
	v_cndmask_b32_e64 v33, v33, v35, s[50:51]
	v_mul_f32_e32 v35, 0x37800000, v33
	v_cndmask_b32_e32 v33, v33, v35, vcc
	v_mul_f32_e32 v34, v34, v34
	v_fma_mix_f32 v0, v0, v0, v34 op_sel_hi:[1,1,0]
	s_waitcnt vmcnt(7)
	v_cvt_f16_f32_e32 v35, v40
	v_fma_mix_f32 v0, v1, v1, v0 op_sel_hi:[1,1,0]
	v_cmp_class_f32_e64 s[50:51], v32, v181
	v_fma_mix_f32 v0, v1, v1, v0 op_sel:[1,1,0] op_sel_hi:[1,1,0]
	s_nop 0
	v_fma_mix_f32 v0, v2, v2, v0 op_sel_hi:[1,1,0]
	s_nop 0
	v_fma_mix_f32 v0, v2, v2, v0 op_sel:[1,1,0] op_sel_hi:[1,1,0]
	v_cndmask_b32_e64 v2, v33, v32, s[50:51]
	v_fma_mix_f32 v0, v3, v3, v0 op_sel_hi:[1,1,0]
	s_nop 0
	v_fma_mix_f32 v0, v3, v3, v0 op_sel:[1,1,0] op_sel_hi:[1,1,0]
	v_cvt_f32_f16_e64 v3, |v35|
	s_waitcnt vmcnt(6)
	v_fma_mix_f32 v0, v28, v28, v0 op_sel_hi:[1,1,0]
	s_nop 0
	v_fma_mix_f32 v0, v28, v28, v0 op_sel:[1,1,0] op_sel_hi:[1,1,0]
	s_nop 0
	v_fma_mix_f32 v0, v29, v29, v0 op_sel_hi:[1,1,0]
	s_nop 0
	v_fma_mix_f32 v0, v29, v29, v0 op_sel:[1,1,0] op_sel_hi:[1,1,0]
	s_nop 0
	v_fma_mix_f32 v0, v30, v30, v0 op_sel_hi:[1,1,0]
	s_nop 0
	v_fma_mix_f32 v0, v30, v30, v0 op_sel:[1,1,0] op_sel_hi:[1,1,0]
	s_nop 0
	v_fma_mix_f32 v0, v31, v31, v0 op_sel_hi:[1,1,0]
	s_nop 0
	v_fma_mix_f32 v0, v31, v31, v0 op_sel:[1,1,0] op_sel_hi:[1,1,0]
	s_waitcnt vmcnt(5)
	v_fma_mix_f32 v0, v24, v24, v0 op_sel_hi:[1,1,0]
	s_nop 0
	v_fma_mix_f32 v0, v24, v24, v0 op_sel:[1,1,0] op_sel_hi:[1,1,0]
	s_nop 0
	v_fma_mix_f32 v0, v25, v25, v0 op_sel_hi:[1,1,0]
	s_nop 0
	v_fma_mix_f32 v0, v25, v25, v0 op_sel:[1,1,0] op_sel_hi:[1,1,0]
	s_nop 0
	v_fma_mix_f32 v0, v26, v26, v0 op_sel_hi:[1,1,0]
	s_nop 0
	v_fma_mix_f32 v0, v26, v26, v0 op_sel:[1,1,0] op_sel_hi:[1,1,0]
	s_nop 0
	v_fma_mix_f32 v0, v27, v27, v0 op_sel_hi:[1,1,0]
	s_nop 0
	v_fma_mix_f32 v0, v27, v27, v0 op_sel:[1,1,0] op_sel_hi:[1,1,0]
	s_waitcnt vmcnt(4)
	v_fma_mix_f32 v0, v20, v20, v0 op_sel_hi:[1,1,0]
	s_nop 0
	v_fma_mix_f32 v0, v20, v20, v0 op_sel:[1,1,0] op_sel_hi:[1,1,0]
	s_nop 0
	v_fma_mix_f32 v0, v21, v21, v0 op_sel_hi:[1,1,0]
	s_nop 0
	v_fma_mix_f32 v0, v21, v21, v0 op_sel:[1,1,0] op_sel_hi:[1,1,0]
	s_nop 0
	v_fma_mix_f32 v0, v22, v22, v0 op_sel_hi:[1,1,0]
	s_nop 0
	v_fma_mix_f32 v0, v22, v22, v0 op_sel:[1,1,0] op_sel_hi:[1,1,0]
	s_nop 0
	v_fma_mix_f32 v0, v23, v23, v0 op_sel_hi:[1,1,0]
	s_nop 0
	v_fma_mix_f32 v0, v23, v23, v0 op_sel:[1,1,0] op_sel_hi:[1,1,0]
	s_waitcnt vmcnt(3)
	v_fma_mix_f32 v0, v16, v16, v0 op_sel_hi:[1,1,0]
	s_nop 0
	v_fma_mix_f32 v0, v16, v16, v0 op_sel:[1,1,0] op_sel_hi:[1,1,0]
	s_nop 0
	v_fma_mix_f32 v0, v17, v17, v0 op_sel_hi:[1,1,0]
	s_nop 0
	v_fma_mix_f32 v0, v17, v17, v0 op_sel:[1,1,0] op_sel_hi:[1,1,0]
	s_nop 0
	v_fma_mix_f32 v0, v18, v18, v0 op_sel_hi:[1,1,0]
	s_nop 0
	v_fma_mix_f32 v0, v18, v18, v0 op_sel:[1,1,0] op_sel_hi:[1,1,0]
	s_nop 0
	v_fma_mix_f32 v0, v19, v19, v0 op_sel_hi:[1,1,0]
	s_nop 0
	v_fma_mix_f32 v0, v19, v19, v0 op_sel:[1,1,0] op_sel_hi:[1,1,0]
	s_waitcnt vmcnt(2)
	v_fma_mix_f32 v0, v12, v12, v0 op_sel_hi:[1,1,0]
	s_nop 0
	v_fma_mix_f32 v0, v12, v12, v0 op_sel:[1,1,0] op_sel_hi:[1,1,0]
	s_nop 0
	v_fma_mix_f32 v0, v13, v13, v0 op_sel_hi:[1,1,0]
	s_nop 0
	v_fma_mix_f32 v0, v13, v13, v0 op_sel:[1,1,0] op_sel_hi:[1,1,0]
	s_nop 0
	v_fma_mix_f32 v0, v14, v14, v0 op_sel_hi:[1,1,0]
	s_nop 0
	v_fma_mix_f32 v0, v14, v14, v0 op_sel:[1,1,0] op_sel_hi:[1,1,0]
	s_nop 0
	v_fma_mix_f32 v0, v15, v15, v0 op_sel_hi:[1,1,0]
	s_nop 0
	v_fma_mix_f32 v0, v15, v15, v0 op_sel:[1,1,0] op_sel_hi:[1,1,0]
	s_waitcnt vmcnt(1)
	v_fma_mix_f32 v0, v8, v8, v0 op_sel_hi:[1,1,0]
	s_nop 0
	v_fma_mix_f32 v0, v8, v8, v0 op_sel:[1,1,0] op_sel_hi:[1,1,0]
	s_nop 0
	v_fma_mix_f32 v0, v9, v9, v0 op_sel_hi:[1,1,0]
	s_nop 0
	v_fma_mix_f32 v0, v9, v9, v0 op_sel:[1,1,0] op_sel_hi:[1,1,0]
	s_nop 0
	v_fma_mix_f32 v0, v10, v10, v0 op_sel_hi:[1,1,0]
	s_nop 0
	v_fma_mix_f32 v0, v10, v10, v0 op_sel:[1,1,0] op_sel_hi:[1,1,0]
	s_nop 0
	v_fma_mix_f32 v0, v11, v11, v0 op_sel_hi:[1,1,0]
	s_nop 0
	v_fma_mix_f32 v0, v11, v11, v0 op_sel:[1,1,0] op_sel_hi:[1,1,0]
	s_waitcnt vmcnt(0)
	v_fma_mix_f32 v0, v4, v4, v0 op_sel_hi:[1,1,0]
	s_nop 0
	v_fma_mix_f32 v0, v4, v4, v0 op_sel:[1,1,0] op_sel_hi:[1,1,0]
	s_nop 0
	v_fma_mix_f32 v0, v5, v5, v0 op_sel_hi:[1,1,0]
	s_nop 0
	v_fma_mix_f32 v0, v5, v5, v0 op_sel:[1,1,0] op_sel_hi:[1,1,0]
	s_nop 0
	v_fma_mix_f32 v0, v6, v6, v0 op_sel_hi:[1,1,0]
	s_nop 0
	v_fma_mix_f32 v0, v6, v6, v0 op_sel:[1,1,0] op_sel_hi:[1,1,0]
	s_nop 0
	v_fma_mix_f32 v0, v7, v7, v0 op_sel_hi:[1,1,0]
	s_nop 0
	v_fma_mix_f32 v0, v7, v7, v0 op_sel:[1,1,0] op_sel_hi:[1,1,0]
	s_nop 0
	v_mul_f32_e32 v1, 0x4f800000, v0
	v_cmp_gt_f32_e32 vcc, s14, v0
	s_nop 1
	v_cndmask_b32_e32 v0, v0, v1, vcc
	v_sqrt_f32_e32 v1, v0
	s_nop 0
	v_add_u32_e32 v4, -1, v1
	v_add_u32_e32 v5, 1, v1
	v_fma_f32 v6, -v4, v1, v0
	v_fma_f32 v7, -v5, v1, v0
	v_cmp_ge_f32_e64 s[50:51], 0, v6
	s_nop 1
	v_cndmask_b32_e64 v1, v1, v4, s[50:51]
	v_cmp_lt_f32_e64 s[50:51], 0, v7
	s_nop 1
	v_cndmask_b32_e64 v1, v1, v5, s[50:51]
	v_mul_f32_e32 v4, 0x37800000, v1
	v_cndmask_b32_e32 v1, v1, v4, vcc
	v_cmp_class_f32_e32 vcc, v0, v181
	s_nop 1
	v_cndmask_b32_e32 v0, v1, v0, vcc
	v_mul_f32_e32 v0, v0, v3
	v_mul_f32_e32 v0, v2, v0
	v_cmp_lt_f32_e32 vcc, s0, v40
	s_nop 1
	v_cndmask_b32_e32 v1, 0, v0, vcc
	v_cmp_gt_f32_e32 vcc, s1, v40
	s_nop 1
	v_mov_b32_dpp v2, v1 quad_perm:[1,0,3,2] row_mask:0xf bank_mask:0xf
	s_waitcnt lgkmcnt(0)
	v_add_f32_e32 v1, v1, v2
	v_cndmask_b32_e32 v0, 0, v0, vcc
	s_nop 1
	v_mov_b32_dpp v3, v0 quad_perm:[1,0,3,2] row_mask:0xf bank_mask:0xf
	v_cmp_eq_u32_e32 vcc, 0, v147
	s_waitcnt lgkmcnt(0)
	v_add_f32_e32 v2, v0, v3
	s_nop 1
	v_mov_b32_dpp v0, v1 quad_perm:[2,3,0,1] row_mask:0xf bank_mask:0xf
	s_nop 1
	v_mov_b32_dpp v3, v2 quad_perm:[2,3,0,1] row_mask:0xf bank_mask:0xf
	s_waitcnt lgkmcnt(0)
	v_add_f32_e32 v0, v1, v0
	s_waitcnt lgkmcnt(0)
	v_add_f32_e32 v1, v2, v3
	s_nop 1
	v_mov_b32_dpp v2, v0 quad_perm:[3,2,1,0] row_mask:0xf bank_mask:0xf
	s_nop 1
	v_mov_b32_dpp v2, v2 row_half_mirror row_mask:0xf bank_mask:0xf
	s_nop 1
	v_mov_b32_dpp v3, v1 quad_perm:[3,2,1,0] row_mask:0xf bank_mask:0xf
	s_nop 1
	v_mov_b32_dpp v3, v3 row_half_mirror row_mask:0xf bank_mask:0xf
	s_and_saveexec_b64 s[50:51], vcc
	s_cbranch_execz .LBB0_1120
	s_waitcnt lgkmcnt(0)
	v_add_f32_e32 v1, v1, v3
	v_add_f32_e32 v0, v0, v2
	v_add_f32_e32 v0, v1, v0
	v_fmamk_f32 v0, v0, 0x3f828f5c, v182
	s_brev_b32 s14, 34
	v_div_scale_f32 v2, s[0:1], v0, v0, s14
	v_rcp_f32_e32 v3, v2
	v_mul_f32_e32 v1, 0x3f828f5c, v1
	s_mov_b32 s0, 0x44800000
	v_fma_f32 v4, -v2, v3, 1.0
	v_fmac_f32_e32 v3, v4, v3
	v_div_scale_f32 v4, vcc, s14, v0, s14
	v_mul_f32_e32 v5, v4, v3
	v_fma_f32 v6, -v2, v5, v4
	v_fmac_f32_e32 v5, v6, v3
	v_fma_f32 v2, -v2, v5, v4
	v_div_fmas_f32 v2, v2, v3, v5
	v_div_fixup_f32 v0, v2, v0, s14
	v_min_f32_e32 v0, 0x476a6000, v0
	v_cvt_f16_f32_e32 v0, v0
	v_cvt_f32_f16_e32 v2, v0
	v_fma_mix_f32 v0, v1, v0, s0 op_sel_hi:[0,1,0]
	v_max_f32_e32 v0, 0x44800000, v0
	v_lshl_add_u32 v1, v153, 2, 0
	v_min_f32_e32 v0, 0x44bfe000, v0
	v_add_u32_e32 v3, 0x26000, v1
	ds_write_b32 v3, v0
	v_add_u32_e32 v0, 0x26100, v1
	ds_write_b32 v0, v2
.LBB0_1120:
	s_or_b64 exec, exec, s[50:51]
	v_ashrrev_i32_e32 v5, 5, v150
	v_lshlrev_b32_e32 v0, 7, v150
	v_and_b32_e32 v52, 0x380, v0
	s_waitcnt lgkmcnt(0)
	v_lshlrev_b32_e32 v2, 3, v5
	v_bfe_u32 v4, v150, 3, 2
	v_lshl_add_u64 v[0:1], s[38:39], 0, v[52:53]
	s_waitcnt lgkmcnt(0)
	v_ashrrev_i32_e32 v3, 31, v2
	v_lshl_add_u64 v[0:1], v[2:3], 1, v[0:1]
	v_or_b32_e32 v2, s82, v4
	v_mov_b32_e32 v3, s83
	v_lshlrev_b64 v[6:7], 10, v[2:3]
	v_or_b32_e32 v2, 4, v2
	v_lshlrev_b64 v[2:3], 10, v[2:3]
	v_lshl_add_u64 v[6:7], v[0:1], 0, v[6:7]
	v_lshl_add_u64 v[0:1], v[0:1], 0, v[2:3]
	global_load_dwordx4 v[74:77], v[6:7], off
	global_load_dwordx4 v[70:73], v[6:7], off offset:32
	global_load_dwordx4 v[66:69], v[6:7], off offset:64
	global_load_dwordx4 v[62:65], v[6:7], off offset:96
	global_load_dwordx4 v[82:85], v[0:1], off
	global_load_dwordx4 v[78:81], v[0:1], off offset:32
	global_load_dwordx4 v[58:61], v[0:1], off offset:64
	global_load_dwordx4 v[54:57], v[0:1], off offset:96
	v_and_b32_e32 v6, 31, v150
	v_cmp_lt_u32_e32 vcc, 7, v6
	s_and_saveexec_b64 s[0:1], vcc
	s_xor_b64 s[0:1], exec, s[0:1]
	v_lshlrev_b32_e32 v4, 2, v5
	s_or_saveexec_b64 s[50:51], s[0:1]
	v_mov_b32_e32 v86, 0
	v_mov_b32_e32 v0, 0
	v_mov_b32_e32 v1, 0
	v_mov_b32_e32 v2, 0
	v_mov_b32_e32 v3, 0
	s_xor_b64 exec, exec, s[50:51]
	s_cbranch_execz .LBB0_1124
	v_or_b32_e32 v0, s82, v6
	v_mov_b32_e32 v1, s83
	v_readlane_b32 s0, v254, 14
	v_lshlrev_b64 v[0:1], 5, v[0:1]
	v_readlane_b32 s1, v254, 15
	v_lshlrev_b32_e32 v4, 2, v5
	v_ashrrev_i32_e32 v5, 31, v4
	v_lshl_add_u64 v[0:1], s[0:1], 0, v[0:1]
	v_lshl_add_u64 v[0:1], v[4:5], 2, v[0:1]
	global_load_dwordx4 v[0:3], v[0:1], off

.LBB0_1376:
	s_or_b64 exec, exec, s[64:65]
	v_lshl_add_u32 v1, v153, 2, 0
	s_waitcnt lgkmcnt(0)
	v_add_u32_e32 v0, 0x26900, v1
	ds_read_b32 v0, v0
	s_waitcnt lgkmcnt(0)
	v_min_i32_e32 v0, 0x60, v0
	s_nop 1
	v_mov_b32_dpp v2, v0 row_ror:8 row_mask:0xf bank_mask:0xf
	s_waitcnt lgkmcnt(0)
	v_max_i32_e32 v2, v0, v2
	ds_bpermute_b32 v3, v159, v2
	s_waitcnt lgkmcnt(0)
	v_max_i32_e32 v2, v2, v3
	ds_bpermute_b32 v3, v160, v2
	s_waitcnt lgkmcnt(0)
	v_max_i32_e32 v2, v2, v3
	s_nop 0
	v_readfirstlane_b32 s24, v2
	s_cmp_lt_i32 s24, 1
	s_cbranch_scc1 .LBB0_1383
	v_add_u32_e32 v2, 0x26300, v1
	v_add_u32_e32 v3, 0x26a00, v1
	ds_read_b32 v1, v2
	ds_read_b32 v2, v3
	s_movk_i32 s1, 0x180
	v_mul_lo_u32 v3, v153, s1
	v_readlane_b32 s0, v254, 33
	v_mul_lo_u32 v5, v152, s1
	v_lshl_add_u32 v4, v153, 9, 0
	v_add_u32_e32 v3, s0, v3
	v_readlane_b32 s0, v254, 60
	s_mov_b32 s25, 0
	s_nop 0
	v_add_u32_e32 v5, s0, v5
	s_branch .LBB0_1379
